# v26 + P3: 36 transition lgkmcnt(0)<->MFMA swaps (MFMA whose operands an earlier wait covered now issues before the wait) + exact vmcnt instead of hipcc's over-draining ladder in the second loop halves
# speedup vs baseline: 1.0242x; 1.0239x over previous
; #define LAS __attribute__((address_space(3)))
; __device__ __forceinline__ void finishSM(f32x16& p0, f32x16& p1, float alpha, float& l_reg, bf16x8& pa0, bf16x8& pa1, bf16x8& pa2, bf16x8& pa3) {
; #pragma unroll
;     for (int r = 0; r < 16; ++r) p1[r] = __builtin_amdgcn_exp2f(p1[r]);
;     float ps = 0;
; #pragma unroll
;     for (int r = 0; r < 16; ++r) ps += p0[r];
; #pragma unroll
;     for (int r = 0; r < 16; ++r) ps += p1[r];
;     { auto rr = __builtin_amdgcn_permlane32_swap(__float_as_uint(ps), __float_as_uint(ps), false, false);
;       ps = __uint_as_float(rr[0]) + __uint_as_float(rr[1]); }
;     l_reg = l_reg * alpha + ps;
;     ...
;     PK4(p0, 0, pa0); PK4(p0, 8, pa1); PK4(p1, 0, pa2); PK4(p1, 8, pa3);
;     ...
; }
; template <int MODE>
; __device__ __forceinline__ void qkt(f32x16& p0, f32x16& p1, const LAS unsigned char* Ks, const bf16x8* qr, const LAS unsigned char* Qs, int r32, int hi, int cbase) {
;     p0 = f32x16{}; p1 = f32x16{};
; #pragma unroll
;     for (int d0 = 0; d0 < Cfg<MODE>::ND; ++d0) { const int cb = cbase + (d0 * 16 + hi * 8) * 2;
;         const bf16x8 b0 = *(const LAS bf16x8*)(Ks + KSWZ(r32, cb));
;         const bf16x8 b1 = *(const LAS bf16x8*)(Ks + KSWZ(32 + r32, cb));
;         bf16x8 q; if constexpr (MODE == 0) q = *(const LAS bf16x8*)(Qs + KSWZ(r32, cb)); else q = qr[d0];
;         p0 = __builtin_amdgcn_mfma_f32_32x32x16_bf16(b0, q, p0, 0, 0, 0);
;         p1 = __builtin_amdgcn_mfma_f32_32x32x16_bf16(b1, q, p1, 0, 0, 0); }
; }
; __device__ __forceinline__ int v_st(int k, int c) { const int kk = (k & ~0xC) | ((k & 4) << 1) | ((k & 8) >> 1); return ((kk >> 3) * 4 + (c >> 5)) * 512 + ((kk & 7) * 32 + (c & 31)) * 2; }
; __device__ __forceinline__ int v_rd_base(int lane) { return ((lane & 3) << 3) | (((lane >> 2) & 3) << 6) | (((lane >> 4) & 1) << 5) | (((lane >> 5) & 1) << 8); }
; template <int OFF> __device__ __forceinline__ s16x4 tr_read(int vb) {
;     s16x4 r; asm volatile("ds_read_b64_tr_b16 %0, %1 offset:%2" : "=&v"(r) : "v"(vb), "i"(OFF) : "memory"); return r;
; }
; template <int D0> __device__ __forceinline__ void pv_one(f32x16& od, int vb, bf16x8 pa0, bf16x8 pa1, bf16x8 pa2, bf16x8 pa3) {
;     const s16x4 l0 = tr_read<v_rd_off(D0, 0, 0)>(vb), h0 = tr_read<v_rd_off(D0, 0, 1)>(vb), l1 = tr_read<v_rd_off(D0, 1, 0)>(vb), h1 = tr_read<v_rd_off(D0, 1, 1)>(vb);
.LBB0_412:
	ds_read_b128 v[68:71], v204 offset:49152
	ds_read_b128 v[72:75], v204 offset:57344
	ds_read_b128 v[224:227], v195 offset:49152
	ds_read_b128 v[228:231], v195 offset:57344
	ds_read_b128 v[232:235], v205 offset:49152
	ds_read_b128 v[236:239], v205 offset:57344
	s_waitcnt lgkmcnt(5)
	v_mfma_f32_32x32x16_bf16 v[82:97], v[68:71], v[110:113], 0
	v_exp_f32_e32 v141, v66
	v_exp_f32_e32 v248, v67
	v_exp_f32_e32 v132, v132
	v_exp_f32_e32 v133, v133
	v_exp_f32_e32 v130, v130
	v_exp_f32_e32 v131, v131
	v_exp_f32_e32 v128, v128
	s_waitcnt lgkmcnt(3)
	v_mfma_f32_32x32x16_bf16 v[82:97], v[224:227], v[106:109], v[82:97]
	v_add_f32_e32 v224, 0, v201
	v_add_f32_e32 v224, v203, v224
	v_add_f32_e32 v224, v153, v224
	v_add_f32_e32 v224, v202, v224
	v_add_f32_e32 v224, v151, v224
	v_add_f32_e32 v224, v200, v224
	v_add_f32_e32 v224, v150, v224
	v_mfma_f32_32x32x16_bf16 v[66:81], v[72:75], v[110:113], 0
	v_add_f32_e32 v224, v152, v224
	v_add_f32_e32 v224, v147, v224
	v_add_f32_e32 v224, v149, v224
	v_add_f32_e32 v224, v145, v224
	v_add_f32_e32 v224, v148, v224
	v_add_f32_e32 v224, v143, v224
	v_add_f32_e32 v224, v146, v224
	s_waitcnt lgkmcnt(2)
	v_mfma_f32_32x32x16_bf16 v[66:81], v[228:231], v[106:109], v[66:81]
	v_add_f32_e32 v224, v142, v224
	v_add_f32_e32 v224, v144, v224
	v_add_f32_e32 v224, v132, v224
	v_add_f32_e32 v224, v133, v224
	v_add_f32_e32 v224, v141, v224
	v_exp_f32_e32 v129, v129
	v_add_f32_e32 v224, v248, v224
	s_waitcnt lgkmcnt(1)
	v_mfma_f32_32x32x16_bf16 v[82:97], v[232:235], v[102:105], v[82:97]
	v_exp_f32_e32 v126, v126
	v_add_f32_e32 v224, v130, v224
	ds_read_b128 v[240:243], v206 offset:49152
	ds_read_b128 v[244:247], v206 offset:57344
	v_exp_f32_e32 v127, v127
	v_add_f32_e32 v224, v131, v224
	v_exp_f32_e32 v138, v138
	v_add_f32_e32 v224, v128, v224
	s_waitcnt lgkmcnt(2)
	v_mfma_f32_32x32x16_bf16 v[66:81], v[236:239], v[102:105], v[66:81]
	v_exp_f32_e32 v139, v139
	v_add_f32_e32 v224, v129, v224
	v_exp_f32_e32 v136, v136
	v_add_f32_e32 v224, v126, v224
	v_exp_f32_e32 v137, v137
	v_add_f32_e32 v224, v127, v224
	v_exp_f32_e32 v134, v134
	s_waitcnt lgkmcnt(1)
	v_mfma_f32_32x32x16_bf16 v[82:97], v[240:243], v[98:101], v[82:97]
	v_add_f32_e32 v224, v138, v224
	v_exp_f32_e32 v135, v135
	v_add_f32_e32 v224, v139, v224
	v_add_f32_e32 v224, v136, v224
	v_add_f32_e32 v224, v137, v224
	v_add_f32_e32 v224, v134, v224
	v_add_f32_e32 v224, v135, v224
	s_waitcnt lgkmcnt(0)
	v_mfma_f32_32x32x16_bf16 v[66:81], v[244:247], v[98:101], v[66:81]
	v_mov_b32_e32 v225, v224
	v_cvt_pk_bf16_f32 v226, v201, v203
	v_cvt_pk_bf16_f32 v227, v153, v202
	v_cvt_pk_bf16_f32 v228, v151, v200
	s_nop 1
	v_permlane32_swap_b32_e32 v224, v225
	v_cvt_pk_bf16_f32 v229, v150, v152
	v_permlane32_swap_b32_e32 v226, v228
	v_cvt_pk_bf16_f32 v150, v147, v149
	v_cvt_pk_bf16_f32 v151, v145, v148
	v_cvt_pk_bf16_f32 v152, v143, v146
	v_cvt_pk_bf16_f32 v153, v142, v144
	v_cvt_pk_bf16_f32 v142, v132, v133
	v_cvt_pk_bf16_f32 v143, v141, v248
	v_cvt_pk_bf16_f32 v144, v130, v131
	v_cvt_pk_bf16_f32 v145, v128, v129
	v_cvt_pk_bf16_f32 v146, v126, v127
	v_cvt_pk_bf16_f32 v147, v138, v139
	v_cvt_pk_bf16_f32 v148, v136, v137
	v_cvt_pk_bf16_f32 v149, v134, v135
	v_permlane32_swap_b32_e32 v227, v229
	v_permlane32_swap_b32_e32 v150, v152
	v_permlane32_swap_b32_e32 v151, v153
	v_permlane32_swap_b32_e32 v142, v144
	v_permlane32_swap_b32_e32 v143, v145
	v_permlane32_swap_b32_e32 v146, v148
	v_permlane32_swap_b32_e32 v147, v149
	v_lshl_add_u64 v[200:201], v[196:197], 0, s[20:21]
	v_add_co_u32_e32 v126, vcc, s43, v200
	v_lshl_add_u64 v[202:203], v[198:199], 0, s[20:21]
	s_nop 0
	v_addc_co_u32_e32 v127, vcc, 0, v201, vcc
	v_add_co_u32_e32 v130, vcc, s45, v200
	s_nop 1
	v_addc_co_u32_e32 v131, vcc, 0, v201, vcc
	v_add_co_u32_e32 v134, vcc, s57, v202
	global_load_dwordx4 v[126:129], v[126:127], off
	s_nop 0
	global_load_dwordx4 v[130:133], v[130:131], off
	v_addc_co_u32_e32 v135, vcc, 0, v203, vcc
	global_load_dwordx4 v[134:137], v[134:135], off
	ds_read_b64_tr_b16 v[230:231], v175 offset:0
	ds_read_b64_tr_b16 v[232:233], v175 offset:0x800
	ds_read_b64_tr_b16 v[234:235], v175 offset:0x1000
	ds_read_b64_tr_b16 v[236:237], v175 offset:0x1800
	ds_read_b64_tr_b16 v[238:239], v175 offset:0x2000
	ds_read_b64_tr_b16 v[240:241], v175 offset:0x2800
	ds_read_b64_tr_b16 v[242:243], v175 offset:0x3000
	ds_read_b64_tr_b16 v[244:245], v175 offset:0x3800
	s_waitcnt lgkmcnt(0)
	s_nop 0
	v_mfma_f32_32x32x16_bf16 v[2:17], v[226:229], v[230:233], v[2:17]
	ds_read_b64_tr_b16 v[230:231], v175 offset:0x200
	ds_read_b64_tr_b16 v[232:233], v175 offset:0xa00
	v_mfma_f32_32x32x16_bf16 v[2:17], v[150:153], v[234:237], v[2:17]
	ds_read_b64_tr_b16 v[234:235], v175 offset:0x1200
	ds_read_b64_tr_b16 v[236:237], v175 offset:0x1a00
	v_mfma_f32_32x32x16_bf16 v[2:17], v[142:145], v[238:241], v[2:17]
	ds_read_b64_tr_b16 v[238:239], v175 offset:0x2200
	ds_read_b64_tr_b16 v[240:241], v175 offset:0x2a00
	ds_read_b64_tr_b16 v[246:247], v175 offset:0x3200
	ds_read_b64_tr_b16 v[248:249], v175 offset:0x3a00
	v_mfma_f32_32x32x16_bf16 v[2:17], v[146:149], v[242:245], v[2:17]
	s_waitcnt lgkmcnt(0)
; #define SBAR() __builtin_amdgcn_sched_barrier(0)
; template <int MODE>
; __device__ __forceinline__ void partialSM(f32x16& p0, f32x16& p1, float& m_reg, float& mn, float& alpha) {
;     constexpr float SCALE = Cfg<MODE>::SCALE, C = SCALE * 1.4426950408889634f;
;     float pmax = p0[0];
; #pragma unroll
;     for (int r = 1; r < 16; ++r) pmax = fmaxf(pmax, p0[r]);
; #pragma unroll
;     for (int r = 0; r < 16; ++r) pmax = fmaxf(pmax, p1[r]);
;     { auto rr = __builtin_amdgcn_permlane32_swap(__float_as_uint(pmax), __float_as_uint(pmax), false, false);
;       pmax = fmaxf(__uint_as_float(rr[0]), __uint_as_float(rr[1])); }
;     if (__builtin_expect(__all(pmax - m_reg <= THR / SCALE), 1)) { mn = m_reg; alpha = 1.f; }
;     else { mn = fmaxf(m_reg, pmax); alpha = __builtin_amdgcn_exp2f((m_reg - mn) * C); m_reg = mn; }
; template <int D0> __device__ __forceinline__ void pv_one(f32x16& od, int vb, bf16x8 pa0, bf16x8 pa1, bf16x8 pa2, bf16x8 pa3) {
;     const s16x4 l0 = tr_read<v_rd_off(D0, 0, 0)>(vb), h0 = tr_read<v_rd_off(D0, 0, 1)>(vb), l1 = tr_read<v_rd_off(D0, 1, 0)>(vb), h1 = tr_read<v_rd_off(D0, 1, 1)>(vb);
;     const s16x4 l2 = tr_read<v_rd_off(D0, 2, 0)>(vb), h2 = tr_read<v_rd_off(D0, 2, 1)>(vb), l3 = tr_read<v_rd_off(D0, 3, 0)>(vb), h3 = tr_read<v_rd_off(D0, 3, 1)>(vb);
;     asm volatile("s_waitcnt lgkmcnt(0)" ::: "memory"); SBAR();
;     ...
;     od = __builtin_amdgcn_mfma_f32_32x32x16_bf16(pa0, PKV(l0, h0), od, 0, 0, 0);
;     od = __builtin_amdgcn_mfma_f32_32x32x16_bf16(pa1, PKV(l1, h1), od, 0, 0, 0);
;     od = __builtin_amdgcn_mfma_f32_32x32x16_bf16(pa2, PKV(l2, h2), od, 0, 0, 0);
;     od = __builtin_amdgcn_mfma_f32_32x32x16_bf16(pa3, PKV(l3, h3), od, 0, 0, 0);
;     ...
; }
; __device__ __forceinline__ void pv_d0(f32x16* o, int vb, bf16x8 pa0, bf16x8 pa1, bf16x8 pa2, bf16x8 pa3) {
;     pv_one<0>(o[0], vb, pa0, pa1, pa2, pa3); pv_one<1>(o[1], vb, pa0, pa1, pa2, pa3); pv_one<2>(o[2], vb, pa0, pa1, pa2, pa3); pv_one<3>(o[3], vb, pa0, pa1, pa2, pa3);
	v_mfma_f32_32x32x16_bf16 v[50:65], v[226:229], v[230:233], v[50:65]
	ds_read_b64_tr_b16 v[230:231], v175 offset:0x400
	ds_read_b64_tr_b16 v[232:233], v175 offset:0xc00
	v_mfma_f32_32x32x16_bf16 v[50:65], v[150:153], v[234:237], v[50:65]
	ds_read_b64_tr_b16 v[234:235], v175 offset:0x1400
	ds_read_b64_tr_b16 v[236:237], v175 offset:0x1c00
	v_mfma_f32_32x32x16_bf16 v[50:65], v[142:145], v[238:241], v[50:65]
	ds_read_b64_tr_b16 v[238:239], v175 offset:0x2400
	ds_read_b64_tr_b16 v[240:241], v175 offset:0x2c00
	ds_read_b64_tr_b16 v[242:243], v175 offset:0x3400
	ds_read_b64_tr_b16 v[244:245], v175 offset:0x3c00
	v_mfma_f32_32x32x16_bf16 v[50:65], v[146:149], v[246:249], v[50:65]
	s_waitcnt lgkmcnt(0)
	v_mfma_f32_32x32x16_bf16 v[34:49], v[226:229], v[230:233], v[34:49]
	ds_read_b64_tr_b16 v[230:231], v175 offset:0x600
	ds_read_b64_tr_b16 v[232:233], v175 offset:0xe00
	v_mfma_f32_32x32x16_bf16 v[34:49], v[150:153], v[234:237], v[34:49]
	ds_read_b64_tr_b16 v[234:235], v175 offset:0x1600
	ds_read_b64_tr_b16 v[236:237], v175 offset:0x1e00
	v_mfma_f32_32x32x16_bf16 v[34:49], v[142:145], v[238:241], v[34:49]
	ds_read_b64_tr_b16 v[238:239], v175 offset:0x2600
	ds_read_b64_tr_b16 v[240:241], v175 offset:0x2e00
	ds_read_b64_tr_b16 v[246:247], v175 offset:0x3600
	ds_read_b64_tr_b16 v[248:249], v175 offset:0x3e00
	v_mfma_f32_32x32x16_bf16 v[34:49], v[146:149], v[242:245], v[34:49]
	s_waitcnt lgkmcnt(0)
	v_mfma_f32_32x32x16_bf16 v[18:33], v[226:229], v[230:233], v[18:33]
	v_max_f32_e32 v138, v83, v83
	v_max_f32_e32 v139, v82, v82
	v_max_f32_e32 v138, v139, v138
	v_max3_f32 v138, v138, v84, v85
	v_max3_f32 v138, v138, v86, v87
	v_max3_f32 v138, v138, v88, v89
	v_max3_f32 v138, v138, v90, v91
	v_max3_f32 v138, v138, v92, v93
	v_mfma_f32_32x32x16_bf16 v[18:33], v[150:153], v[234:237], v[18:33]
	v_max3_f32 v138, v138, v94, v95
	v_max3_f32 v138, v138, v96, v97
	v_max3_f32 v138, v138, v66, v67
	v_max3_f32 v138, v138, v68, v69
	v_max3_f32 v138, v138, v70, v71
	v_max3_f32 v138, v138, v72, v73
	v_max3_f32 v138, v138, v74, v75
	v_max3_f32 v138, v138, v76, v77
	v_mfma_f32_32x32x16_bf16 v[18:33], v[142:145], v[238:241], v[18:33]
	v_max3_f32 v138, v138, v78, v79
	v_max3_f32 v138, v138, v80, v81
	v_mov_b32_e32 v139, v138
	s_nop 1
	v_permlane32_swap_b32_e32 v138, v139
	v_max_f32_e32 v139, v139, v139
	v_max_f32_e32 v138, v138, v138
	v_max_f32_e32 v138, v138, v139
	v_max_f32_e32 v141, v140, v140
	v_sub_f32_e32 v139, v138, v140
	v_max_f32_e32 v138, v141, v138
	v_mfma_f32_32x32x16_bf16 v[18:33], v[146:149], v[246:249], v[18:33]
	v_sub_f32_e32 v141, v140, v138
	v_mul_f32_e32 v141, 0x3e38aa3b, v141
	v_exp_f32_e32 v141, v141
	v_cmp_ge_f32_e32 vcc, s7, v139
	s_cmp_eq_u64 vcc, exec
	s_cselect_b64 s[4:5], -1, 0
	s_barrier
	s_waitcnt vmcnt(3)
	v_cndmask_b32_e64 v226, v141, 1.0, s[4:5]
	v_cmp_gt_f32_e32 vcc, 1.0, v226
	s_waitcnt vmcnt(3)
	ds_write_b128 v215, v[118:121]
	ds_write_b128 v216, v[122:125]
	ds_write_b128 v222, v[114:117] offset:32768
	s_cbranch_vccz .LBB0_416
	s_and_saveexec_b64 s[48:49], s[0:1]
	ds_write_b32 v171, v226 offset:128
	s_or_b64 exec, exec, s[48:49]
	s_waitcnt lgkmcnt(0)
	ds_read_b128 v[142:145], v207 offset:224
	ds_read_b128 v[146:149], v207 offset:192
	ds_read_b128 v[150:153], v207 offset:160
	ds_read_b128 v[228:231], v207 offset:128
	s_waitcnt lgkmcnt(3)
	v_pk_mul_f32 v[16:17], v[16:17], v[144:145]
	s_waitcnt lgkmcnt(2)
	v_pk_mul_f32 v[12:13], v[12:13], v[148:149]
	s_waitcnt lgkmcnt(1)
	v_pk_mul_f32 v[8:9], v[8:9], v[152:153]
	s_waitcnt lgkmcnt(0)
	v_pk_mul_f32 v[4:5], v[4:5], v[230:231]
	v_pk_mul_f32 v[14:15], v[14:15], v[142:143]
	v_pk_mul_f32 v[10:11], v[10:11], v[146:147]
	v_pk_mul_f32 v[6:7], v[6:7], v[150:151]
	v_pk_mul_f32 v[2:3], v[2:3], v[228:229]
	v_pk_mul_f32 v[64:65], v[64:65], v[144:145]
	v_pk_mul_f32 v[60:61], v[60:61], v[148:149]
	v_pk_mul_f32 v[56:57], v[56:57], v[152:153]
	v_pk_mul_f32 v[52:53], v[52:53], v[230:231]
	v_pk_mul_f32 v[62:63], v[62:63], v[142:143]
	v_pk_mul_f32 v[58:59], v[58:59], v[146:147]
	v_pk_mul_f32 v[54:55], v[54:55], v[150:151]
	v_pk_mul_f32 v[50:51], v[50:51], v[228:229]
	v_pk_mul_f32 v[48:49], v[48:49], v[144:145]
	v_pk_mul_f32 v[44:45], v[44:45], v[148:149]
	v_pk_mul_f32 v[40:41], v[40:41], v[152:153]
	v_pk_mul_f32 v[36:37], v[36:37], v[230:231]
	v_pk_mul_f32 v[46:47], v[46:47], v[142:143]
	v_pk_mul_f32 v[42:43], v[42:43], v[146:147]
	v_pk_mul_f32 v[38:39], v[38:39], v[150:151]
	v_pk_mul_f32 v[34:35], v[34:35], v[228:229]
	v_pk_mul_f32 v[32:33], v[32:33], v[144:145]
	v_pk_mul_f32 v[28:29], v[28:29], v[148:149]
	v_pk_mul_f32 v[24:25], v[24:25], v[152:153]
	v_pk_mul_f32 v[20:21], v[20:21], v[230:231]
	v_pk_mul_f32 v[30:31], v[30:31], v[142:143]
	v_pk_mul_f32 v[26:27], v[26:27], v[146:147]
	v_pk_mul_f32 v[22:23], v[22:23], v[150:151]
	v_pk_mul_f32 v[18:19], v[18:19], v[228:229]

; #define SBAR() __builtin_amdgcn_sched_barrier(0)
; #define SWAIT() do { if constexpr (MODE == 1) asm volatile("s_waitcnt vmcnt(3)" ::: "memory"); else asm volatile("s_waitcnt vmcnt(4)" ::: "memory"); } while (0)
; template <int D0> __device__ __forceinline__ void pv_one(f32x16& od, int vb, bf16x8 pa0, bf16x8 pa1, bf16x8 pa2, bf16x8 pa3) {
;     const s16x4 l0 = tr_read<v_rd_off(D0, 0, 0)>(vb), h0 = tr_read<v_rd_off(D0, 0, 1)>(vb), l1 = tr_read<v_rd_off(D0, 1, 0)>(vb), h1 = tr_read<v_rd_off(D0, 1, 1)>(vb);
;     const s16x4 l2 = tr_read<v_rd_off(D0, 2, 0)>(vb), h2 = tr_read<v_rd_off(D0, 2, 1)>(vb), l3 = tr_read<v_rd_off(D0, 3, 0)>(vb), h3 = tr_read<v_rd_off(D0, 3, 1)>(vb);
;     asm volatile("s_waitcnt lgkmcnt(0)" ::: "memory"); SBAR();
;     ...
;     od = __builtin_amdgcn_mfma_f32_32x32x16_bf16(pa0, PKV(l0, h0), od, 0, 0, 0);
;     od = __builtin_amdgcn_mfma_f32_32x32x16_bf16(pa1, PKV(l1, h1), od, 0, 0, 0);
;     od = __builtin_amdgcn_mfma_f32_32x32x16_bf16(pa2, PKV(l2, h2), od, 0, 0, 0);
;     od = __builtin_amdgcn_mfma_f32_32x32x16_bf16(pa3, PKV(l3, h3), od, 0, 0, 0);
;     ...
; }
; __device__ __forceinline__ void pv_d0(f32x16* o, int vb, bf16x8 pa0, bf16x8 pa1, bf16x8 pa2, bf16x8 pa3) {
;     pv_one<0>(o[0], vb, pa0, pa1, pa2, pa3); pv_one<1>(o[1], vb, pa0, pa1, pa2, pa3); pv_one<2>(o[2], vb, pa0, pa1, pa2, pa3); pv_one<3>(o[3], vb, pa0, pa1, pa2, pa3);
; template <int MODE>
; __device__ __forceinline__ void attn_pass(const bf16_t* __restrict__ Qb, const bf16_t* __restrict__ Kh, const bf16_t* __restrict__ Vh, const int NT, const int kr0, const int g4, const int map,
;                                           LAS unsigned char* lds, f32x16 (&o)[4]) {
;     ...
;         __syncthreads(); SWAIT(); SWRITE(0, SE);
;         RESC(alB); __syncthreads();
;         SBAR(); qkt<MODE>(pA0, pA1, K_lds, qr, Qs, r32, hi, cbase); MASK(pA0, pA1, j + 1);
;         finishSM(pB0, pB1, alB, l_reg, pa0, pa1, pa2, pa3); SBAR();
;         if (j + 3 < NT) SLOAD(SE, j + 3); SBAR();
;         pv_d0(o, vb0 + SHM_V, pa0, pa1, pa2, pa3); partialSM<MODE>(pA0, pA1, m_reg, mnA, alA);
;         __syncthreads(); SWAIT(); SWRITE(1, SO);
;         RESC(alA); __syncthreads();
.LBB0_418:
	ds_read_b64_tr_b16 v[200:201], v173 offset:0
	ds_read_b64_tr_b16 v[202:203], v173 offset:0x800
	ds_read_b64_tr_b16 v[230:231], v173 offset:0x1000
	ds_read_b64_tr_b16 v[232:233], v173 offset:0x1800
	ds_read_b64_tr_b16 v[234:235], v173 offset:0x2000
	ds_read_b64_tr_b16 v[236:237], v173 offset:0x2800
	ds_read_b64_tr_b16 v[238:239], v173 offset:0x3000
	ds_read_b64_tr_b16 v[240:241], v173 offset:0x3800
	s_waitcnt lgkmcnt(0)
	s_nop 0
	v_mfma_f32_32x32x16_bf16 v[2:17], v[138:141], v[200:203], v[2:17]
	ds_read_b64_tr_b16 v[200:201], v173 offset:0x200
	ds_read_b64_tr_b16 v[202:203], v173 offset:0xa00
	v_mfma_f32_32x32x16_bf16 v[2:17], v[142:145], v[230:233], v[2:17]
	ds_read_b64_tr_b16 v[230:231], v173 offset:0x1200
	ds_read_b64_tr_b16 v[232:233], v173 offset:0x1a00
	v_mfma_f32_32x32x16_bf16 v[2:17], v[150:153], v[234:237], v[2:17]
	ds_read_b64_tr_b16 v[234:235], v173 offset:0x2200
	ds_read_b64_tr_b16 v[236:237], v173 offset:0x2a00
	ds_read_b64_tr_b16 v[242:243], v173 offset:0x3200
	ds_read_b64_tr_b16 v[244:245], v173 offset:0x3a00
	v_mfma_f32_32x32x16_bf16 v[2:17], v[146:149], v[238:241], v[2:17]
	s_waitcnt lgkmcnt(0)
	v_mfma_f32_32x32x16_bf16 v[50:65], v[138:141], v[200:203], v[50:65]
	ds_read_b64_tr_b16 v[200:201], v173 offset:0x400
	ds_read_b64_tr_b16 v[202:203], v173 offset:0xc00
	v_mfma_f32_32x32x16_bf16 v[50:65], v[142:145], v[230:233], v[50:65]
	ds_read_b64_tr_b16 v[230:231], v173 offset:0x1400
	ds_read_b64_tr_b16 v[232:233], v173 offset:0x1c00
	v_mfma_f32_32x32x16_bf16 v[50:65], v[150:153], v[234:237], v[50:65]
	ds_read_b64_tr_b16 v[234:235], v173 offset:0x2400
	ds_read_b64_tr_b16 v[236:237], v173 offset:0x2c00
	ds_read_b64_tr_b16 v[238:239], v173 offset:0x3400
	ds_read_b64_tr_b16 v[240:241], v173 offset:0x3c00
	v_mfma_f32_32x32x16_bf16 v[50:65], v[146:149], v[242:245], v[50:65]
	s_waitcnt lgkmcnt(0)
	v_mfma_f32_32x32x16_bf16 v[34:49], v[138:141], v[200:203], v[34:49]
	ds_read_b64_tr_b16 v[200:201], v173 offset:0x600
	ds_read_b64_tr_b16 v[202:203], v173 offset:0xe00
	v_mfma_f32_32x32x16_bf16 v[34:49], v[142:145], v[230:233], v[34:49]
	ds_read_b64_tr_b16 v[230:231], v173 offset:0x1600
	ds_read_b64_tr_b16 v[232:233], v173 offset:0x1e00
	v_mfma_f32_32x32x16_bf16 v[34:49], v[150:153], v[234:237], v[34:49]
	ds_read_b64_tr_b16 v[234:235], v173 offset:0x2600
	ds_read_b64_tr_b16 v[236:237], v173 offset:0x2e00
	ds_read_b64_tr_b16 v[242:243], v173 offset:0x3600
	ds_read_b64_tr_b16 v[244:245], v173 offset:0x3e00
	v_mfma_f32_32x32x16_bf16 v[34:49], v[146:149], v[238:241], v[34:49]
	s_waitcnt lgkmcnt(0)
	v_mfma_f32_32x32x16_bf16 v[18:33], v[138:141], v[200:203], v[18:33]
	v_max_f32_e32 v238, v83, v83
	v_max_f32_e32 v239, v82, v82
	v_max_f32_e32 v238, v239, v238
	v_max3_f32 v238, v238, v84, v85
	v_max3_f32 v238, v238, v86, v87
	v_max3_f32 v138, v238, v88, v89
	v_max3_f32 v138, v138, v90, v91
	v_max3_f32 v138, v138, v92, v93
	v_mfma_f32_32x32x16_bf16 v[18:33], v[142:145], v[230:233], v[18:33]
	v_max3_f32 v138, v138, v94, v95
	v_max3_f32 v138, v138, v96, v97
	v_max3_f32 v138, v138, v66, v67
	v_max3_f32 v138, v138, v68, v69
	v_max3_f32 v138, v138, v70, v71
	v_max3_f32 v138, v138, v72, v73
	v_max3_f32 v138, v138, v74, v75
	v_max3_f32 v138, v138, v76, v77
	v_mfma_f32_32x32x16_bf16 v[18:33], v[150:153], v[234:237], v[18:33]
	v_max3_f32 v138, v138, v78, v79
	v_max3_f32 v138, v138, v80, v81
	v_mov_b32_e32 v139, v138
	s_nop 1
	v_permlane32_swap_b32_e32 v138, v139
	v_max_f32_e32 v139, v139, v139
	v_max_f32_e32 v138, v138, v138
	v_max_f32_e32 v138, v138, v139
	v_max_f32_e32 v140, v227, v227
	v_sub_f32_e32 v139, v138, v227
	v_max_f32_e32 v138, v140, v138
	v_mfma_f32_32x32x16_bf16 v[18:33], v[146:149], v[242:245], v[18:33]
	v_sub_f32_e32 v140, v227, v138
	v_mul_f32_e32 v140, 0x3e38aa3b, v140
	v_exp_f32_e32 v140, v140
	v_cmp_ge_f32_e32 vcc, s7, v139
	s_cmp_eq_u64 vcc, exec
	s_cselect_b64 s[4:5], -1, 0
	s_barrier
	s_waitcnt vmcnt(3)
	v_cndmask_b32_e64 v141, v140, 1.0, s[4:5]
	v_cmp_gt_f32_e32 vcc, 1.0, v141
	s_waitcnt vmcnt(3)
	ds_write_b128 v215, v[126:129] offset:16384
	s_waitcnt vmcnt(3)
	ds_write_b128 v216, v[130:133] offset:16384
	s_waitcnt vmcnt(3)
	ds_write_b128 v222, v[134:137] offset:49152
	s_cbranch_vccz .LBB0_422
	s_and_saveexec_b64 s[52:53], s[0:1]
	ds_write_b32 v171, v141 offset:128
	s_or_b64 exec, exec, s[52:53]
	s_waitcnt lgkmcnt(0)
	ds_read_b128 v[126:129], v207 offset:224
	ds_read_b128 v[130:133], v207 offset:192
	ds_read_b128 v[134:137], v207 offset:160
	ds_read_b128 v[142:145], v207 offset:128
	s_waitcnt lgkmcnt(3)
	v_pk_mul_f32 v[16:17], v[16:17], v[128:129]
	s_waitcnt lgkmcnt(2)
	v_pk_mul_f32 v[12:13], v[12:13], v[132:133]
	s_waitcnt lgkmcnt(1)
	v_pk_mul_f32 v[8:9], v[8:9], v[136:137]
	s_waitcnt lgkmcnt(0)
	v_pk_mul_f32 v[4:5], v[4:5], v[144:145]
	v_pk_mul_f32 v[14:15], v[14:15], v[126:127]
	v_pk_mul_f32 v[10:11], v[10:11], v[130:131]
	v_pk_mul_f32 v[6:7], v[6:7], v[134:135]
	v_pk_mul_f32 v[2:3], v[2:3], v[142:143]
	v_pk_mul_f32 v[64:65], v[64:65], v[128:129]
	v_pk_mul_f32 v[60:61], v[60:61], v[132:133]
	v_pk_mul_f32 v[56:57], v[56:57], v[136:137]
	v_pk_mul_f32 v[52:53], v[52:53], v[144:145]
	v_pk_mul_f32 v[62:63], v[62:63], v[126:127]
	v_pk_mul_f32 v[58:59], v[58:59], v[130:131]
	v_pk_mul_f32 v[54:55], v[54:55], v[134:135]
	v_pk_mul_f32 v[50:51], v[50:51], v[142:143]
	v_pk_mul_f32 v[48:49], v[48:49], v[128:129]
	v_pk_mul_f32 v[44:45], v[44:45], v[132:133]
	v_pk_mul_f32 v[40:41], v[40:41], v[136:137]
	v_pk_mul_f32 v[36:37], v[36:37], v[144:145]
	v_pk_mul_f32 v[46:47], v[46:47], v[126:127]
	v_pk_mul_f32 v[42:43], v[42:43], v[130:131]
	v_pk_mul_f32 v[38:39], v[38:39], v[134:135]
	v_pk_mul_f32 v[34:35], v[34:35], v[142:143]
	v_pk_mul_f32 v[32:33], v[32:33], v[128:129]
	v_pk_mul_f32 v[28:29], v[28:29], v[132:133]
	v_pk_mul_f32 v[24:25], v[24:25], v[136:137]
	v_pk_mul_f32 v[20:21], v[20:21], v[144:145]
	v_pk_mul_f32 v[30:31], v[30:31], v[126:127]
	v_pk_mul_f32 v[26:27], v[26:27], v[130:131]
	v_pk_mul_f32 v[22:23], v[22:23], v[134:135]
	v_pk_mul_f32 v[18:19], v[18:19], v[142:143]

; #define LAS __attribute__((address_space(3)))
; __device__ __forceinline__ void finishSM(f32x16& p0, f32x16& p1, float alpha, float& l_reg, bf16x8& pa0, bf16x8& pa1, bf16x8& pa2, bf16x8& pa3) {
; #pragma unroll
;     for (int r = 0; r < 16; ++r) p1[r] = __builtin_amdgcn_exp2f(p1[r]);
;     float ps = 0;
; #pragma unroll
;     for (int r = 0; r < 16; ++r) ps += p0[r];
; #pragma unroll
;     for (int r = 0; r < 16; ++r) ps += p1[r];
;     { auto rr = __builtin_amdgcn_permlane32_swap(__float_as_uint(ps), __float_as_uint(ps), false, false);
;       ps = __uint_as_float(rr[0]) + __uint_as_float(rr[1]); }
;     l_reg = l_reg * alpha + ps;
;     ...
;     PK4(p0, 0, pa0); PK4(p0, 8, pa1); PK4(p1, 0, pa2); PK4(p1, 8, pa3);
;     ...
; }
; template <int MODE>
; __device__ __forceinline__ void qkt(f32x16& p0, f32x16& p1, const LAS unsigned char* Ks, const bf16x8* qr, const LAS unsigned char* Qs, int r32, int hi, int cbase) {
;     p0 = f32x16{}; p1 = f32x16{};
; #pragma unroll
;     for (int d0 = 0; d0 < Cfg<MODE>::ND; ++d0) { const int cb = cbase + (d0 * 16 + hi * 8) * 2;
;         const bf16x8 b0 = *(const LAS bf16x8*)(Ks + KSWZ(r32, cb));
;         const bf16x8 b1 = *(const LAS bf16x8*)(Ks + KSWZ(32 + r32, cb));
;         bf16x8 q; if constexpr (MODE == 0) q = *(const LAS bf16x8*)(Qs + KSWZ(r32, cb)); else q = qr[d0];
;         p0 = __builtin_amdgcn_mfma_f32_32x32x16_bf16(b0, q, p0, 0, 0, 0);
;         p1 = __builtin_amdgcn_mfma_f32_32x32x16_bf16(b1, q, p1, 0, 0, 0); }
; }
; __device__ __forceinline__ int v_st(int k, int c) { const int kk = (k & ~0xC) | ((k & 4) << 1) | ((k & 8) >> 1); return ((kk >> 3) * 4 + (c >> 5)) * 512 + ((kk & 7) * 32 + (c & 31)) * 2; }
; __device__ __forceinline__ int v_rd_base(int lane) { return ((lane & 3) << 3) | (((lane >> 2) & 3) << 6) | (((lane >> 4) & 1) << 5) | (((lane >> 5) & 1) << 8); }
; template <int OFF> __device__ __forceinline__ s16x4 tr_read(int vb) {
;     s16x4 r; asm volatile("ds_read_b64_tr_b16 %0, %1 offset:%2" : "=&v"(r) : "v"(vb), "i"(OFF) : "memory"); return r;
; }
; template <int D0> __device__ __forceinline__ void pv_one(f32x16& od, int vb, bf16x8 pa0, bf16x8 pa1, bf16x8 pa2, bf16x8 pa3) {
;     const s16x4 l0 = tr_read<v_rd_off(D0, 0, 0)>(vb), h0 = tr_read<v_rd_off(D0, 0, 1)>(vb), l1 = tr_read<v_rd_off(D0, 1, 0)>(vb), h1 = tr_read<v_rd_off(D0, 1, 1)>(vb);
.LBB0_424:
	v_mul_f32_e32 v68, 0x3fb8aa3b, v194
	s_mov_b32 s4, 0x3fb8aa3b
	v_rndne_f32_e32 v69, v68
	v_sub_f32_e32 v70, v68, v69
	v_fma_f32 v68, v194, s4, -v68
	v_fmamk_f32 v68, v194, 0x32a5705f, v68
	v_add_f32_e32 v68, v70, v68
	v_exp_f32_e32 v68, v68
	v_cvt_i32_f32_e32 v69, v69
	s_mov_b32 s4, 0xc2ce8ed0
	v_cmp_ngt_f32_e32 vcc, s4, v194
	s_mov_b32 s4, 0x42b17218
	v_ldexp_f32 v68, v68, v69
	v_cndmask_b32_e32 v114, 0, v68, vcc
	v_cmp_nlt_f32_e64 s[4:5], s4, v194
	v_mov_b32_e32 v115, 0x7f800000
	ds_read_b128 v[68:71], v204 offset:49152
	ds_read_b128 v[72:75], v204 offset:57344
	ds_read_b128 v[116:119], v195 offset:49152
	ds_read_b128 v[120:123], v195 offset:57344
	ds_read_b128 v[196:199], v205 offset:49152
	ds_read_b128 v[222:225], v205 offset:57344
	s_waitcnt lgkmcnt(5)
	v_mfma_f32_32x32x16_bf16 v[82:97], v[68:71], v[110:113], 0
	v_exp_f32_e32 v124, v132
	v_exp_f32_e32 v125, v133
	v_exp_f32_e32 v132, v66
	v_exp_f32_e32 v133, v67
	v_exp_f32_e32 v130, v130
	ds_read_b128 v[226:229], v206 offset:49152
	ds_read_b128 v[230:233], v206 offset:57344
	s_waitcnt lgkmcnt(6)
	v_mfma_f32_32x32x16_bf16 v[66:81], v[72:75], v[110:113], 0
	v_exp_f32_e32 v110, v131
	v_exp_f32_e32 v111, v128
	v_exp_f32_e32 v112, v129
	v_exp_f32_e32 v113, v126
	v_exp_f32_e32 v126, v127
	v_exp_f32_e32 v127, v138
	v_exp_f32_e32 v128, v139
	s_waitcnt lgkmcnt(5)
	v_mfma_f32_32x32x16_bf16 v[82:97], v[116:119], v[106:109], v[82:97]
	v_add_f32_e32 v116, 0, v201
	v_add_f32_e32 v116, v203, v116
	v_add_f32_e32 v116, v153, v116
	v_exp_f32_e32 v118, v136
	v_exp_f32_e32 v119, v137
	v_exp_f32_e32 v129, v134
	v_exp_f32_e32 v131, v135
	s_waitcnt lgkmcnt(4)
	v_mfma_f32_32x32x16_bf16 v[66:81], v[120:123], v[106:109], v[66:81]
	v_add_f32_e32 v106, v202, v116
	v_add_f32_e32 v106, v151, v106
	v_add_f32_e32 v106, v200, v106
	v_add_f32_e32 v106, v150, v106
	v_add_f32_e32 v106, v152, v106
	v_add_f32_e32 v106, v147, v106
	v_add_f32_e32 v106, v149, v106
	v_add_f32_e32 v106, v145, v106
	v_add_f32_e32 v106, v148, v106
	v_add_f32_e32 v106, v143, v106
	v_add_f32_e32 v106, v146, v106
	v_add_f32_e32 v106, v142, v106
	v_add_f32_e32 v106, v144, v106
	v_add_f32_e32 v106, v124, v106
	s_waitcnt lgkmcnt(3)
	v_mfma_f32_32x32x16_bf16 v[82:97], v[196:199], v[102:105], v[82:97]
	s_waitcnt lgkmcnt(2)
	v_mfma_f32_32x32x16_bf16 v[66:81], v[222:225], v[102:105], v[66:81]
	v_add_f32_e32 v102, v125, v106
	v_add_f32_e32 v102, v132, v102
	v_add_f32_e32 v102, v133, v102
	v_add_f32_e32 v102, v130, v102
	v_add_f32_e32 v102, v110, v102
	v_add_f32_e32 v102, v111, v102
	v_add_f32_e32 v102, v112, v102
	v_add_f32_e32 v102, v113, v102
	v_add_f32_e32 v102, v126, v102
	s_waitcnt lgkmcnt(1)
	v_mfma_f32_32x32x16_bf16 v[82:97], v[226:229], v[98:101], v[82:97]
	v_add_f32_e32 v102, v127, v102
	v_add_f32_e32 v102, v128, v102
	v_add_f32_e32 v102, v118, v102
	v_add_f32_e32 v102, v119, v102
	v_add_f32_e32 v102, v129, v102
	s_waitcnt lgkmcnt(0)
	v_mfma_f32_32x32x16_bf16 v[66:81], v[230:233], v[98:101], v[66:81]
	v_add_f32_e32 v98, v131, v102
	v_mov_b32_e32 v99, v98
	v_cvt_pk_bf16_f32 v100, v201, v203
	v_cvt_pk_bf16_f32 v101, v153, v202
	v_cvt_pk_bf16_f32 v102, v151, v200
	v_cvt_pk_bf16_f32 v103, v150, v152
	s_nop 1
	v_permlane32_swap_b32_e32 v98, v99
	v_permlane32_swap_b32_e32 v100, v102
	v_permlane32_swap_b32_e32 v101, v103
	v_cvt_pk_bf16_f32 v104, v147, v149
	v_cvt_pk_bf16_f32 v105, v145, v148
	v_cvt_pk_bf16_f32 v106, v143, v146
	v_cvt_pk_bf16_f32 v107, v142, v144
	v_cvt_pk_bf16_f32 v108, v124, v125
	v_cvt_pk_bf16_f32 v109, v132, v133
	v_cvt_pk_bf16_f32 v110, v130, v110
	v_cvt_pk_bf16_f32 v111, v111, v112
	v_cvt_pk_bf16_f32 v116, v113, v126
	v_cvt_pk_bf16_f32 v117, v127, v128
	v_cvt_pk_bf16_f32 v118, v118, v119
	v_cvt_pk_bf16_f32 v119, v129, v131
	s_nop 0
	v_permlane32_swap_b32_e32 v104, v106
	v_permlane32_swap_b32_e32 v105, v107
	v_permlane32_swap_b32_e32 v108, v110
	v_permlane32_swap_b32_e32 v109, v111
	v_permlane32_swap_b32_e32 v116, v118
	v_permlane32_swap_b32_e32 v117, v119
	ds_read_b64_tr_b16 v[120:121], v175 offset:0
	ds_read_b64_tr_b16 v[122:123], v175 offset:0x800
	ds_read_b64_tr_b16 v[124:125], v175 offset:0x1000
	ds_read_b64_tr_b16 v[126:127], v175 offset:0x1800
	ds_read_b64_tr_b16 v[128:129], v175 offset:0x2000
	ds_read_b64_tr_b16 v[130:131], v175 offset:0x2800
	ds_read_b64_tr_b16 v[132:133], v175 offset:0x3000
	ds_read_b64_tr_b16 v[134:135], v175 offset:0x3800
	s_waitcnt lgkmcnt(0)
	s_nop 0
	v_mfma_f32_32x32x16_bf16 v[2:17], v[100:103], v[120:123], v[2:17]
	ds_read_b64_tr_b16 v[120:121], v175 offset:0x200
	ds_read_b64_tr_b16 v[122:123], v175 offset:0xa00
	v_mfma_f32_32x32x16_bf16 v[2:17], v[104:107], v[124:127], v[2:17]
	ds_read_b64_tr_b16 v[124:125], v175 offset:0x1200
	ds_read_b64_tr_b16 v[126:127], v175 offset:0x1a00
	v_mfma_f32_32x32x16_bf16 v[2:17], v[108:111], v[128:131], v[2:17]
	ds_read_b64_tr_b16 v[128:129], v175 offset:0x2200
	ds_read_b64_tr_b16 v[130:131], v175 offset:0x2a00
	ds_read_b64_tr_b16 v[136:137], v175 offset:0x3200
	ds_read_b64_tr_b16 v[138:139], v175 offset:0x3a00
	v_mfma_f32_32x32x16_bf16 v[2:17], v[116:119], v[132:135], v[2:17]
	s_waitcnt lgkmcnt(0)
	v_mfma_f32_32x32x16_bf16 v[50:65], v[100:103], v[120:123], v[50:65]
	ds_read_b64_tr_b16 v[120:121], v175 offset:0x400
	ds_read_b64_tr_b16 v[122:123], v175 offset:0xc00
	v_mfma_f32_32x32x16_bf16 v[50:65], v[104:107], v[124:127], v[50:65]
	ds_read_b64_tr_b16 v[124:125], v175 offset:0x1400
	ds_read_b64_tr_b16 v[126:127], v175 offset:0x1c00
	v_mfma_f32_32x32x16_bf16 v[50:65], v[108:111], v[128:131], v[50:65]
	ds_read_b64_tr_b16 v[128:129], v175 offset:0x2400
	ds_read_b64_tr_b16 v[130:131], v175 offset:0x2c00
	ds_read_b64_tr_b16 v[132:133], v175 offset:0x3400
	ds_read_b64_tr_b16 v[134:135], v175 offset:0x3c00
	v_mfma_f32_32x32x16_bf16 v[50:65], v[116:119], v[136:139], v[50:65]
	s_waitcnt lgkmcnt(0)
; #define SBAR() __builtin_amdgcn_sched_barrier(0)
; template <int MODE>
; __device__ __forceinline__ void partialSM(f32x16& p0, f32x16& p1, float& m_reg, float& mn, float& alpha) {
;     constexpr float SCALE = Cfg<MODE>::SCALE, C = SCALE * 1.4426950408889634f;
;     float pmax = p0[0];
; #pragma unroll
;     for (int r = 1; r < 16; ++r) pmax = fmaxf(pmax, p0[r]);
; #pragma unroll
;     for (int r = 0; r < 16; ++r) pmax = fmaxf(pmax, p1[r]);
;     { auto rr = __builtin_amdgcn_permlane32_swap(__float_as_uint(pmax), __float_as_uint(pmax), false, false);
;       pmax = fmaxf(__uint_as_float(rr[0]), __uint_as_float(rr[1])); }
;     if (__builtin_expect(__all(pmax - m_reg <= THR / SCALE), 1)) { mn = m_reg; alpha = 1.f; }
;     else { mn = fmaxf(m_reg, pmax); alpha = __builtin_amdgcn_exp2f((m_reg - mn) * C); m_reg = mn; }
;     const float mnC = -mn * C;
; #pragma unroll
;     for (int r = 0; r < 16; ++r) p0[r] = fmaf(p0[r], C, mnC);
; #pragma unroll
;     for (int r = 0; r < 16; ++r) p1[r] = fmaf(p1[r], C, mnC);
; #pragma unroll
;     for (int r = 0; r < 16; ++r) p0[r] = __builtin_amdgcn_exp2f(p0[r]);
; }
; template <int D0> __device__ __forceinline__ void pv_one(f32x16& od, int vb, bf16x8 pa0, bf16x8 pa1, bf16x8 pa2, bf16x8 pa3) {
;     const s16x4 l0 = tr_read<v_rd_off(D0, 0, 0)>(vb), h0 = tr_read<v_rd_off(D0, 0, 1)>(vb), l1 = tr_read<v_rd_off(D0, 1, 0)>(vb), h1 = tr_read<v_rd_off(D0, 1, 1)>(vb);
;     const s16x4 l2 = tr_read<v_rd_off(D0, 2, 0)>(vb), h2 = tr_read<v_rd_off(D0, 2, 1)>(vb), l3 = tr_read<v_rd_off(D0, 3, 0)>(vb), h3 = tr_read<v_rd_off(D0, 3, 1)>(vb);
;     asm volatile("s_waitcnt lgkmcnt(0)" ::: "memory"); SBAR();
;     ...
;     od = __builtin_amdgcn_mfma_f32_32x32x16_bf16(pa0, PKV(l0, h0), od, 0, 0, 0);
;     od = __builtin_amdgcn_mfma_f32_32x32x16_bf16(pa1, PKV(l1, h1), od, 0, 0, 0);
;     od = __builtin_amdgcn_mfma_f32_32x32x16_bf16(pa2, PKV(l2, h2), od, 0, 0, 0);
;     od = __builtin_amdgcn_mfma_f32_32x32x16_bf16(pa3, PKV(l3, h3), od, 0, 0, 0);
;     ...
; }
; __device__ __forceinline__ void pv_d0(f32x16* o, int vb, bf16x8 pa0, bf16x8 pa1, bf16x8 pa2, bf16x8 pa3) {
;     pv_one<0>(o[0], vb, pa0, pa1, pa2, pa3); pv_one<1>(o[1], vb, pa0, pa1, pa2, pa3); pv_one<2>(o[2], vb, pa0, pa1, pa2, pa3); pv_one<3>(o[3], vb, pa0, pa1, pa2, pa3);
	v_mfma_f32_32x32x16_bf16 v[34:49], v[100:103], v[120:123], v[34:49]
	ds_read_b64_tr_b16 v[120:121], v175 offset:0x600
	ds_read_b64_tr_b16 v[122:123], v175 offset:0xe00
	v_mfma_f32_32x32x16_bf16 v[34:49], v[104:107], v[124:127], v[34:49]
	ds_read_b64_tr_b16 v[124:125], v175 offset:0x1600
	ds_read_b64_tr_b16 v[126:127], v175 offset:0x1e00
	v_mfma_f32_32x32x16_bf16 v[34:49], v[108:111], v[128:131], v[34:49]
	ds_read_b64_tr_b16 v[128:129], v175 offset:0x2600
	ds_read_b64_tr_b16 v[130:131], v175 offset:0x2e00
	ds_read_b64_tr_b16 v[136:137], v175 offset:0x3600
	ds_read_b64_tr_b16 v[138:139], v175 offset:0x3e00
	v_mfma_f32_32x32x16_bf16 v[34:49], v[116:119], v[132:135], v[34:49]
	s_waitcnt lgkmcnt(0)
	v_mfma_f32_32x32x16_bf16 v[18:33], v[100:103], v[120:123], v[18:33]
	v_max_f32_e32 v112, v83, v83
	v_max_f32_e32 v113, v82, v82
	v_max_f32_e32 v112, v113, v112
	v_max3_f32 v112, v112, v84, v85
	v_max3_f32 v112, v112, v86, v87
	v_max3_f32 v100, v112, v88, v89
	v_max3_f32 v100, v100, v90, v91
	v_max3_f32 v100, v100, v92, v93
	v_mfma_f32_32x32x16_bf16 v[18:33], v[104:107], v[124:127], v[18:33]
	v_max3_f32 v100, v100, v94, v95
	v_max3_f32 v100, v100, v96, v97
	v_max3_f32 v100, v100, v66, v67
	v_max3_f32 v100, v100, v68, v69
	v_max3_f32 v100, v100, v70, v71
	v_max3_f32 v100, v100, v72, v73
	v_max3_f32 v100, v100, v74, v75
	v_max3_f32 v100, v100, v76, v77
	v_mfma_f32_32x32x16_bf16 v[18:33], v[108:111], v[128:131], v[18:33]
	v_max3_f32 v100, v100, v78, v79
	v_max3_f32 v100, v100, v80, v81
	v_mov_b32_e32 v101, v100
	s_nop 1
	v_permlane32_swap_b32_e32 v100, v101
	v_max_f32_e32 v101, v101, v101
	v_max_f32_e32 v100, v100, v100
	v_max_f32_e32 v100, v100, v101
	v_max_f32_e32 v102, v140, v140
	v_max_f32_e32 v102, v102, v100
	v_sub_f32_e32 v101, v100, v140
	v_mfma_f32_32x32x16_bf16 v[18:33], v[116:119], v[136:139], v[18:33]
	v_sub_f32_e32 v100, v140, v102
	s_mov_b32 s6, 0x42800000
	v_mul_f32_e32 v100, 0x3e38aa3b, v100
	v_exp_f32_e32 v100, v100
	v_cmp_ge_f32_e32 vcc, s6, v101
	s_cmp_eq_u64 vcc, exec
	s_cselect_b64 vcc, -1, 0
	v_cndmask_b32_e32 v101, v102, v140, vcc
	v_cndmask_b32_e64 v100, v100, 1.0, vcc
	v_mul_f32_e32 v101, 0xbe38aa3b, v101
	v_fmamk_f32 v82, v82, 0x3e38aa3b, v101
	v_fmamk_f32 v83, v83, 0x3e38aa3b, v101
	v_fmamk_f32 v84, v84, 0x3e38aa3b, v101
	v_fmamk_f32 v85, v85, 0x3e38aa3b, v101
	v_fmamk_f32 v86, v86, 0x3e38aa3b, v101
	v_fmamk_f32 v87, v87, 0x3e38aa3b, v101
	v_fmamk_f32 v88, v88, 0x3e38aa3b, v101
	v_fmamk_f32 v89, v89, 0x3e38aa3b, v101
	v_fmamk_f32 v90, v90, 0x3e38aa3b, v101
	v_fmamk_f32 v91, v91, 0x3e38aa3b, v101
	v_fmamk_f32 v92, v92, 0x3e38aa3b, v101
	v_fmamk_f32 v93, v93, 0x3e38aa3b, v101
	v_fmamk_f32 v94, v94, 0x3e38aa3b, v101
	v_fmamk_f32 v95, v95, 0x3e38aa3b, v101
	v_fmamk_f32 v96, v96, 0x3e38aa3b, v101
	v_fmamk_f32 v97, v97, 0x3e38aa3b, v101
	v_cmp_gt_f32_e32 vcc, 1.0, v100
	s_barrier
	s_cbranch_vccz .LBB0_428
	s_and_saveexec_b64 s[44:45], s[0:1]
	ds_write_b32 v171, v100 offset:128
	s_or_b64 exec, exec, s[44:45]
	s_waitcnt lgkmcnt(0)
	ds_read_b128 v[102:105], v207 offset:224
	ds_read_b128 v[106:109], v207 offset:192
	ds_read_b128 v[110:113], v207 offset:160
	ds_read_b128 v[116:119], v207 offset:128
	s_waitcnt lgkmcnt(3)
	v_pk_mul_f32 v[16:17], v[16:17], v[104:105]
	s_waitcnt lgkmcnt(2)
	v_pk_mul_f32 v[12:13], v[12:13], v[108:109]
	s_waitcnt lgkmcnt(1)
	v_pk_mul_f32 v[8:9], v[8:9], v[112:113]
	s_waitcnt lgkmcnt(0)
	v_pk_mul_f32 v[4:5], v[4:5], v[118:119]
	v_pk_mul_f32 v[14:15], v[14:15], v[102:103]
	v_pk_mul_f32 v[10:11], v[10:11], v[106:107]
	v_pk_mul_f32 v[6:7], v[6:7], v[110:111]
	v_pk_mul_f32 v[2:3], v[2:3], v[116:117]
	v_pk_mul_f32 v[64:65], v[64:65], v[104:105]
	v_pk_mul_f32 v[60:61], v[60:61], v[108:109]
	v_pk_mul_f32 v[56:57], v[56:57], v[112:113]
	v_pk_mul_f32 v[52:53], v[52:53], v[118:119]
	v_pk_mul_f32 v[62:63], v[62:63], v[102:103]
	v_pk_mul_f32 v[58:59], v[58:59], v[106:107]
	v_pk_mul_f32 v[54:55], v[54:55], v[110:111]
	v_pk_mul_f32 v[50:51], v[50:51], v[116:117]
	v_pk_mul_f32 v[48:49], v[48:49], v[104:105]
	v_pk_mul_f32 v[44:45], v[44:45], v[108:109]
	v_pk_mul_f32 v[40:41], v[40:41], v[112:113]
	v_pk_mul_f32 v[36:37], v[36:37], v[118:119]
	v_pk_mul_f32 v[46:47], v[46:47], v[102:103]
	v_pk_mul_f32 v[42:43], v[42:43], v[106:107]
	v_pk_mul_f32 v[38:39], v[38:39], v[110:111]
	v_pk_mul_f32 v[34:35], v[34:35], v[116:117]
	v_pk_mul_f32 v[32:33], v[32:33], v[104:105]
	v_pk_mul_f32 v[28:29], v[28:29], v[108:109]
	v_pk_mul_f32 v[24:25], v[24:25], v[112:113]
	v_pk_mul_f32 v[20:21], v[20:21], v[118:119]
	v_pk_mul_f32 v[30:31], v[30:31], v[102:103]
	v_pk_mul_f32 v[26:27], v[26:27], v[106:107]
	v_pk_mul_f32 v[22:23], v[22:23], v[110:111]
	v_pk_mul_f32 v[18:19], v[18:19], v[116:117]
; #define LAS __attribute__((address_space(3)))
; __device__ __forceinline__ void finishSM(f32x16& p0, f32x16& p1, float alpha, float& l_reg, bf16x8& pa0, bf16x8& pa1, bf16x8& pa2, bf16x8& pa3) {
; #pragma unroll
;     for (int r = 0; r < 16; ++r) p1[r] = __builtin_amdgcn_exp2f(p1[r]);
;     float ps = 0;
; #pragma unroll
;     for (int r = 0; r < 16; ++r) ps += p0[r];
; #pragma unroll
;     for (int r = 0; r < 16; ++r) ps += p1[r];
;     { auto rr = __builtin_amdgcn_permlane32_swap(__float_as_uint(ps), __float_as_uint(ps), false, false);
;       ps = __uint_as_float(rr[0]) + __uint_as_float(rr[1]); }
;     l_reg = l_reg * alpha + ps;
;     ...
;     PK4(p0, 0, pa0); PK4(p0, 8, pa1); PK4(p1, 0, pa2); PK4(p1, 8, pa3);
;     ...
; }
; template <int MODE>
; __device__ __forceinline__ void qkt(f32x16& p0, f32x16& p1, const LAS unsigned char* Ks, const bf16x8* qr, const LAS unsigned char* Qs, int r32, int hi, int cbase) {
;     p0 = f32x16{}; p1 = f32x16{};
; #pragma unroll
;     for (int d0 = 0; d0 < Cfg<MODE>::ND; ++d0) { const int cb = cbase + (d0 * 16 + hi * 8) * 2;
;         const bf16x8 b0 = *(const LAS bf16x8*)(Ks + KSWZ(r32, cb));
;         const bf16x8 b1 = *(const LAS bf16x8*)(Ks + KSWZ(32 + r32, cb));
;         bf16x8 q; if constexpr (MODE == 0) q = *(const LAS bf16x8*)(Qs + KSWZ(r32, cb)); else q = qr[d0];
;         p0 = __builtin_amdgcn_mfma_f32_32x32x16_bf16(b0, q, p0, 0, 0, 0);
;         p1 = __builtin_amdgcn_mfma_f32_32x32x16_bf16(b1, q, p1, 0, 0, 0); }
; }
; __device__ __forceinline__ int v_st(int k, int c) { const int kk = (k & ~0xC) | ((k & 4) << 1) | ((k & 8) >> 1); return ((kk >> 3) * 4 + (c >> 5)) * 512 + ((kk & 7) * 32 + (c & 31)) * 2; }
; __device__ __forceinline__ int v_rd_base(int lane) { return ((lane & 3) << 3) | (((lane >> 2) & 3) << 6) | (((lane >> 4) & 1) << 5) | (((lane >> 5) & 1) << 8); }
; template <int OFF> __device__ __forceinline__ s16x4 tr_read(int vb) {
;     s16x4 r; asm volatile("ds_read_b64_tr_b16 %0, %1 offset:%2" : "=&v"(r) : "v"(vb), "i"(OFF) : "memory"); return r;
; }
; template <int D0> __device__ __forceinline__ void pv_one(f32x16& od, int vb, bf16x8 pa0, bf16x8 pa1, bf16x8 pa2, bf16x8 pa3) {
;     const s16x4 l0 = tr_read<v_rd_off(D0, 0, 0)>(vb), h0 = tr_read<v_rd_off(D0, 0, 1)>(vb), l1 = tr_read<v_rd_off(D0, 1, 0)>(vb), h1 = tr_read<v_rd_off(D0, 1, 1)>(vb);
.LBB0_428:
	v_exp_f32_e32 v102, v82
	v_exp_f32_e32 v103, v83
	v_exp_f32_e32 v82, v84
	v_fmamk_f32 v66, v66, 0x3e38aa3b, v101
	v_exp_f32_e32 v84, v85
	v_fmamk_f32 v113, v77, 0x3e38aa3b, v101
	v_exp_f32_e32 v77, v86
	v_exp_f32_e32 v85, v66
	v_add_f32_e32 v66, 0, v102
	v_exp_f32_e32 v83, v87
	v_add_f32_e32 v66, v103, v66
	v_fmamk_f32 v112, v76, 0x3e38aa3b, v101
	v_exp_f32_e32 v76, v88
	v_add_f32_e32 v66, v82, v66
	v_cndmask_b32_e64 v199, v115, v114, s[4:5]
	v_fmamk_f32 v114, v78, 0x3e38aa3b, v101
	v_exp_f32_e32 v78, v89
	v_add_f32_e32 v66, v84, v66
	v_fmamk_f32 v109, v73, 0x3e38aa3b, v101
	v_exp_f32_e32 v73, v90
	v_add_f32_e32 v66, v77, v66
	v_fmamk_f32 v111, v75, 0x3e38aa3b, v101
	v_exp_f32_e32 v75, v91
	v_add_f32_e32 v66, v83, v66
	v_fmamk_f32 v107, v71, 0x3e38aa3b, v101
	v_exp_f32_e32 v71, v92
	v_add_f32_e32 v66, v76, v66
	v_fmamk_f32 v110, v74, 0x3e38aa3b, v101
	v_exp_f32_e32 v74, v93
	v_add_f32_e32 v66, v78, v66
	v_fmamk_f32 v105, v69, 0x3e38aa3b, v101
	v_exp_f32_e32 v69, v94
	v_add_f32_e32 v66, v73, v66
	v_fmamk_f32 v108, v72, 0x3e38aa3b, v101
	v_exp_f32_e32 v72, v95
	v_add_f32_e32 v66, v75, v66
	v_fmamk_f32 v104, v68, 0x3e38aa3b, v101
	v_exp_f32_e32 v68, v96
	v_add_f32_e32 v66, v71, v66
	v_fmamk_f32 v106, v70, 0x3e38aa3b, v101
	v_exp_f32_e32 v70, v97
	v_add_f32_e32 v66, v74, v66
	v_fmamk_f32 v67, v67, 0x3e38aa3b, v101
	v_add_f32_e32 v66, v69, v66
	v_exp_f32_e32 v86, v67
	v_add_f32_e32 v66, v72, v66
	v_exp_f32_e32 v87, v104
	v_add_f32_e32 v66, v68, v66
	v_exp_f32_e32 v88, v105
	v_add_f32_e32 v66, v70, v66
	v_exp_f32_e32 v89, v106
	v_add_f32_e32 v66, v85, v66
	v_exp_f32_e32 v90, v107
	v_add_f32_e32 v66, v86, v66
	v_exp_f32_e32 v91, v108
	v_add_f32_e32 v66, v87, v66
	v_exp_f32_e32 v92, v109
	v_add_f32_e32 v66, v88, v66
	v_exp_f32_e32 v93, v110
	v_add_f32_e32 v66, v89, v66
	v_exp_f32_e32 v94, v111
	v_add_f32_e32 v66, v90, v66
	v_exp_f32_e32 v95, v112
	v_add_f32_e32 v66, v91, v66
	v_exp_f32_e32 v96, v113
	v_add_f32_e32 v66, v92, v66
	v_fmamk_f32 v79, v79, 0x3e38aa3b, v101
	v_exp_f32_e32 v97, v114
	v_add_f32_e32 v66, v93, v66
	v_fmamk_f32 v80, v80, 0x3e38aa3b, v101
	v_exp_f32_e32 v104, v79
	v_add_f32_e32 v66, v94, v66
	v_fmac_f32_e32 v101, 0x3e38aa3b, v81
	v_exp_f32_e32 v105, v80
	v_add_f32_e32 v66, v95, v66
	v_exp_f32_e32 v101, v101
	v_add_f32_e32 v66, v96, v66
	v_add_f32_e32 v66, v97, v66
	v_add_f32_e32 v66, v104, v66
	v_add_f32_e32 v66, v105, v66
	v_add_f32_e32 v66, v101, v66
	v_mov_b32_e32 v67, v66
	s_mov_b32 s64, 0
	s_nop 0
	v_permlane32_swap_b32_e32 v66, v67
	v_cvt_pk_bf16_f32 v80, v102, v103
	v_cvt_pk_bf16_f32 v81, v82, v84
	v_cvt_pk_bf16_f32 v82, v77, v83
	v_cvt_pk_bf16_f32 v83, v76, v78
	v_cvt_pk_bf16_f32 v76, v73, v75
	v_cvt_pk_bf16_f32 v77, v71, v74
	v_cvt_pk_bf16_f32 v78, v69, v72
	v_cvt_pk_bf16_f32 v79, v68, v70
	v_cvt_pk_bf16_f32 v68, v85, v86
	v_cvt_pk_bf16_f32 v69, v87, v88
	v_cvt_pk_bf16_f32 v70, v89, v90
	v_cvt_pk_bf16_f32 v71, v91, v92
	v_cvt_pk_bf16_f32 v72, v93, v94
	v_cvt_pk_bf16_f32 v73, v95, v96
	v_cvt_pk_bf16_f32 v74, v97, v104
	v_cvt_pk_bf16_f32 v75, v105, v101
	s_nop 0
	v_permlane32_swap_b32_e32 v80, v82
	v_permlane32_swap_b32_e32 v81, v83
	v_permlane32_swap_b32_e32 v76, v78
	v_permlane32_swap_b32_e32 v77, v79
	v_permlane32_swap_b32_e32 v68, v70
	v_permlane32_swap_b32_e32 v69, v71
	v_permlane32_swap_b32_e32 v72, v74
	v_permlane32_swap_b32_e32 v73, v75
	ds_read_b64_tr_b16 v[84:85], v173 offset:0
	ds_read_b64_tr_b16 v[86:87], v173 offset:0x800
	ds_read_b64_tr_b16 v[88:89], v173 offset:0x1000
	ds_read_b64_tr_b16 v[90:91], v173 offset:0x1800
	ds_read_b64_tr_b16 v[92:93], v173 offset:0x2000
	ds_read_b64_tr_b16 v[94:95], v173 offset:0x2800
	ds_read_b64_tr_b16 v[102:103], v173 offset:0x3000
	ds_read_b64_tr_b16 v[104:105], v173 offset:0x3800
	s_waitcnt lgkmcnt(0)
	s_nop 0
	v_mfma_f32_32x32x16_bf16 v[2:17], v[80:83], v[84:87], v[2:17]
	ds_read_b64_tr_b16 v[84:85], v173 offset:0x200
	ds_read_b64_tr_b16 v[86:87], v173 offset:0xa00
	v_mfma_f32_32x32x16_bf16 v[2:17], v[76:79], v[88:91], v[2:17]
	ds_read_b64_tr_b16 v[88:89], v173 offset:0x1200
	ds_read_b64_tr_b16 v[90:91], v173 offset:0x1a00
	v_mfma_f32_32x32x16_bf16 v[2:17], v[68:71], v[92:95], v[2:17]
	ds_read_b64_tr_b16 v[92:93], v173 offset:0x2200
	ds_read_b64_tr_b16 v[94:95], v173 offset:0x2a00
	ds_read_b64_tr_b16 v[106:107], v173 offset:0x3200
	ds_read_b64_tr_b16 v[108:109], v173 offset:0x3a00
	v_mfma_f32_32x32x16_bf16 v[2:17], v[72:75], v[102:105], v[2:17]
	s_waitcnt lgkmcnt(0)
	v_mfma_f32_32x32x16_bf16 v[50:65], v[80:83], v[84:87], v[50:65]
	ds_read_b64_tr_b16 v[84:85], v173 offset:0x400
	ds_read_b64_tr_b16 v[86:87], v173 offset:0xc00
	v_mfma_f32_32x32x16_bf16 v[50:65], v[76:79], v[88:91], v[50:65]
	ds_read_b64_tr_b16 v[88:89], v173 offset:0x1400
	ds_read_b64_tr_b16 v[90:91], v173 offset:0x1c00
	v_mfma_f32_32x32x16_bf16 v[50:65], v[68:71], v[92:95], v[50:65]
	ds_read_b64_tr_b16 v[92:93], v173 offset:0x2400
	ds_read_b64_tr_b16 v[94:95], v173 offset:0x2c00
	ds_read_b64_tr_b16 v[102:103], v173 offset:0x3400
	ds_read_b64_tr_b16 v[104:105], v173 offset:0x3c00
	v_mfma_f32_32x32x16_bf16 v[50:65], v[72:75], v[106:109], v[50:65]
	s_waitcnt lgkmcnt(0)
	v_mfma_f32_32x32x16_bf16 v[34:49], v[80:83], v[84:87], v[34:49]
	ds_read_b64_tr_b16 v[84:85], v173 offset:0x600
	ds_read_b64_tr_b16 v[86:87], v173 offset:0xe00
	v_mfma_f32_32x32x16_bf16 v[34:49], v[76:79], v[88:91], v[34:49]
	ds_read_b64_tr_b16 v[88:89], v173 offset:0x1600
	ds_read_b64_tr_b16 v[90:91], v173 offset:0x1e00
	v_mfma_f32_32x32x16_bf16 v[34:49], v[68:71], v[92:95], v[34:49]
	ds_read_b64_tr_b16 v[92:93], v173 offset:0x2600
	ds_read_b64_tr_b16 v[94:95], v173 offset:0x2e00
	ds_read_b64_tr_b16 v[106:107], v173 offset:0x3600
	ds_read_b64_tr_b16 v[108:109], v173 offset:0x3e00
	v_mfma_f32_32x32x16_bf16 v[34:49], v[72:75], v[102:105], v[34:49]
	s_waitcnt lgkmcnt(0)
; #define LAS __attribute__((address_space(3)))
; __device__ __forceinline__ unsigned cvt_pk_bf16(float lo, float hi) { unsigned r; asm volatile("v_cvt_pk_bf16_f32 %0, %1, %2" : "=v"(r) : "v"(lo), "v"(hi)); return r; }
; __device__ __forceinline__ int crow(int r, int hi) { return (r & 3) + 8 * (r >> 2) + 4 * hi; }
; template <int MODE>
; __device__ __forceinline__ void attn_pass(const bf16_t* __restrict__ Qb, const bf16_t* __restrict__ Kh, const bf16_t* __restrict__ Vh, const int NT, const int kr0, const int g4, const int map,
;                                           LAS unsigned char* lds, f32x16 (&o)[4]) {
;     ...
;     if (hi == 0) li_l[r32] = l_reg; asm volatile("s_waitcnt lgkmcnt(0)" ::: "memory");
; #pragma unroll
;     for (int r = 0; r < 16; ++r) { const float rl = __builtin_amdgcn_rcpf(li_l[crow(r, hi)]);
; #pragma unroll
;         for (int d = 0; d < 4; ++d) o[d][r] *= rl; }
; __device__ __forceinline__ void p3_attention(Frame& F) {
;     ...
;         LAS u32x4* o1l = (LAS u32x4*)(F.lds + attn::OFF_Q) + tid;
;         attn::attn_pass<1>(Qb, Kh, Vh, RPB / 64, 0, 0, 0, F.lds, o);
; #pragma unroll
;         for (int k = 0; k < 8; ++k) { const int d = k >> 1, r0 = (k & 1) * 8; u32x4 w;
;             w.x = cvt_pk_bf16(o[d][r0], o[d][r0 + 1]); w.y = cvt_pk_bf16(o[d][r0 + 2], o[d][r0 + 3]); w.z = cvt_pk_bf16(o[d][r0 + 4], o[d][r0 + 5]); w.w = cvt_pk_bf16(o[d][r0 + 6], o[d][r0 + 7]);
;             o1l[k * 512] = w; }
;         attn::attn_pass<1>(Qb + 64, Kh, Vh, RPB / 64, 0, 0, 1, F.lds, o);
	v_mfma_f32_32x32x16_bf16 v[18:33], v[80:83], v[84:87], v[18:33]
	v_mfma_f32_32x32x16_bf16 v[18:33], v[76:79], v[88:91], v[18:33]
	v_mfma_f32_32x32x16_bf16 v[18:33], v[68:71], v[92:95], v[18:33]
	v_mfma_f32_32x32x16_bf16 v[18:33], v[72:75], v[106:109], v[18:33]
	s_and_saveexec_b64 s[4:5], s[0:1]
	v_add_f32_e32 v68, v98, v99
	v_fmac_f32_e32 v68, v167, v141
	v_add_f32_e32 v66, v66, v67
	v_fmac_f32_e32 v66, v68, v100
	ds_write_b32 v171, v66
	s_or_b64 exec, exec, s[4:5]
	s_waitcnt lgkmcnt(0)
	ds_read_b128 v[66:69], v207
	ds_read_b128 v[70:73], v207 offset:32
	v_lshl_add_u32 v74, v0, 4, 0
	v_add_u32_e32 v200, 0x11800, v74
	s_movk_i32 s4, 0x80
	s_waitcnt lgkmcnt(1)
	v_rcp_f32_e32 v66, v66
	v_rcp_f32_e32 v67, v67
	v_bitop3_b32 v197, v166, v219, s4 bitop3:0x36
	s_movk_i32 s4, 0xa0
	v_mul_f32_e32 v74, v2, v66
	v_mul_f32_e32 v50, v50, v66
	v_mul_f32_e32 v34, v34, v66
	v_mul_f32_e32 v18, v18, v66
	v_mul_f32_e32 v66, v3, v67
	v_rcp_f32_e32 v2, v68
	v_rcp_f32_e32 v3, v69
	v_mul_f32_e32 v51, v51, v67
	v_mul_f32_e32 v35, v35, v67
	v_mul_f32_e32 v19, v19, v67
	v_mul_f32_e32 v67, v4, v2
	v_mul_f32_e32 v52, v52, v2
	v_mul_f32_e32 v36, v36, v2
	v_mul_f32_e32 v20, v20, v2
	v_mul_f32_e32 v68, v5, v3
	s_waitcnt lgkmcnt(0)
	v_rcp_f32_e32 v2, v70
	v_mul_f32_e32 v53, v53, v3
	v_mul_f32_e32 v37, v37, v3
	v_mul_f32_e32 v21, v21, v3
	v_rcp_f32_e32 v3, v71
	v_mul_f32_e32 v69, v6, v2
	v_mul_f32_e32 v54, v54, v2
	v_mul_f32_e32 v38, v38, v2
	v_mul_f32_e32 v22, v22, v2
	v_mul_f32_e32 v70, v7, v3
	v_mul_f32_e32 v55, v55, v3
	v_mul_f32_e32 v39, v39, v3
	v_mul_f32_e32 v23, v23, v3
	ds_read_b128 v[2:5], v207 offset:64
	v_rcp_f32_e32 v6, v72
	v_rcp_f32_e32 v72, v73
	v_bitop3_b32 v198, v166, v219, s4 bitop3:0x36
	s_movk_i32 s4, 0xc0
	v_mul_f32_e32 v71, v8, v6
	v_mul_f32_e32 v56, v56, v6
	v_mul_f32_e32 v40, v40, v6
	v_mul_f32_e32 v24, v24, v6
	v_mul_f32_e32 v73, v9, v72
	ds_read_b128 v[6:9], v207 offset:96
	s_waitcnt lgkmcnt(1)
	v_rcp_f32_e32 v2, v2
	v_rcp_f32_e32 v3, v3
	s_waitcnt lgkmcnt(0)
	s_barrier
	v_mul_f32_e32 v10, v10, v2
	v_mul_f32_e32 v58, v58, v2
	v_mul_f32_e32 v42, v42, v2
	v_mul_f32_e32 v26, v26, v2
	v_mul_f32_e32 v11, v11, v3
	v_rcp_f32_e32 v2, v4
	v_mul_f32_e32 v59, v59, v3
	v_mul_f32_e32 v43, v43, v3
	v_mul_f32_e32 v27, v27, v3
	v_rcp_f32_e32 v3, v5
	v_mul_f32_e32 v12, v12, v2
	v_mul_f32_e32 v60, v60, v2
	v_mul_f32_e32 v44, v44, v2
	v_mul_f32_e32 v28, v28, v2
	v_mul_f32_e32 v13, v13, v3
	v_rcp_f32_e32 v2, v6
	v_mul_f32_e32 v6, v61, v3
	v_mul_f32_e32 v45, v45, v3
	v_mul_f32_e32 v29, v29, v3
	v_rcp_f32_e32 v3, v7
	v_mul_f32_e32 v14, v14, v2
	v_mul_f32_e32 v7, v62, v2
	v_mul_f32_e32 v46, v46, v2
	v_mul_f32_e32 v30, v30, v2
	v_mul_f32_e32 v15, v15, v3
	v_rcp_f32_e32 v2, v8
	v_mul_f32_e32 v8, v63, v3
	v_mul_f32_e32 v47, v47, v3
	v_mul_f32_e32 v31, v31, v3
	v_rcp_f32_e32 v3, v9
	v_mul_f32_e32 v16, v16, v2
	v_mul_f32_e32 v9, v64, v2
	v_mul_f32_e32 v48, v48, v2
	v_mul_f32_e32 v32, v32, v2
	v_mul_f32_e32 v17, v17, v3
	v_mul_f32_e32 v61, v65, v3
	v_mul_f32_e32 v49, v49, v3
	v_mul_f32_e32 v33, v33, v3
	v_cvt_pk_bf16_f32 v2, v74, v66
	v_cvt_pk_bf16_f32 v3, v67, v68
	v_cvt_pk_bf16_f32 v4, v69, v70
	v_cvt_pk_bf16_f32 v5, v71, v73
	ds_write_b128 v200, v[2:5]
	v_cvt_pk_bf16_f32 v2, v10, v11
	v_cvt_pk_bf16_f32 v3, v12, v13
	v_cvt_pk_bf16_f32 v4, v14, v15
	v_cvt_pk_bf16_f32 v5, v16, v17
	v_mul_f32_e32 v57, v57, v72
	ds_write_b128 v200, v[2:5] offset:8192
	v_cvt_pk_bf16_f32 v2, v50, v51
	v_cvt_pk_bf16_f32 v3, v52, v53
	v_cvt_pk_bf16_f32 v4, v54, v55
	v_cvt_pk_bf16_f32 v5, v56, v57
	ds_write_b128 v200, v[2:5] offset:16384
	v_cvt_pk_bf16_f32 v2, v58, v59
	v_cvt_pk_bf16_f32 v3, v60, v6
	v_cvt_pk_bf16_f32 v4, v7, v8
	v_cvt_pk_bf16_f32 v5, v9, v61
	v_mul_f32_e32 v41, v41, v72
	ds_write_b128 v200, v[2:5] offset:24576
	v_cvt_pk_bf16_f32 v2, v34, v35
	v_cvt_pk_bf16_f32 v3, v36, v37
	v_cvt_pk_bf16_f32 v4, v38, v39
	v_cvt_pk_bf16_f32 v5, v40, v41
	ds_write_b128 v200, v[2:5] offset:32768
	v_cvt_pk_bf16_f32 v2, v42, v43
	v_cvt_pk_bf16_f32 v3, v44, v45
	v_cvt_pk_bf16_f32 v4, v46, v47
	v_cvt_pk_bf16_f32 v5, v48, v49
	v_mul_f32_e32 v25, v25, v72
	ds_write_b128 v200, v[2:5] offset:40960
	v_cvt_pk_bf16_f32 v2, v18, v19
	v_cvt_pk_bf16_f32 v3, v20, v21
	v_cvt_pk_bf16_f32 v4, v22, v23
	v_cvt_pk_bf16_f32 v5, v24, v25
	ds_write_b128 v200, v[2:5] offset:49152
	v_cvt_pk_bf16_f32 v2, v26, v27
	v_cvt_pk_bf16_f32 v3, v28, v29
	v_cvt_pk_bf16_f32 v4, v30, v31
	v_cvt_pk_bf16_f32 v5, v32, v33
	global_load_dwordx4 v[6:9], v[182:183], off
	global_load_dwordx4 v[10:13], v[184:185], off
	global_load_dwordx4 v[14:17], v[168:169], off offset:128
	global_load_dwordx4 v[110:113], v[178:179], off offset:128
	global_load_dwordx4 v[106:109], v[178:179], off offset:160
	global_load_dwordx4 v[102:105], v[178:179], off offset:192
	global_load_dwordx4 v[98:101], v[178:179], off offset:224
	ds_write_b128 v200, v[2:5] offset:57344
	v_mov_b32_e32 v2, 0x80
	v_lshl_or_b32 v58, v217, 1, v2
	v_bitop3_b32 v2, v58, v220, v221 bitop3:0xde
	v_add_u32_e32 v179, 0, v2
	v_add_u32_e32 v182, v218, v197
	s_waitcnt vmcnt(0)
	s_waitcnt vmcnt(6)
	ds_write_b128 v215, v[6:9]
	s_waitcnt vmcnt(5)
	ds_write_b128 v216, v[10:13]
	s_waitcnt vmcnt(4)
	ds_write_b128 v179, v[14:17] offset:32768
	s_waitcnt lgkmcnt(0)
	s_barrier
; template <int MODE>
; __device__ __forceinline__ void partialSM(f32x16& p0, f32x16& p1, float& m_reg, float& mn, float& alpha) {
;     constexpr float SCALE = Cfg<MODE>::SCALE, C = SCALE * 1.4426950408889634f;
;     float pmax = p0[0];
; #pragma unroll
;     for (int r = 1; r < 16; ++r) pmax = fmaxf(pmax, p0[r]);
; #pragma unroll
;     for (int r = 0; r < 16; ++r) pmax = fmaxf(pmax, p1[r]);
;     { auto rr = __builtin_amdgcn_permlane32_swap(__float_as_uint(pmax), __float_as_uint(pmax), false, false);
;       pmax = fmaxf(__uint_as_float(rr[0]), __uint_as_float(rr[1])); }
;     if (__builtin_expect(__all(pmax - m_reg <= THR / SCALE), 1)) { mn = m_reg; alpha = 1.f; }
; template <int MODE>
; __device__ __forceinline__ void attn_pass(const bf16_t* __restrict__ Qb, const bf16_t* __restrict__ Kh, const bf16_t* __restrict__ Vh, const int NT, const int kr0, const int g4, const int map,
;                                           LAS unsigned char* lds, f32x16 (&o)[4]) {
;     ...
;     float m_reg = -1e30f, l_reg = 0;
; #pragma unroll
;     for (int d = 0; d < 4; ++d) o[d] = f32x16{};
;     bf16x8 qr[ND];
;     const bf16_t* Qw = Qb + (long)(wid * QBLK + r32) * LDK + hi * 8;
;     LAS unsigned char* Qs = lds + OFF_Q + wid * (QBLK * 256);
; #pragma unroll
;     for (int d0 = 0; d0 < ND; ++d0) { qr[d0] = *(const bf16x8*)(Qw + d0 * 16); if constexpr (MODE == 0) *(LAS bf16x8*)(Qs + KSWZ(r32, (d0 * 16 + hi * 8) * 2)) = qr[d0]; }
;     const int cbase = MODE == 1 ? map * 128 : 0;
;     const int sr = tid >> 4, sc = (tid & 15) * 8, vst0 = v_st(sr, sc), vst1 = v_st(32 + sr, sc);
;     const int vb0 = (int)(uintptr_t)V_lds + v_rd_base(lane);
;     const int qR = g4 * 4 + (wid >> 1), qc = 32 * (wid & 1) + r32, cs = qc < 8 ? 0 : (qc > 56 ? 48 : qc - 8);
;     const int r0w = qR < 4 ? 0 : (qR > 60 ? 56 : qR - 4);
;     struct { bf16x8 vs0, vs1, ks0, ks1; } sr_[2];
;     ...
;     const int kr1 = tid >> 3, kc1 = map * 64 + (tid & 7) * 8;
;     ...
;     f32x16 pA0, pA1, pB0, pB1; float mnA, mnB, alA, alB; bf16x8 pa0, pa1, pa2, pa3;
;     constexpr int SE = 0, SO = 1;
;     SLOAD(SE, 0); asm volatile("s_waitcnt vmcnt(0)" ::: "memory"); SWRITE(0, SE); __syncthreads();
;     qkt<MODE>(pA0, pA1, K_lds, qr, Qs, r32, hi, cbase); MASK(pA0, pA1, 0); partialSM<MODE>(pA0, pA1, m_reg, mnA, alA);
;     SLOAD(SO, 1); if (2 < NT) SLOAD(SE, 2);
;     SWAIT(); SWRITE(1, SO); __syncthreads();
	ds_read_b128 v[2:5], v182 offset:32768
	ds_read_b128 v[6:9], v182 offset:40960
	s_waitcnt vmcnt(3) lgkmcnt(1)
	v_mfma_f32_32x32x16_bf16 v[34:49], v[2:5], v[110:113], 0
	v_add_u32_e32 v184, v218, v198
	v_bitop3_b32 v196, v166, v219, s4 bitop3:0x36
	v_add_u32_e32 v183, v218, v196
	s_movk_i32 s4, 0xe0
	v_bitop3_b32 v194, v166, v219, s4 bitop3:0x36
	v_add_u32_e32 v185, v218, v194
	s_mov_b32 s4, 0x40000
	s_waitcnt lgkmcnt(0)
	v_mfma_f32_32x32x16_bf16 v[18:33], v[6:9], v[110:113], 0
	ds_read_b128 v[2:5], v184 offset:32768
	ds_read_b128 v[6:9], v184 offset:40960
	ds_read_b128 v[50:53], v185 offset:40960
	v_mov_b32_e32 v59, 0
	v_lshl_add_u64 v[58:59], v[180:181], 0, v[58:59]
	s_mov_b32 s7, 0x42800000
	s_mov_b32 s65, s64
	s_mov_b32 s66, s64
	s_waitcnt vmcnt(2) lgkmcnt(2)
	v_mfma_f32_32x32x16_bf16 v[34:49], v[2:5], v[106:109], v[34:49]
	ds_read_b128 v[2:5], v183 offset:32768
	s_mov_b32 s67, s64
	s_mov_b32 s68, s64
	s_mov_b32 s69, s64
	s_mov_b32 s70, s64
	s_mov_b32 s71, s64
	s_mov_b32 s72, s64
	s_waitcnt lgkmcnt(2)
	v_mfma_f32_32x32x16_bf16 v[18:33], v[6:9], v[106:109], v[18:33]
	ds_read_b128 v[6:9], v183 offset:40960
	s_mov_b32 s73, s64
	s_mov_b32 s74, s64
	s_mov_b32 s75, s64
	s_mov_b32 s76, s64
	s_mov_b32 s77, s64
	s_mov_b32 s78, s64
	s_waitcnt vmcnt(1) lgkmcnt(1)
	v_mfma_f32_32x32x16_bf16 v[34:49], v[2:5], v[102:105], v[34:49]
	ds_read_b128 v[2:5], v185 offset:32768
	s_mov_b32 s79, s64
	s_mov_b32 s44, 0x3e38aa3b
	v_mov_b32_e32 v178, 0
	s_mov_b32 s6, 1
	s_mov_b32 s43, 0x39560000
	s_mov_b32 s57, 0x38460000
	s_waitcnt lgkmcnt(1)
	v_mfma_f32_32x32x16_bf16 v[18:33], v[6:9], v[102:105], v[18:33]
	s_mov_b64 s[46:47], 0x40000
	s_waitcnt vmcnt(0) lgkmcnt(0)
	v_mfma_f32_32x32x16_bf16 v[34:49], v[2:5], v[98:101], v[34:49]
	v_mov_b64_e32 v[2:3], s[64:65]
	v_mov_b64_e32 v[16:17], s[78:79]
	v_mov_b64_e32 v[4:5], s[66:67]
	v_mov_b64_e32 v[6:7], s[68:69]
	v_mov_b64_e32 v[8:9], s[70:71]
	v_mov_b64_e32 v[10:11], s[72:73]
	v_mov_b64_e32 v[12:13], s[74:75]
	v_mfma_f32_32x32x16_bf16 v[18:33], v[50:53], v[98:101], v[18:33]
	s_nop 3
	v_max_f32_e32 v50, v35, v35
	v_max_f32_e32 v51, v34, v34
	v_max_f32_e32 v50, v51, v50
	v_max3_f32 v50, v50, v36, v37
	v_max3_f32 v50, v50, v38, v39
	v_max3_f32 v50, v50, v40, v41
	v_max3_f32 v50, v50, v42, v43
	v_max3_f32 v50, v50, v44, v45
	v_max3_f32 v50, v50, v46, v47
	v_max3_f32 v50, v50, v48, v49
	v_max3_f32 v62, v50, v18, v19
	v_max3_f32 v62, v62, v20, v21
	v_max3_f32 v62, v62, v22, v23
	v_max3_f32 v62, v62, v24, v25
	v_max3_f32 v64, v62, v26, v27
	v_add_co_u32_e32 v62, vcc, s4, v168
	global_load_dwordx4 v[50:53], v[190:191], off
	global_load_dwordx4 v[54:57], v[192:193], off
	v_addc_co_u32_e32 v63, vcc, 0, v169, vcc
	global_load_dwordx4 v[58:61], v[58:59], off
	s_nop 0
	global_load_dwordx4 v[122:125], v[62:63], off offset:128
	global_load_dwordx4 v[118:121], v[186:187], off
	global_load_dwordx4 v[114:117], v[188:189], off
	v_max3_f32 v62, v64, v28, v29
	v_max3_f32 v62, v62, v30, v31
	v_max3_f32 v62, v62, v32, v33
	v_mov_b32_e32 v63, v62
	s_nop 1
	v_permlane32_swap_b32_e32 v62, v63
	v_max_f32_e32 v63, v63, v63
	v_max_f32_e32 v62, v62, v62
	v_max_f32_e32 v62, v62, v63
	v_add_f32_e32 v63, 0x7149f2ca, v62
	v_max_f32_e32 v62, 0xf149f2ca, v62
	v_cmp_ge_f32_e32 vcc, s7, v63
	v_sub_f32_e32 v63, 0xf149f2ca, v62
	v_mul_f32_e32 v63, 0x3e38aa3b, v63
	s_cmp_eq_u64 vcc, exec
	v_exp_f32_e32 v63, v63
	v_mov_b32_e32 v64, 0xf149f2ca
	s_cselect_b64 vcc, -1, 0
	v_cndmask_b32_e32 v140, v62, v64, vcc
	v_mul_f32_e32 v62, 0xbe38aa3b, v140
	v_cndmask_b32_e64 v180, v63, 1.0, vcc
	v_mov_b32_e32 v63, v62
	v_fmamk_f32 v34, v34, 0x3e38aa3b, v62
	v_fmamk_f32 v35, v35, 0x3e38aa3b, v62
	v_fmamk_f32 v36, v36, 0x3e38aa3b, v62
	v_fmamk_f32 v37, v37, 0x3e38aa3b, v62
	v_fmamk_f32 v38, v38, 0x3e38aa3b, v62
	v_fmamk_f32 v39, v39, 0x3e38aa3b, v62
	v_fmamk_f32 v40, v40, 0x3e38aa3b, v62
	v_fmamk_f32 v41, v41, 0x3e38aa3b, v62
	v_fmamk_f32 v42, v42, 0x3e38aa3b, v62
	v_fmamk_f32 v43, v43, 0x3e38aa3b, v62
	v_fmamk_f32 v44, v44, 0x3e38aa3b, v62
	v_fmamk_f32 v45, v45, 0x3e38aa3b, v62
	v_fmamk_f32 v46, v46, 0x3e38aa3b, v62
	v_fmamk_f32 v47, v47, 0x3e38aa3b, v62
	v_fmamk_f32 v48, v48, 0x3e38aa3b, v62
	v_fmac_f32_e32 v63, 0x3e38aa3b, v49
	v_exp_f32_e32 v167, v34
	v_exp_f32_e32 v169, v35
	v_exp_f32_e32 v153, v36
	v_exp_f32_e32 v168, v37
	v_exp_f32_e32 v151, v38
	v_exp_f32_e32 v166, v39
	v_exp_f32_e32 v150, v40
	v_exp_f32_e32 v152, v41
	v_exp_f32_e32 v147, v42
	v_exp_f32_e32 v149, v43
	v_exp_f32_e32 v145, v44
	v_exp_f32_e32 v148, v45
	v_exp_f32_e32 v143, v46
	v_exp_f32_e32 v146, v47
	v_exp_f32_e32 v142, v48
	v_exp_f32_e32 v144, v63
	s_waitcnt vmcnt(3)
	v_mov_b64_e32 v[14:15], s[76:77]
	v_pk_fma_f32 v[134:135], v[32:33], s[44:45], v[62:63] op_sel_hi:[1,0,0]
	v_pk_fma_f32 v[136:137], v[30:31], s[44:45], v[62:63] op_sel_hi:[1,0,0]
	v_pk_fma_f32 v[138:139], v[28:29], s[44:45], v[62:63] op_sel_hi:[1,0,0]
	v_pk_fma_f32 v[126:127], v[26:27], s[44:45], v[62:63] op_sel_hi:[1,0,0]
	v_pk_fma_f32 v[128:129], v[24:25], s[44:45], v[62:63] op_sel_hi:[1,0,0]
	v_pk_fma_f32 v[130:131], v[22:23], s[44:45], v[62:63] op_sel_hi:[1,0,0]
	v_pk_fma_f32 v[66:67], v[20:21], s[44:45], v[62:63] op_sel_hi:[1,0,0]
	v_pk_fma_f32 v[132:133], v[18:19], s[44:45], v[62:63] op_sel_hi:[1,0,0]
	s_waitcnt vmcnt(5)
	ds_write_b128 v215, v[50:53] offset:16384
	s_waitcnt vmcnt(4)
	ds_write_b128 v216, v[54:57] offset:16384
	s_waitcnt vmcnt(3)
	ds_write_b128 v179, v[58:61] offset:49152
	v_mov_b64_e32 v[64:65], v[16:17]
	v_mov_b64_e32 v[48:49], v[16:17]
	v_mov_b64_e32 v[32:33], v[16:17]
	s_mov_b32 s45, 0x39570000
	v_mov_b64_e32 v[62:63], v[14:15]
	v_mov_b64_e32 v[60:61], v[12:13]
	v_mov_b64_e32 v[58:59], v[10:11]
	v_mov_b64_e32 v[56:57], v[8:9]
	v_mov_b64_e32 v[54:55], v[6:7]
	v_mov_b64_e32 v[52:53], v[4:5]
	v_mov_b64_e32 v[50:51], v[2:3]
	v_mov_b64_e32 v[46:47], v[14:15]
	v_mov_b64_e32 v[44:45], v[12:13]
	v_mov_b64_e32 v[42:43], v[10:11]
	v_mov_b64_e32 v[40:41], v[8:9]
	v_mov_b64_e32 v[38:39], v[6:7]
	v_mov_b64_e32 v[36:37], v[4:5]
	v_mov_b64_e32 v[34:35], v[2:3]
	v_mov_b64_e32 v[30:31], v[14:15]
	v_mov_b64_e32 v[28:29], v[12:13]
	v_mov_b64_e32 v[26:27], v[10:11]
	v_mov_b64_e32 v[24:25], v[8:9]
	v_mov_b64_e32 v[22:23], v[6:7]
	v_mov_b64_e32 v[20:21], v[4:5]
	v_mov_b64_e32 v[18:19], v[2:3]
	s_waitcnt lgkmcnt(0)
	s_barrier
; #define LAS __attribute__((address_space(3)))
; __device__ __forceinline__ void finishSM(f32x16& p0, f32x16& p1, float alpha, float& l_reg, bf16x8& pa0, bf16x8& pa1, bf16x8& pa2, bf16x8& pa3) {
; #pragma unroll
;     for (int r = 0; r < 16; ++r) p1[r] = __builtin_amdgcn_exp2f(p1[r]);
;     float ps = 0;
; #pragma unroll
;     for (int r = 0; r < 16; ++r) ps += p0[r];
; #pragma unroll
;     for (int r = 0; r < 16; ++r) ps += p1[r];
;     { auto rr = __builtin_amdgcn_permlane32_swap(__float_as_uint(ps), __float_as_uint(ps), false, false);
;       ps = __uint_as_float(rr[0]) + __uint_as_float(rr[1]); }
;     l_reg = l_reg * alpha + ps;
;     ...
;     PK4(p0, 0, pa0); PK4(p0, 8, pa1); PK4(p1, 0, pa2); PK4(p1, 8, pa3);
;     ...
; }
; template <int MODE>
; __device__ __forceinline__ void qkt(f32x16& p0, f32x16& p1, const LAS unsigned char* Ks, const bf16x8* qr, const LAS unsigned char* Qs, int r32, int hi, int cbase) {
;     p0 = f32x16{}; p1 = f32x16{};
; #pragma unroll
;     for (int d0 = 0; d0 < Cfg<MODE>::ND; ++d0) { const int cb = cbase + (d0 * 16 + hi * 8) * 2;
;         const bf16x8 b0 = *(const LAS bf16x8*)(Ks + KSWZ(r32, cb));
;         const bf16x8 b1 = *(const LAS bf16x8*)(Ks + KSWZ(32 + r32, cb));
;         bf16x8 q; if constexpr (MODE == 0) q = *(const LAS bf16x8*)(Qs + KSWZ(r32, cb)); else q = qr[d0];
;         p0 = __builtin_amdgcn_mfma_f32_32x32x16_bf16(b0, q, p0, 0, 0, 0);
;         p1 = __builtin_amdgcn_mfma_f32_32x32x16_bf16(b1, q, p1, 0, 0, 0); }
; }
; __device__ __forceinline__ int v_st(int k, int c) { const int kk = (k & ~0xC) | ((k & 4) << 1) | ((k & 8) >> 1); return ((kk >> 3) * 4 + (c >> 5)) * 512 + ((kk & 7) * 32 + (c & 31)) * 2; }
; __device__ __forceinline__ int v_rd_base(int lane) { return ((lane & 3) << 3) | (((lane >> 2) & 3) << 6) | (((lane >> 4) & 1) << 5) | (((lane >> 5) & 1) << 8); }
; template <int OFF> __device__ __forceinline__ s16x4 tr_read(int vb) {
;     s16x4 r; asm volatile("ds_read_b64_tr_b16 %0, %1 offset:%2" : "=&v"(r) : "v"(vb), "i"(OFF) : "memory"); return r;
; }
; template <int D0> __device__ __forceinline__ void pv_one(f32x16& od, int vb, bf16x8 pa0, bf16x8 pa1, bf16x8 pa2, bf16x8 pa3) {
;     const s16x4 l0 = tr_read<v_rd_off(D0, 0, 0)>(vb), h0 = tr_read<v_rd_off(D0, 0, 1)>(vb), l1 = tr_read<v_rd_off(D0, 1, 0)>(vb), h1 = tr_read<v_rd_off(D0, 1, 1)>(vb);
.LBB0_431:
	v_add_f32_e32 v181, 0, v167
	ds_read_b128 v[68:71], v182 offset:49152
	ds_read_b128 v[72:75], v182 offset:57344
	ds_read_b128 v[186:189], v184 offset:49152
	ds_read_b128 v[190:193], v184 offset:57344
	ds_read_b128 v[218:221], v183 offset:49152
	ds_read_b128 v[222:225], v183 offset:57344
	v_add_f32_e32 v181, v169, v181
	s_waitcnt lgkmcnt(5)
	v_mfma_f32_32x32x16_bf16 v[82:97], v[68:71], v[110:113], 0
	v_exp_f32_e32 v141, v66
	v_exp_f32_e32 v201, v67
	v_add_f32_e32 v181, v153, v181
	v_add_f32_e32 v181, v168, v181
	v_add_f32_e32 v181, v151, v181
	v_add_f32_e32 v181, v166, v181
	v_add_f32_e32 v181, v150, v181
	s_waitcnt lgkmcnt(4)
	v_mfma_f32_32x32x16_bf16 v[66:81], v[72:75], v[110:113], 0
	v_add_f32_e32 v181, v152, v181
	v_add_f32_e32 v181, v147, v181
	v_add_f32_e32 v181, v149, v181
	v_add_f32_e32 v181, v145, v181
	v_add_f32_e32 v181, v148, v181
	v_exp_f32_e32 v132, v132
	v_add_f32_e32 v181, v143, v181
	s_waitcnt lgkmcnt(3)
	v_mfma_f32_32x32x16_bf16 v[82:97], v[186:189], v[106:109], v[82:97]
	v_exp_f32_e32 v133, v133
	v_add_f32_e32 v181, v146, v181
	v_add_f32_e32 v181, v142, v181
	v_add_f32_e32 v181, v144, v181
	v_exp_f32_e32 v130, v130
	v_add_f32_e32 v181, v132, v181
	v_exp_f32_e32 v131, v131
	s_waitcnt lgkmcnt(2)
	v_mfma_f32_32x32x16_bf16 v[66:81], v[190:193], v[106:109], v[66:81]
	v_add_f32_e32 v181, v133, v181
	v_exp_f32_e32 v128, v128
	v_add_f32_e32 v181, v141, v181
	v_exp_f32_e32 v129, v129
	v_add_f32_e32 v181, v201, v181
	v_exp_f32_e32 v126, v126
	v_add_f32_e32 v181, v130, v181
	s_waitcnt lgkmcnt(1)
	v_mfma_f32_32x32x16_bf16 v[82:97], v[218:221], v[102:105], v[82:97]
	ds_read_b128 v[226:229], v185 offset:49152
	ds_read_b128 v[230:233], v185 offset:57344
	v_exp_f32_e32 v127, v127
	v_add_f32_e32 v181, v131, v181
	v_exp_f32_e32 v138, v138
	v_add_f32_e32 v181, v128, v181
	v_exp_f32_e32 v139, v139
	v_add_f32_e32 v181, v129, v181
	s_waitcnt lgkmcnt(2)
	v_mfma_f32_32x32x16_bf16 v[66:81], v[222:225], v[102:105], v[66:81]
	v_exp_f32_e32 v136, v136
	v_add_f32_e32 v181, v126, v181
	v_exp_f32_e32 v137, v137
	v_add_f32_e32 v181, v127, v181
	v_exp_f32_e32 v134, v134
	v_add_f32_e32 v181, v138, v181
	v_exp_f32_e32 v135, v135
	s_waitcnt lgkmcnt(1)
	v_mfma_f32_32x32x16_bf16 v[82:97], v[226:229], v[98:101], v[82:97]
	v_add_f32_e32 v181, v139, v181
	v_add_f32_e32 v181, v136, v181
	v_add_f32_e32 v181, v137, v181
	v_add_f32_e32 v181, v134, v181
	v_add_f32_e32 v181, v135, v181
	v_mov_b32_e32 v186, v181
	s_nop 1
	v_permlane32_swap_b32_e32 v181, v186
	s_waitcnt lgkmcnt(0)
	v_mfma_f32_32x32x16_bf16 v[66:81], v[230:233], v[98:101], v[66:81]
	v_cvt_pk_bf16_f32 v188, v167, v169
	v_cvt_pk_bf16_f32 v189, v153, v168
	v_cvt_pk_bf16_f32 v190, v151, v166
	v_cvt_pk_bf16_f32 v191, v150, v152
	v_cvt_pk_bf16_f32 v150, v147, v149
	v_cvt_pk_bf16_f32 v151, v145, v148
	v_cvt_pk_bf16_f32 v152, v143, v146
	v_cvt_pk_bf16_f32 v153, v142, v144
	v_cvt_pk_bf16_f32 v142, v132, v133
	v_cvt_pk_bf16_f32 v143, v141, v201
	v_cvt_pk_bf16_f32 v144, v130, v131
	v_cvt_pk_bf16_f32 v145, v128, v129
	v_cvt_pk_bf16_f32 v146, v126, v127
	v_cvt_pk_bf16_f32 v147, v138, v139
	v_cvt_pk_bf16_f32 v148, v136, v137
	v_cvt_pk_bf16_f32 v149, v134, v135
	s_nop 0
	v_permlane32_swap_b32_e32 v188, v190
	v_permlane32_swap_b32_e32 v189, v191
	v_permlane32_swap_b32_e32 v150, v152
	v_permlane32_swap_b32_e32 v151, v153
	v_permlane32_swap_b32_e32 v142, v144
	v_permlane32_swap_b32_e32 v143, v145
	v_permlane32_swap_b32_e32 v146, v148
	v_permlane32_swap_b32_e32 v147, v149
	v_lshl_add_u64 v[166:167], v[164:165], 0, s[20:21]
	v_add_co_u32_e32 v126, vcc, s43, v166
	v_lshl_add_u64 v[168:169], v[162:163], 0, s[20:21]
	s_nop 0
	v_addc_co_u32_e32 v127, vcc, 0, v167, vcc
	v_add_co_u32_e32 v130, vcc, s45, v166
	s_nop 1
	v_addc_co_u32_e32 v131, vcc, 0, v167, vcc
	v_add_co_u32_e32 v134, vcc, s57, v168
	global_load_dwordx4 v[126:129], v[126:127], off
	s_nop 0
	global_load_dwordx4 v[130:133], v[130:131], off
	v_addc_co_u32_e32 v135, vcc, 0, v169, vcc
	global_load_dwordx4 v[134:137], v[134:135], off offset:128
	ds_read_b64_tr_b16 v[218:219], v175 offset:0
	ds_read_b64_tr_b16 v[220:221], v175 offset:0x800
	ds_read_b64_tr_b16 v[222:223], v175 offset:0x1000
	ds_read_b64_tr_b16 v[224:225], v175 offset:0x1800
	ds_read_b64_tr_b16 v[226:227], v175 offset:0x2000
	ds_read_b64_tr_b16 v[228:229], v175 offset:0x2800
	ds_read_b64_tr_b16 v[230:231], v175 offset:0x3000
	ds_read_b64_tr_b16 v[232:233], v175 offset:0x3800
	s_waitcnt lgkmcnt(0)
	s_nop 0
	v_mfma_f32_32x32x16_bf16 v[2:17], v[188:191], v[218:221], v[2:17]
	ds_read_b64_tr_b16 v[218:219], v175 offset:0x200
	ds_read_b64_tr_b16 v[220:221], v175 offset:0xa00
	v_mfma_f32_32x32x16_bf16 v[2:17], v[150:153], v[222:225], v[2:17]
	ds_read_b64_tr_b16 v[222:223], v175 offset:0x1200
	ds_read_b64_tr_b16 v[224:225], v175 offset:0x1a00
	v_mfma_f32_32x32x16_bf16 v[2:17], v[142:145], v[226:229], v[2:17]
	ds_read_b64_tr_b16 v[226:227], v175 offset:0x2200
	ds_read_b64_tr_b16 v[228:229], v175 offset:0x2a00
	ds_read_b64_tr_b16 v[234:235], v175 offset:0x3200
	ds_read_b64_tr_b16 v[236:237], v175 offset:0x3a00
	v_mfma_f32_32x32x16_bf16 v[2:17], v[146:149], v[230:233], v[2:17]
	s_waitcnt lgkmcnt(0)
; #define SBAR() __builtin_amdgcn_sched_barrier(0)
; template <int MODE>
; __device__ __forceinline__ void partialSM(f32x16& p0, f32x16& p1, float& m_reg, float& mn, float& alpha) {
;     constexpr float SCALE = Cfg<MODE>::SCALE, C = SCALE * 1.4426950408889634f;
;     float pmax = p0[0];
; #pragma unroll
;     for (int r = 1; r < 16; ++r) pmax = fmaxf(pmax, p0[r]);
; #pragma unroll
;     for (int r = 0; r < 16; ++r) pmax = fmaxf(pmax, p1[r]);
;     { auto rr = __builtin_amdgcn_permlane32_swap(__float_as_uint(pmax), __float_as_uint(pmax), false, false);
;       pmax = fmaxf(__uint_as_float(rr[0]), __uint_as_float(rr[1])); }
;     if (__builtin_expect(__all(pmax - m_reg <= THR / SCALE), 1)) { mn = m_reg; alpha = 1.f; }
;     else { mn = fmaxf(m_reg, pmax); alpha = __builtin_amdgcn_exp2f((m_reg - mn) * C); m_reg = mn; }
; template <int D0> __device__ __forceinline__ void pv_one(f32x16& od, int vb, bf16x8 pa0, bf16x8 pa1, bf16x8 pa2, bf16x8 pa3) {
;     const s16x4 l0 = tr_read<v_rd_off(D0, 0, 0)>(vb), h0 = tr_read<v_rd_off(D0, 0, 1)>(vb), l1 = tr_read<v_rd_off(D0, 1, 0)>(vb), h1 = tr_read<v_rd_off(D0, 1, 1)>(vb);
;     const s16x4 l2 = tr_read<v_rd_off(D0, 2, 0)>(vb), h2 = tr_read<v_rd_off(D0, 2, 1)>(vb), l3 = tr_read<v_rd_off(D0, 3, 0)>(vb), h3 = tr_read<v_rd_off(D0, 3, 1)>(vb);
;     asm volatile("s_waitcnt lgkmcnt(0)" ::: "memory"); SBAR();
;     ...
;     od = __builtin_amdgcn_mfma_f32_32x32x16_bf16(pa0, PKV(l0, h0), od, 0, 0, 0);
;     od = __builtin_amdgcn_mfma_f32_32x32x16_bf16(pa1, PKV(l1, h1), od, 0, 0, 0);
;     od = __builtin_amdgcn_mfma_f32_32x32x16_bf16(pa2, PKV(l2, h2), od, 0, 0, 0);
;     od = __builtin_amdgcn_mfma_f32_32x32x16_bf16(pa3, PKV(l3, h3), od, 0, 0, 0);
;     ...
; }
; __device__ __forceinline__ void pv_d0(f32x16* o, int vb, bf16x8 pa0, bf16x8 pa1, bf16x8 pa2, bf16x8 pa3) {
;     pv_one<0>(o[0], vb, pa0, pa1, pa2, pa3); pv_one<1>(o[1], vb, pa0, pa1, pa2, pa3); pv_one<2>(o[2], vb, pa0, pa1, pa2, pa3); pv_one<3>(o[3], vb, pa0, pa1, pa2, pa3);
	v_mfma_f32_32x32x16_bf16 v[50:65], v[188:191], v[218:221], v[50:65]
	ds_read_b64_tr_b16 v[218:219], v175 offset:0x400
	ds_read_b64_tr_b16 v[220:221], v175 offset:0xc00
	v_mfma_f32_32x32x16_bf16 v[50:65], v[150:153], v[222:225], v[50:65]
	ds_read_b64_tr_b16 v[222:223], v175 offset:0x1400
	ds_read_b64_tr_b16 v[224:225], v175 offset:0x1c00
	v_mfma_f32_32x32x16_bf16 v[50:65], v[142:145], v[226:229], v[50:65]
	ds_read_b64_tr_b16 v[226:227], v175 offset:0x2400
	ds_read_b64_tr_b16 v[228:229], v175 offset:0x2c00
	ds_read_b64_tr_b16 v[230:231], v175 offset:0x3400
	ds_read_b64_tr_b16 v[232:233], v175 offset:0x3c00
	v_mfma_f32_32x32x16_bf16 v[50:65], v[146:149], v[234:237], v[50:65]
	s_waitcnt lgkmcnt(0)
	v_mfma_f32_32x32x16_bf16 v[34:49], v[188:191], v[218:221], v[34:49]
	ds_read_b64_tr_b16 v[218:219], v175 offset:0x600
	ds_read_b64_tr_b16 v[220:221], v175 offset:0xe00
	v_mfma_f32_32x32x16_bf16 v[34:49], v[150:153], v[222:225], v[34:49]
	ds_read_b64_tr_b16 v[222:223], v175 offset:0x1600
	ds_read_b64_tr_b16 v[224:225], v175 offset:0x1e00
	v_mfma_f32_32x32x16_bf16 v[34:49], v[142:145], v[226:229], v[34:49]
	ds_read_b64_tr_b16 v[226:227], v175 offset:0x2600
	ds_read_b64_tr_b16 v[228:229], v175 offset:0x2e00
	ds_read_b64_tr_b16 v[234:235], v175 offset:0x3600
	ds_read_b64_tr_b16 v[236:237], v175 offset:0x3e00
	v_mfma_f32_32x32x16_bf16 v[34:49], v[146:149], v[230:233], v[34:49]
	s_waitcnt lgkmcnt(0)
	v_mfma_f32_32x32x16_bf16 v[18:33], v[188:191], v[218:221], v[18:33]
	v_max_f32_e32 v138, v83, v83
	v_max_f32_e32 v139, v82, v82
	v_max_f32_e32 v138, v139, v138
	v_max3_f32 v138, v138, v84, v85
	v_max3_f32 v138, v138, v86, v87
	v_max3_f32 v138, v138, v88, v89
	v_max3_f32 v138, v138, v90, v91
	v_max3_f32 v138, v138, v92, v93
	v_mfma_f32_32x32x16_bf16 v[18:33], v[150:153], v[222:225], v[18:33]
	v_max3_f32 v138, v138, v94, v95
	v_max3_f32 v138, v138, v96, v97
	v_max3_f32 v138, v138, v66, v67
	v_max3_f32 v138, v138, v68, v69
	v_max3_f32 v138, v138, v70, v71
	v_max3_f32 v138, v138, v72, v73
	v_max3_f32 v138, v138, v74, v75
	v_max3_f32 v138, v138, v76, v77
	v_mfma_f32_32x32x16_bf16 v[18:33], v[142:145], v[226:229], v[18:33]
	v_max3_f32 v138, v138, v78, v79
	v_max3_f32 v138, v138, v80, v81
	v_mov_b32_e32 v139, v138
	s_nop 1
	v_permlane32_swap_b32_e32 v138, v139
	v_max_f32_e32 v139, v139, v139
	v_max_f32_e32 v138, v138, v138
	v_max_f32_e32 v138, v138, v139
	v_max_f32_e32 v141, v140, v140
	v_sub_f32_e32 v139, v138, v140
	v_max_f32_e32 v138, v141, v138
	v_mfma_f32_32x32x16_bf16 v[18:33], v[146:149], v[234:237], v[18:33]
	v_sub_f32_e32 v141, v140, v138
	v_mul_f32_e32 v141, 0x3e38aa3b, v141
	v_exp_f32_e32 v141, v141
	v_cmp_ge_f32_e32 vcc, s7, v139
	s_cmp_eq_u64 vcc, exec
	s_cselect_b64 s[4:5], -1, 0
	s_barrier
	s_waitcnt vmcnt(3)
	v_cndmask_b32_e64 v187, v141, 1.0, s[4:5]
	v_cmp_gt_f32_e32 vcc, 1.0, v187
	s_waitcnt vmcnt(3)
	ds_write_b128 v215, v[114:117]
	ds_write_b128 v216, v[118:121]
	ds_write_b128 v179, v[122:125] offset:32768
	s_cbranch_vccz .LBB0_435
	s_and_saveexec_b64 s[48:49], s[0:1]
	ds_write_b32 v171, v187 offset:128
	s_or_b64 exec, exec, s[48:49]
	s_waitcnt lgkmcnt(0)
	ds_read_b128 v[142:145], v207 offset:224
	ds_read_b128 v[146:149], v207 offset:192
	ds_read_b128 v[150:153], v207 offset:160
	ds_read_b128 v[188:191], v207 offset:128
	s_waitcnt lgkmcnt(3)
	v_pk_mul_f32 v[16:17], v[16:17], v[144:145]
	s_waitcnt lgkmcnt(2)
	v_pk_mul_f32 v[12:13], v[12:13], v[148:149]
	s_waitcnt lgkmcnt(1)
	v_pk_mul_f32 v[8:9], v[8:9], v[152:153]
	s_waitcnt lgkmcnt(0)
	v_pk_mul_f32 v[4:5], v[4:5], v[190:191]
	v_pk_mul_f32 v[14:15], v[14:15], v[142:143]
	v_pk_mul_f32 v[10:11], v[10:11], v[146:147]
	v_pk_mul_f32 v[6:7], v[6:7], v[150:151]
	v_pk_mul_f32 v[2:3], v[2:3], v[188:189]
	v_pk_mul_f32 v[64:65], v[64:65], v[144:145]
	v_pk_mul_f32 v[60:61], v[60:61], v[148:149]
	v_pk_mul_f32 v[56:57], v[56:57], v[152:153]
	v_pk_mul_f32 v[52:53], v[52:53], v[190:191]
	v_pk_mul_f32 v[62:63], v[62:63], v[142:143]
	v_pk_mul_f32 v[58:59], v[58:59], v[146:147]
	v_pk_mul_f32 v[54:55], v[54:55], v[150:151]
	v_pk_mul_f32 v[50:51], v[50:51], v[188:189]
	v_pk_mul_f32 v[48:49], v[48:49], v[144:145]
	v_pk_mul_f32 v[44:45], v[44:45], v[148:149]
	v_pk_mul_f32 v[40:41], v[40:41], v[152:153]
	v_pk_mul_f32 v[36:37], v[36:37], v[190:191]
	v_pk_mul_f32 v[46:47], v[46:47], v[142:143]
	v_pk_mul_f32 v[42:43], v[42:43], v[146:147]
	v_pk_mul_f32 v[38:39], v[38:39], v[150:151]
	v_pk_mul_f32 v[34:35], v[34:35], v[188:189]
	v_pk_mul_f32 v[32:33], v[32:33], v[144:145]
	v_pk_mul_f32 v[28:29], v[28:29], v[148:149]
	v_pk_mul_f32 v[24:25], v[24:25], v[152:153]
	v_pk_mul_f32 v[20:21], v[20:21], v[190:191]
	v_pk_mul_f32 v[30:31], v[30:31], v[142:143]
	v_pk_mul_f32 v[26:27], v[26:27], v[146:147]
	v_pk_mul_f32 v[22:23], v[22:23], v[150:151]
	v_pk_mul_f32 v[18:19], v[18:19], v[188:189]

; #define SBAR() __builtin_amdgcn_sched_barrier(0)
; #define SWAIT() do { if constexpr (MODE == 1) asm volatile("s_waitcnt vmcnt(3)" ::: "memory"); else asm volatile("s_waitcnt vmcnt(4)" ::: "memory"); } while (0)
; template <int D0> __device__ __forceinline__ void pv_one(f32x16& od, int vb, bf16x8 pa0, bf16x8 pa1, bf16x8 pa2, bf16x8 pa3) {
;     const s16x4 l0 = tr_read<v_rd_off(D0, 0, 0)>(vb), h0 = tr_read<v_rd_off(D0, 0, 1)>(vb), l1 = tr_read<v_rd_off(D0, 1, 0)>(vb), h1 = tr_read<v_rd_off(D0, 1, 1)>(vb);
;     const s16x4 l2 = tr_read<v_rd_off(D0, 2, 0)>(vb), h2 = tr_read<v_rd_off(D0, 2, 1)>(vb), l3 = tr_read<v_rd_off(D0, 3, 0)>(vb), h3 = tr_read<v_rd_off(D0, 3, 1)>(vb);
;     asm volatile("s_waitcnt lgkmcnt(0)" ::: "memory"); SBAR();
;     ...
;     od = __builtin_amdgcn_mfma_f32_32x32x16_bf16(pa0, PKV(l0, h0), od, 0, 0, 0);
;     od = __builtin_amdgcn_mfma_f32_32x32x16_bf16(pa1, PKV(l1, h1), od, 0, 0, 0);
;     od = __builtin_amdgcn_mfma_f32_32x32x16_bf16(pa2, PKV(l2, h2), od, 0, 0, 0);
;     od = __builtin_amdgcn_mfma_f32_32x32x16_bf16(pa3, PKV(l3, h3), od, 0, 0, 0);
;     ...
; }
; __device__ __forceinline__ void pv_d0(f32x16* o, int vb, bf16x8 pa0, bf16x8 pa1, bf16x8 pa2, bf16x8 pa3) {
;     pv_one<0>(o[0], vb, pa0, pa1, pa2, pa3); pv_one<1>(o[1], vb, pa0, pa1, pa2, pa3); pv_one<2>(o[2], vb, pa0, pa1, pa2, pa3); pv_one<3>(o[3], vb, pa0, pa1, pa2, pa3);
; template <int MODE>
; __device__ __forceinline__ void attn_pass(const bf16_t* __restrict__ Qb, const bf16_t* __restrict__ Kh, const bf16_t* __restrict__ Vh, const int NT, const int kr0, const int g4, const int map,
;                                           LAS unsigned char* lds, f32x16 (&o)[4]) {
;     ...
;         __syncthreads(); SWAIT(); SWRITE(0, SE);
;         RESC(alB); __syncthreads();
;         SBAR(); qkt<MODE>(pA0, pA1, K_lds, qr, Qs, r32, hi, cbase); MASK(pA0, pA1, j + 1);
;         finishSM(pB0, pB1, alB, l_reg, pa0, pa1, pa2, pa3); SBAR();
;         if (j + 3 < NT) SLOAD(SE, j + 3); SBAR();
;         pv_d0(o, vb0 + SHM_V, pa0, pa1, pa2, pa3); partialSM<MODE>(pA0, pA1, m_reg, mnA, alA);
;         __syncthreads(); SWAIT(); SWRITE(1, SO);
;         RESC(alA); __syncthreads();
.LBB0_437:
	ds_read_b64_tr_b16 v[166:167], v173 offset:0
	ds_read_b64_tr_b16 v[168:169], v173 offset:0x800
	ds_read_b64_tr_b16 v[218:219], v173 offset:0x1000
	ds_read_b64_tr_b16 v[220:221], v173 offset:0x1800
	ds_read_b64_tr_b16 v[222:223], v173 offset:0x2000
	ds_read_b64_tr_b16 v[224:225], v173 offset:0x2800
	ds_read_b64_tr_b16 v[226:227], v173 offset:0x3000
	ds_read_b64_tr_b16 v[228:229], v173 offset:0x3800
	s_waitcnt lgkmcnt(0)
	s_nop 0
	v_mfma_f32_32x32x16_bf16 v[2:17], v[138:141], v[166:169], v[2:17]
	ds_read_b64_tr_b16 v[166:167], v173 offset:0x200
	ds_read_b64_tr_b16 v[168:169], v173 offset:0xa00
	v_mfma_f32_32x32x16_bf16 v[2:17], v[142:145], v[218:221], v[2:17]
	ds_read_b64_tr_b16 v[218:219], v173 offset:0x1200
	ds_read_b64_tr_b16 v[220:221], v173 offset:0x1a00
	v_mfma_f32_32x32x16_bf16 v[2:17], v[150:153], v[222:225], v[2:17]
	ds_read_b64_tr_b16 v[222:223], v173 offset:0x2200
	ds_read_b64_tr_b16 v[224:225], v173 offset:0x2a00
	ds_read_b64_tr_b16 v[230:231], v173 offset:0x3200
	ds_read_b64_tr_b16 v[232:233], v173 offset:0x3a00
	v_mfma_f32_32x32x16_bf16 v[2:17], v[146:149], v[226:229], v[2:17]
	s_waitcnt lgkmcnt(0)
	v_mfma_f32_32x32x16_bf16 v[50:65], v[138:141], v[166:169], v[50:65]
	ds_read_b64_tr_b16 v[166:167], v173 offset:0x400
	ds_read_b64_tr_b16 v[168:169], v173 offset:0xc00
	v_mfma_f32_32x32x16_bf16 v[50:65], v[142:145], v[218:221], v[50:65]
	ds_read_b64_tr_b16 v[218:219], v173 offset:0x1400
	ds_read_b64_tr_b16 v[220:221], v173 offset:0x1c00
	v_mfma_f32_32x32x16_bf16 v[50:65], v[150:153], v[222:225], v[50:65]
	ds_read_b64_tr_b16 v[222:223], v173 offset:0x2400
	ds_read_b64_tr_b16 v[224:225], v173 offset:0x2c00
	ds_read_b64_tr_b16 v[226:227], v173 offset:0x3400
	ds_read_b64_tr_b16 v[228:229], v173 offset:0x3c00
	v_mfma_f32_32x32x16_bf16 v[50:65], v[146:149], v[230:233], v[50:65]
	s_waitcnt lgkmcnt(0)
	v_mfma_f32_32x32x16_bf16 v[34:49], v[138:141], v[166:169], v[34:49]
	ds_read_b64_tr_b16 v[166:167], v173 offset:0x600
	ds_read_b64_tr_b16 v[168:169], v173 offset:0xe00
	v_mfma_f32_32x32x16_bf16 v[34:49], v[142:145], v[218:221], v[34:49]
	ds_read_b64_tr_b16 v[218:219], v173 offset:0x1600
	ds_read_b64_tr_b16 v[220:221], v173 offset:0x1e00
	v_mfma_f32_32x32x16_bf16 v[34:49], v[150:153], v[222:225], v[34:49]
	ds_read_b64_tr_b16 v[222:223], v173 offset:0x2600
	ds_read_b64_tr_b16 v[224:225], v173 offset:0x2e00
	ds_read_b64_tr_b16 v[230:231], v173 offset:0x3600
	ds_read_b64_tr_b16 v[232:233], v173 offset:0x3e00
	v_mfma_f32_32x32x16_bf16 v[34:49], v[146:149], v[226:229], v[34:49]
	s_waitcnt lgkmcnt(0)
	v_mfma_f32_32x32x16_bf16 v[18:33], v[138:141], v[166:169], v[18:33]
	v_max_f32_e32 v191, v83, v83
	v_max_f32_e32 v192, v82, v82
	v_max_f32_e32 v191, v192, v191
	v_max3_f32 v191, v191, v84, v85
	v_max3_f32 v191, v191, v86, v87
	v_max3_f32 v138, v191, v88, v89
	v_max3_f32 v138, v138, v90, v91
	v_max3_f32 v138, v138, v92, v93
	v_mfma_f32_32x32x16_bf16 v[18:33], v[142:145], v[218:221], v[18:33]
	v_max3_f32 v138, v138, v94, v95
	v_max3_f32 v138, v138, v96, v97
	v_max3_f32 v138, v138, v66, v67
	v_max3_f32 v138, v138, v68, v69
	v_max3_f32 v138, v138, v70, v71
	v_max3_f32 v138, v138, v72, v73
	v_max3_f32 v138, v138, v74, v75
	v_max3_f32 v138, v138, v76, v77
	v_mfma_f32_32x32x16_bf16 v[18:33], v[150:153], v[222:225], v[18:33]
	v_max3_f32 v138, v138, v78, v79
	v_max3_f32 v138, v138, v80, v81
	v_mov_b32_e32 v139, v138
	s_nop 1
	v_permlane32_swap_b32_e32 v138, v139
	v_max_f32_e32 v139, v139, v139
	v_max_f32_e32 v138, v138, v138
	v_max_f32_e32 v138, v138, v139
	v_max_f32_e32 v140, v188, v188
	v_sub_f32_e32 v139, v138, v188
	v_max_f32_e32 v138, v140, v138
	v_mfma_f32_32x32x16_bf16 v[18:33], v[146:149], v[230:233], v[18:33]
	v_sub_f32_e32 v140, v188, v138
	v_mul_f32_e32 v140, 0x3e38aa3b, v140
	v_exp_f32_e32 v140, v140
	v_cmp_ge_f32_e32 vcc, s7, v139
	s_cmp_eq_u64 vcc, exec
	s_cselect_b64 s[4:5], -1, 0
	s_barrier
	s_waitcnt vmcnt(3)
	v_cndmask_b32_e64 v141, v140, 1.0, s[4:5]
	v_cmp_gt_f32_e32 vcc, 1.0, v141
	s_waitcnt vmcnt(3)
	ds_write_b128 v215, v[126:129] offset:16384
	s_waitcnt vmcnt(3)
	ds_write_b128 v216, v[130:133] offset:16384
	s_waitcnt vmcnt(3)
	ds_write_b128 v179, v[134:137] offset:49152
	s_cbranch_vccz .LBB0_441
	s_and_saveexec_b64 s[52:53], s[0:1]
	ds_write_b32 v171, v141 offset:128
	s_or_b64 exec, exec, s[52:53]
	s_waitcnt lgkmcnt(0)
	ds_read_b128 v[126:129], v207 offset:224
	ds_read_b128 v[130:133], v207 offset:192
	ds_read_b128 v[134:137], v207 offset:160
	ds_read_b128 v[142:145], v207 offset:128
	s_waitcnt lgkmcnt(3)
	v_pk_mul_f32 v[16:17], v[16:17], v[128:129]
	s_waitcnt lgkmcnt(2)
	v_pk_mul_f32 v[12:13], v[12:13], v[132:133]
	s_waitcnt lgkmcnt(1)
	v_pk_mul_f32 v[8:9], v[8:9], v[136:137]
	s_waitcnt lgkmcnt(0)
	v_pk_mul_f32 v[4:5], v[4:5], v[144:145]
	v_pk_mul_f32 v[14:15], v[14:15], v[126:127]
	v_pk_mul_f32 v[10:11], v[10:11], v[130:131]
	v_pk_mul_f32 v[6:7], v[6:7], v[134:135]
	v_pk_mul_f32 v[2:3], v[2:3], v[142:143]
	v_pk_mul_f32 v[64:65], v[64:65], v[128:129]
	v_pk_mul_f32 v[60:61], v[60:61], v[132:133]
	v_pk_mul_f32 v[56:57], v[56:57], v[136:137]
	v_pk_mul_f32 v[52:53], v[52:53], v[144:145]
	v_pk_mul_f32 v[62:63], v[62:63], v[126:127]
	v_pk_mul_f32 v[58:59], v[58:59], v[130:131]
	v_pk_mul_f32 v[54:55], v[54:55], v[134:135]
	v_pk_mul_f32 v[50:51], v[50:51], v[142:143]
	v_pk_mul_f32 v[48:49], v[48:49], v[128:129]
	v_pk_mul_f32 v[44:45], v[44:45], v[132:133]
	v_pk_mul_f32 v[40:41], v[40:41], v[136:137]
	v_pk_mul_f32 v[36:37], v[36:37], v[144:145]
	v_pk_mul_f32 v[46:47], v[46:47], v[126:127]
	v_pk_mul_f32 v[42:43], v[42:43], v[130:131]
	v_pk_mul_f32 v[38:39], v[38:39], v[134:135]
	v_pk_mul_f32 v[34:35], v[34:35], v[142:143]
	v_pk_mul_f32 v[32:33], v[32:33], v[128:129]
	v_pk_mul_f32 v[28:29], v[28:29], v[132:133]
	v_pk_mul_f32 v[24:25], v[24:25], v[136:137]
	v_pk_mul_f32 v[20:21], v[20:21], v[144:145]
	v_pk_mul_f32 v[30:31], v[30:31], v[126:127]
	v_pk_mul_f32 v[26:27], v[26:27], v[130:131]
	v_pk_mul_f32 v[22:23], v[22:23], v[134:135]
	v_pk_mul_f32 v[18:19], v[18:19], v[142:143]

; #define LAS __attribute__((address_space(3)))
; __device__ __forceinline__ void finishSM(f32x16& p0, f32x16& p1, float alpha, float& l_reg, bf16x8& pa0, bf16x8& pa1, bf16x8& pa2, bf16x8& pa3) {
; #pragma unroll
;     for (int r = 0; r < 16; ++r) p1[r] = __builtin_amdgcn_exp2f(p1[r]);
;     float ps = 0;
; #pragma unroll
;     for (int r = 0; r < 16; ++r) ps += p0[r];
; #pragma unroll
;     for (int r = 0; r < 16; ++r) ps += p1[r];
;     { auto rr = __builtin_amdgcn_permlane32_swap(__float_as_uint(ps), __float_as_uint(ps), false, false);
;       ps = __uint_as_float(rr[0]) + __uint_as_float(rr[1]); }
;     l_reg = l_reg * alpha + ps;
;     ...
;     PK4(p0, 0, pa0); PK4(p0, 8, pa1); PK4(p1, 0, pa2); PK4(p1, 8, pa3);
;     ...
; }
; template <int MODE>
; __device__ __forceinline__ void qkt(f32x16& p0, f32x16& p1, const LAS unsigned char* Ks, const bf16x8* qr, const LAS unsigned char* Qs, int r32, int hi, int cbase) {
;     p0 = f32x16{}; p1 = f32x16{};
; #pragma unroll
;     for (int d0 = 0; d0 < Cfg<MODE>::ND; ++d0) { const int cb = cbase + (d0 * 16 + hi * 8) * 2;
;         const bf16x8 b0 = *(const LAS bf16x8*)(Ks + KSWZ(r32, cb));
;         const bf16x8 b1 = *(const LAS bf16x8*)(Ks + KSWZ(32 + r32, cb));
;         bf16x8 q; if constexpr (MODE == 0) q = *(const LAS bf16x8*)(Qs + KSWZ(r32, cb)); else q = qr[d0];
;         p0 = __builtin_amdgcn_mfma_f32_32x32x16_bf16(b0, q, p0, 0, 0, 0);
;         p1 = __builtin_amdgcn_mfma_f32_32x32x16_bf16(b1, q, p1, 0, 0, 0); }
; }
; __device__ __forceinline__ int v_st(int k, int c) { const int kk = (k & ~0xC) | ((k & 4) << 1) | ((k & 8) >> 1); return ((kk >> 3) * 4 + (c >> 5)) * 512 + ((kk & 7) * 32 + (c & 31)) * 2; }
; __device__ __forceinline__ int v_rd_base(int lane) { return ((lane & 3) << 3) | (((lane >> 2) & 3) << 6) | (((lane >> 4) & 1) << 5) | (((lane >> 5) & 1) << 8); }
; template <int OFF> __device__ __forceinline__ s16x4 tr_read(int vb) {
;     s16x4 r; asm volatile("ds_read_b64_tr_b16 %0, %1 offset:%2" : "=&v"(r) : "v"(vb), "i"(OFF) : "memory"); return r;
; }
; template <int D0> __device__ __forceinline__ void pv_one(f32x16& od, int vb, bf16x8 pa0, bf16x8 pa1, bf16x8 pa2, bf16x8 pa3) {
;     const s16x4 l0 = tr_read<v_rd_off(D0, 0, 0)>(vb), h0 = tr_read<v_rd_off(D0, 0, 1)>(vb), l1 = tr_read<v_rd_off(D0, 1, 0)>(vb), h1 = tr_read<v_rd_off(D0, 1, 1)>(vb);
.LBB0_443:
	ds_read_b128 v[68:71], v182 offset:49152
	ds_read_b128 v[72:75], v182 offset:57344
	ds_read_b128 v[114:117], v184 offset:49152
	ds_read_b128 v[118:121], v184 offset:57344
	ds_read_b128 v[122:125], v183 offset:49152
	ds_read_b128 v[162:165], v183 offset:57344
	s_waitcnt lgkmcnt(5)
	v_mfma_f32_32x32x16_bf16 v[82:97], v[68:71], v[110:113], 0
	v_exp_f32_e32 v179, v66
	v_exp_f32_e32 v180, v67
	v_exp_f32_e32 v132, v132
	v_exp_f32_e32 v133, v133
	v_exp_f32_e32 v130, v130
	ds_read_b128 v[186:189], v185 offset:49152
	ds_read_b128 v[190:193], v185 offset:57344
	s_waitcnt lgkmcnt(6)
	v_mfma_f32_32x32x16_bf16 v[66:81], v[72:75], v[110:113], 0
	v_exp_f32_e32 v112, v129
	v_add_f32_e32 v129, 0, v167
	v_add_f32_e32 v129, v169, v129
	v_add_f32_e32 v129, v153, v129
	v_exp_f32_e32 v110, v131
	v_exp_f32_e32 v111, v128
	v_exp_f32_e32 v113, v126
	s_waitcnt lgkmcnt(5)
	v_mfma_f32_32x32x16_bf16 v[82:97], v[114:117], v[106:109], v[82:97]
	v_exp_f32_e32 v126, v127
	v_exp_f32_e32 v127, v138
	v_exp_f32_e32 v128, v139
	v_exp_f32_e32 v114, v136
	v_exp_f32_e32 v115, v137
	v_exp_f32_e32 v116, v134
	v_exp_f32_e32 v117, v135
	s_waitcnt lgkmcnt(4)
	v_mfma_f32_32x32x16_bf16 v[66:81], v[118:121], v[106:109], v[66:81]
	v_add_f32_e32 v106, v168, v129
	v_add_f32_e32 v106, v151, v106
	v_add_f32_e32 v106, v166, v106
	v_add_f32_e32 v106, v150, v106
	v_add_f32_e32 v106, v152, v106
	v_add_f32_e32 v106, v147, v106
	v_add_f32_e32 v106, v149, v106
	v_add_f32_e32 v106, v145, v106
	v_add_f32_e32 v106, v148, v106
	v_add_f32_e32 v106, v143, v106
	v_add_f32_e32 v106, v146, v106
	v_add_f32_e32 v106, v142, v106
	v_add_f32_e32 v106, v144, v106
	v_add_f32_e32 v106, v132, v106
	s_waitcnt lgkmcnt(3)
	v_mfma_f32_32x32x16_bf16 v[82:97], v[122:125], v[102:105], v[82:97]
	s_waitcnt lgkmcnt(2)
	v_mfma_f32_32x32x16_bf16 v[66:81], v[162:165], v[102:105], v[66:81]
	v_add_f32_e32 v102, v133, v106
	v_add_f32_e32 v102, v179, v102
	v_add_f32_e32 v102, v180, v102
	v_add_f32_e32 v102, v130, v102
	v_add_f32_e32 v102, v110, v102
	v_add_f32_e32 v102, v111, v102
	v_add_f32_e32 v102, v112, v102
	v_add_f32_e32 v102, v113, v102
	v_add_f32_e32 v102, v126, v102
	s_waitcnt lgkmcnt(1)
	v_mfma_f32_32x32x16_bf16 v[82:97], v[186:189], v[98:101], v[82:97]
	v_add_f32_e32 v102, v127, v102
	v_add_f32_e32 v102, v128, v102
	v_add_f32_e32 v102, v114, v102
	v_add_f32_e32 v102, v115, v102
	v_add_f32_e32 v102, v116, v102
	s_waitcnt lgkmcnt(0)
	v_mfma_f32_32x32x16_bf16 v[66:81], v[190:193], v[98:101], v[66:81]
	v_add_f32_e32 v98, v117, v102
	v_mov_b32_e32 v99, v98
	v_cvt_pk_bf16_f32 v100, v167, v169
	v_cvt_pk_bf16_f32 v101, v153, v168
	v_cvt_pk_bf16_f32 v102, v151, v166
	v_cvt_pk_bf16_f32 v103, v150, v152
	s_nop 1
	v_permlane32_swap_b32_e32 v98, v99
	v_permlane32_swap_b32_e32 v100, v102
	v_permlane32_swap_b32_e32 v101, v103
	v_cvt_pk_bf16_f32 v104, v147, v149
	v_cvt_pk_bf16_f32 v105, v145, v148
	v_cvt_pk_bf16_f32 v106, v143, v146
	v_cvt_pk_bf16_f32 v107, v142, v144
	v_cvt_pk_bf16_f32 v108, v132, v133
	v_cvt_pk_bf16_f32 v109, v179, v180
	v_cvt_pk_bf16_f32 v110, v130, v110
	v_cvt_pk_bf16_f32 v111, v111, v112
	v_cvt_pk_bf16_f32 v112, v113, v126
	v_cvt_pk_bf16_f32 v113, v127, v128
	v_cvt_pk_bf16_f32 v114, v114, v115
	v_cvt_pk_bf16_f32 v115, v116, v117
	s_nop 0
	v_permlane32_swap_b32_e32 v104, v106
	v_permlane32_swap_b32_e32 v105, v107
	v_permlane32_swap_b32_e32 v108, v110
	v_permlane32_swap_b32_e32 v109, v111
	v_permlane32_swap_b32_e32 v112, v114
	v_permlane32_swap_b32_e32 v113, v115
	ds_read_b64_tr_b16 v[116:117], v175 offset:0
	ds_read_b64_tr_b16 v[118:119], v175 offset:0x800
	ds_read_b64_tr_b16 v[120:121], v175 offset:0x1000
	ds_read_b64_tr_b16 v[122:123], v175 offset:0x1800
	ds_read_b64_tr_b16 v[124:125], v175 offset:0x2000
	ds_read_b64_tr_b16 v[126:127], v175 offset:0x2800
	ds_read_b64_tr_b16 v[128:129], v175 offset:0x3000
	ds_read_b64_tr_b16 v[130:131], v175 offset:0x3800
	s_waitcnt lgkmcnt(0)
	s_nop 0
	v_mfma_f32_32x32x16_bf16 v[2:17], v[100:103], v[116:119], v[2:17]
	ds_read_b64_tr_b16 v[116:117], v175 offset:0x200
	ds_read_b64_tr_b16 v[118:119], v175 offset:0xa00
	v_mfma_f32_32x32x16_bf16 v[2:17], v[104:107], v[120:123], v[2:17]
	ds_read_b64_tr_b16 v[120:121], v175 offset:0x1200
	ds_read_b64_tr_b16 v[122:123], v175 offset:0x1a00
	v_mfma_f32_32x32x16_bf16 v[2:17], v[108:111], v[124:127], v[2:17]
	ds_read_b64_tr_b16 v[124:125], v175 offset:0x2200
	ds_read_b64_tr_b16 v[126:127], v175 offset:0x2a00
	ds_read_b64_tr_b16 v[132:133], v175 offset:0x3200
	ds_read_b64_tr_b16 v[134:135], v175 offset:0x3a00
	v_mfma_f32_32x32x16_bf16 v[2:17], v[112:115], v[128:131], v[2:17]
	s_waitcnt lgkmcnt(0)
	v_mfma_f32_32x32x16_bf16 v[50:65], v[100:103], v[116:119], v[50:65]
	ds_read_b64_tr_b16 v[116:117], v175 offset:0x400
	ds_read_b64_tr_b16 v[118:119], v175 offset:0xc00
	v_mfma_f32_32x32x16_bf16 v[50:65], v[104:107], v[120:123], v[50:65]
	ds_read_b64_tr_b16 v[120:121], v175 offset:0x1400
	ds_read_b64_tr_b16 v[122:123], v175 offset:0x1c00
	v_mfma_f32_32x32x16_bf16 v[50:65], v[108:111], v[124:127], v[50:65]
	ds_read_b64_tr_b16 v[124:125], v175 offset:0x2400
	ds_read_b64_tr_b16 v[126:127], v175 offset:0x2c00
	ds_read_b64_tr_b16 v[128:129], v175 offset:0x3400
	ds_read_b64_tr_b16 v[130:131], v175 offset:0x3c00
	v_mfma_f32_32x32x16_bf16 v[50:65], v[112:115], v[132:135], v[50:65]
	s_waitcnt lgkmcnt(0)
; #define SBAR() __builtin_amdgcn_sched_barrier(0)
; template <int MODE>
; __device__ __forceinline__ void partialSM(f32x16& p0, f32x16& p1, float& m_reg, float& mn, float& alpha) {
;     constexpr float SCALE = Cfg<MODE>::SCALE, C = SCALE * 1.4426950408889634f;
;     float pmax = p0[0];
; #pragma unroll
;     for (int r = 1; r < 16; ++r) pmax = fmaxf(pmax, p0[r]);
; #pragma unroll
;     for (int r = 0; r < 16; ++r) pmax = fmaxf(pmax, p1[r]);
;     { auto rr = __builtin_amdgcn_permlane32_swap(__float_as_uint(pmax), __float_as_uint(pmax), false, false);
;       pmax = fmaxf(__uint_as_float(rr[0]), __uint_as_float(rr[1])); }
;     if (__builtin_expect(__all(pmax - m_reg <= THR / SCALE), 1)) { mn = m_reg; alpha = 1.f; }
;     else { mn = fmaxf(m_reg, pmax); alpha = __builtin_amdgcn_exp2f((m_reg - mn) * C); m_reg = mn; }
;     const float mnC = -mn * C;
; #pragma unroll
;     for (int r = 0; r < 16; ++r) p0[r] = fmaf(p0[r], C, mnC);
; #pragma unroll
;     for (int r = 0; r < 16; ++r) p1[r] = fmaf(p1[r], C, mnC);
; #pragma unroll
;     for (int r = 0; r < 16; ++r) p0[r] = __builtin_amdgcn_exp2f(p0[r]);
; }
; template <int D0> __device__ __forceinline__ void pv_one(f32x16& od, int vb, bf16x8 pa0, bf16x8 pa1, bf16x8 pa2, bf16x8 pa3) {
;     const s16x4 l0 = tr_read<v_rd_off(D0, 0, 0)>(vb), h0 = tr_read<v_rd_off(D0, 0, 1)>(vb), l1 = tr_read<v_rd_off(D0, 1, 0)>(vb), h1 = tr_read<v_rd_off(D0, 1, 1)>(vb);
;     const s16x4 l2 = tr_read<v_rd_off(D0, 2, 0)>(vb), h2 = tr_read<v_rd_off(D0, 2, 1)>(vb), l3 = tr_read<v_rd_off(D0, 3, 0)>(vb), h3 = tr_read<v_rd_off(D0, 3, 1)>(vb);
;     asm volatile("s_waitcnt lgkmcnt(0)" ::: "memory"); SBAR();
;     ...
;     od = __builtin_amdgcn_mfma_f32_32x32x16_bf16(pa0, PKV(l0, h0), od, 0, 0, 0);
;     od = __builtin_amdgcn_mfma_f32_32x32x16_bf16(pa1, PKV(l1, h1), od, 0, 0, 0);
;     od = __builtin_amdgcn_mfma_f32_32x32x16_bf16(pa2, PKV(l2, h2), od, 0, 0, 0);
;     od = __builtin_amdgcn_mfma_f32_32x32x16_bf16(pa3, PKV(l3, h3), od, 0, 0, 0);
;     ...
; }
; __device__ __forceinline__ void pv_d0(f32x16* o, int vb, bf16x8 pa0, bf16x8 pa1, bf16x8 pa2, bf16x8 pa3) {
;     pv_one<0>(o[0], vb, pa0, pa1, pa2, pa3); pv_one<1>(o[1], vb, pa0, pa1, pa2, pa3); pv_one<2>(o[2], vb, pa0, pa1, pa2, pa3); pv_one<3>(o[3], vb, pa0, pa1, pa2, pa3);
	v_mfma_f32_32x32x16_bf16 v[34:49], v[100:103], v[116:119], v[34:49]
	ds_read_b64_tr_b16 v[116:117], v175 offset:0x600
	ds_read_b64_tr_b16 v[118:119], v175 offset:0xe00
	v_mfma_f32_32x32x16_bf16 v[34:49], v[104:107], v[120:123], v[34:49]
	ds_read_b64_tr_b16 v[120:121], v175 offset:0x1600
	ds_read_b64_tr_b16 v[122:123], v175 offset:0x1e00
	v_mfma_f32_32x32x16_bf16 v[34:49], v[108:111], v[124:127], v[34:49]
	ds_read_b64_tr_b16 v[124:125], v175 offset:0x2600
	ds_read_b64_tr_b16 v[126:127], v175 offset:0x2e00
	ds_read_b64_tr_b16 v[132:133], v175 offset:0x3600
	ds_read_b64_tr_b16 v[134:135], v175 offset:0x3e00
	v_mfma_f32_32x32x16_bf16 v[34:49], v[112:115], v[128:131], v[34:49]
	s_waitcnt lgkmcnt(0)
	v_mfma_f32_32x32x16_bf16 v[18:33], v[100:103], v[116:119], v[18:33]
	v_max_f32_e32 v128, v83, v83
	v_max_f32_e32 v129, v82, v82
	v_max_f32_e32 v128, v129, v128
	v_max3_f32 v128, v128, v84, v85
	v_max3_f32 v128, v128, v86, v87
	v_max3_f32 v100, v128, v88, v89
	v_max3_f32 v100, v100, v90, v91
	v_max3_f32 v100, v100, v92, v93
	v_mfma_f32_32x32x16_bf16 v[18:33], v[104:107], v[120:123], v[18:33]
	v_max3_f32 v100, v100, v94, v95
	v_max3_f32 v100, v100, v96, v97
	v_max3_f32 v100, v100, v66, v67
	v_max3_f32 v100, v100, v68, v69
	v_max3_f32 v100, v100, v70, v71
	v_max3_f32 v100, v100, v72, v73
	v_max3_f32 v100, v100, v74, v75
	v_max3_f32 v100, v100, v76, v77
	v_mfma_f32_32x32x16_bf16 v[18:33], v[108:111], v[124:127], v[18:33]
	v_max3_f32 v100, v100, v78, v79
	v_max3_f32 v100, v100, v80, v81
	v_mov_b32_e32 v101, v100
	s_nop 1
	v_permlane32_swap_b32_e32 v100, v101
	v_max_f32_e32 v101, v101, v101
	v_max_f32_e32 v100, v100, v100
	v_max_f32_e32 v100, v100, v101
	v_max_f32_e32 v102, v140, v140
	v_max_f32_e32 v102, v102, v100
	v_sub_f32_e32 v101, v100, v140
	v_mfma_f32_32x32x16_bf16 v[18:33], v[112:115], v[132:135], v[18:33]
	v_sub_f32_e32 v100, v140, v102
	s_mov_b32 s4, 0x42800000
	v_mul_f32_e32 v100, 0x3e38aa3b, v100
	v_exp_f32_e32 v100, v100
	v_cmp_ge_f32_e32 vcc, s4, v101
	s_cmp_eq_u64 vcc, exec
	s_cselect_b64 vcc, -1, 0
	v_cndmask_b32_e32 v101, v102, v140, vcc
	v_cndmask_b32_e64 v100, v100, 1.0, vcc
	v_mul_f32_e32 v101, 0xbe38aa3b, v101
	v_fmamk_f32 v82, v82, 0x3e38aa3b, v101
	v_fmamk_f32 v83, v83, 0x3e38aa3b, v101
	v_fmamk_f32 v84, v84, 0x3e38aa3b, v101
	v_fmamk_f32 v85, v85, 0x3e38aa3b, v101
	v_fmamk_f32 v86, v86, 0x3e38aa3b, v101
	v_fmamk_f32 v87, v87, 0x3e38aa3b, v101
	v_fmamk_f32 v88, v88, 0x3e38aa3b, v101
	v_fmamk_f32 v89, v89, 0x3e38aa3b, v101
	v_fmamk_f32 v90, v90, 0x3e38aa3b, v101
	v_fmamk_f32 v91, v91, 0x3e38aa3b, v101
	v_fmamk_f32 v92, v92, 0x3e38aa3b, v101
	v_fmamk_f32 v93, v93, 0x3e38aa3b, v101
	v_fmamk_f32 v94, v94, 0x3e38aa3b, v101
	v_fmamk_f32 v95, v95, 0x3e38aa3b, v101
	v_fmamk_f32 v96, v96, 0x3e38aa3b, v101
	v_fmamk_f32 v97, v97, 0x3e38aa3b, v101
	v_cmp_gt_f32_e32 vcc, 1.0, v100
	s_barrier
	s_cbranch_vccz .LBB0_447
	s_and_saveexec_b64 s[4:5], s[0:1]
	ds_write_b32 v171, v100 offset:128
	s_or_b64 exec, exec, s[4:5]
	s_waitcnt lgkmcnt(0)
	ds_read_b128 v[102:105], v207 offset:224
	ds_read_b128 v[106:109], v207 offset:192
	ds_read_b128 v[110:113], v207 offset:160
	ds_read_b128 v[114:117], v207 offset:128
	s_waitcnt lgkmcnt(3)
	v_pk_mul_f32 v[16:17], v[16:17], v[104:105]
	s_waitcnt lgkmcnt(2)
	v_pk_mul_f32 v[12:13], v[12:13], v[108:109]
	s_waitcnt lgkmcnt(1)
	v_pk_mul_f32 v[8:9], v[8:9], v[112:113]
	s_waitcnt lgkmcnt(0)
	v_pk_mul_f32 v[4:5], v[4:5], v[116:117]
	v_pk_mul_f32 v[14:15], v[14:15], v[102:103]
	v_pk_mul_f32 v[10:11], v[10:11], v[106:107]
	v_pk_mul_f32 v[6:7], v[6:7], v[110:111]
	v_pk_mul_f32 v[2:3], v[2:3], v[114:115]
	v_pk_mul_f32 v[64:65], v[64:65], v[104:105]
	v_pk_mul_f32 v[60:61], v[60:61], v[108:109]
	v_pk_mul_f32 v[56:57], v[56:57], v[112:113]
	v_pk_mul_f32 v[52:53], v[52:53], v[116:117]
	v_pk_mul_f32 v[62:63], v[62:63], v[102:103]
	v_pk_mul_f32 v[58:59], v[58:59], v[106:107]
	v_pk_mul_f32 v[54:55], v[54:55], v[110:111]
	v_pk_mul_f32 v[50:51], v[50:51], v[114:115]
	v_pk_mul_f32 v[48:49], v[48:49], v[104:105]
	v_pk_mul_f32 v[44:45], v[44:45], v[108:109]
	v_pk_mul_f32 v[40:41], v[40:41], v[112:113]
	v_pk_mul_f32 v[36:37], v[36:37], v[116:117]
	v_pk_mul_f32 v[46:47], v[46:47], v[102:103]
	v_pk_mul_f32 v[42:43], v[42:43], v[106:107]
	v_pk_mul_f32 v[38:39], v[38:39], v[110:111]
	v_pk_mul_f32 v[34:35], v[34:35], v[114:115]
	v_pk_mul_f32 v[32:33], v[32:33], v[104:105]
	v_pk_mul_f32 v[28:29], v[28:29], v[108:109]
	v_pk_mul_f32 v[24:25], v[24:25], v[112:113]
	v_pk_mul_f32 v[20:21], v[20:21], v[116:117]
	v_pk_mul_f32 v[30:31], v[30:31], v[102:103]
	v_pk_mul_f32 v[26:27], v[26:27], v[106:107]
	v_pk_mul_f32 v[22:23], v[22:23], v[110:111]
	v_pk_mul_f32 v[18:19], v[18:19], v[114:115]
; #define LAS __attribute__((address_space(3)))
; __device__ __forceinline__ void finishSM(f32x16& p0, f32x16& p1, float alpha, float& l_reg, bf16x8& pa0, bf16x8& pa1, bf16x8& pa2, bf16x8& pa3) {
; #pragma unroll
;     for (int r = 0; r < 16; ++r) p1[r] = __builtin_amdgcn_exp2f(p1[r]);
;     float ps = 0;
; #pragma unroll
;     for (int r = 0; r < 16; ++r) ps += p0[r];
; #pragma unroll
;     for (int r = 0; r < 16; ++r) ps += p1[r];
;     { auto rr = __builtin_amdgcn_permlane32_swap(__float_as_uint(ps), __float_as_uint(ps), false, false);
;       ps = __uint_as_float(rr[0]) + __uint_as_float(rr[1]); }
;     l_reg = l_reg * alpha + ps;
;     ...
;     PK4(p0, 0, pa0); PK4(p0, 8, pa1); PK4(p1, 0, pa2); PK4(p1, 8, pa3);
;     ...
; }
; template <int MODE>
; __device__ __forceinline__ void qkt(f32x16& p0, f32x16& p1, const LAS unsigned char* Ks, const bf16x8* qr, const LAS unsigned char* Qs, int r32, int hi, int cbase) {
;     p0 = f32x16{}; p1 = f32x16{};
; #pragma unroll
;     for (int d0 = 0; d0 < Cfg<MODE>::ND; ++d0) { const int cb = cbase + (d0 * 16 + hi * 8) * 2;
;         const bf16x8 b0 = *(const LAS bf16x8*)(Ks + KSWZ(r32, cb));
;         const bf16x8 b1 = *(const LAS bf16x8*)(Ks + KSWZ(32 + r32, cb));
;         bf16x8 q; if constexpr (MODE == 0) q = *(const LAS bf16x8*)(Qs + KSWZ(r32, cb)); else q = qr[d0];
;         p0 = __builtin_amdgcn_mfma_f32_32x32x16_bf16(b0, q, p0, 0, 0, 0);
;         p1 = __builtin_amdgcn_mfma_f32_32x32x16_bf16(b1, q, p1, 0, 0, 0); }
; }
; __device__ __forceinline__ int v_st(int k, int c) { const int kk = (k & ~0xC) | ((k & 4) << 1) | ((k & 8) >> 1); return ((kk >> 3) * 4 + (c >> 5)) * 512 + ((kk & 7) * 32 + (c & 31)) * 2; }
; __device__ __forceinline__ int v_rd_base(int lane) { return ((lane & 3) << 3) | (((lane >> 2) & 3) << 6) | (((lane >> 4) & 1) << 5) | (((lane >> 5) & 1) << 8); }
; template <int OFF> __device__ __forceinline__ s16x4 tr_read(int vb) {
;     s16x4 r; asm volatile("ds_read_b64_tr_b16 %0, %1 offset:%2" : "=&v"(r) : "v"(vb), "i"(OFF) : "memory"); return r;
; }
; template <int D0> __device__ __forceinline__ void pv_one(f32x16& od, int vb, bf16x8 pa0, bf16x8 pa1, bf16x8 pa2, bf16x8 pa3) {
;     const s16x4 l0 = tr_read<v_rd_off(D0, 0, 0)>(vb), h0 = tr_read<v_rd_off(D0, 0, 1)>(vb), l1 = tr_read<v_rd_off(D0, 1, 0)>(vb), h1 = tr_read<v_rd_off(D0, 1, 1)>(vb);
.LBB0_447:
	v_exp_f32_e32 v102, v82
	v_exp_f32_e32 v103, v83
	v_exp_f32_e32 v82, v84
	v_fmamk_f32 v66, v66, 0x3e38aa3b, v101
	v_exp_f32_e32 v84, v85
	v_fmamk_f32 v113, v77, 0x3e38aa3b, v101
	v_exp_f32_e32 v77, v86
	v_exp_f32_e32 v85, v66
	v_add_f32_e32 v66, 0, v102
	v_exp_f32_e32 v83, v87
	v_add_f32_e32 v66, v103, v66
	v_fmamk_f32 v112, v76, 0x3e38aa3b, v101
	v_exp_f32_e32 v76, v88
	v_add_f32_e32 v66, v82, v66
	v_fmamk_f32 v114, v78, 0x3e38aa3b, v101
	v_exp_f32_e32 v78, v89
	v_add_f32_e32 v66, v84, v66
	v_fmamk_f32 v109, v73, 0x3e38aa3b, v101
	v_exp_f32_e32 v73, v90
	v_add_f32_e32 v66, v77, v66
	v_fmamk_f32 v111, v75, 0x3e38aa3b, v101
	v_exp_f32_e32 v75, v91
	v_add_f32_e32 v66, v83, v66
	v_fmamk_f32 v107, v71, 0x3e38aa3b, v101
	v_exp_f32_e32 v71, v92
	v_add_f32_e32 v66, v76, v66
	v_fmamk_f32 v110, v74, 0x3e38aa3b, v101
	v_exp_f32_e32 v74, v93
	v_add_f32_e32 v66, v78, v66
	v_fmamk_f32 v105, v69, 0x3e38aa3b, v101
	v_exp_f32_e32 v69, v94
	v_add_f32_e32 v66, v73, v66
	v_fmamk_f32 v108, v72, 0x3e38aa3b, v101
	v_exp_f32_e32 v72, v95
	v_add_f32_e32 v66, v75, v66
	v_fmamk_f32 v104, v68, 0x3e38aa3b, v101
	v_exp_f32_e32 v68, v96
	v_add_f32_e32 v66, v71, v66
	v_fmamk_f32 v106, v70, 0x3e38aa3b, v101
	v_exp_f32_e32 v70, v97
	v_add_f32_e32 v66, v74, v66
	v_fmamk_f32 v67, v67, 0x3e38aa3b, v101
	v_add_f32_e32 v66, v69, v66
	v_exp_f32_e32 v86, v67
	v_add_f32_e32 v66, v72, v66
	v_exp_f32_e32 v87, v104
	v_add_f32_e32 v66, v68, v66
	v_exp_f32_e32 v88, v105
	v_add_f32_e32 v66, v70, v66
	v_exp_f32_e32 v89, v106
	v_add_f32_e32 v66, v85, v66
	v_exp_f32_e32 v90, v107
	v_add_f32_e32 v66, v86, v66
	v_exp_f32_e32 v91, v108
	v_add_f32_e32 v66, v87, v66
	v_exp_f32_e32 v92, v109
	v_add_f32_e32 v66, v88, v66
	v_exp_f32_e32 v93, v110
	v_add_f32_e32 v66, v89, v66
	v_exp_f32_e32 v94, v111
	v_add_f32_e32 v66, v90, v66
	v_exp_f32_e32 v95, v112
	v_add_f32_e32 v66, v91, v66
	v_exp_f32_e32 v96, v113
	v_add_f32_e32 v66, v92, v66
	v_fmamk_f32 v79, v79, 0x3e38aa3b, v101
	v_exp_f32_e32 v97, v114
	v_add_f32_e32 v66, v93, v66
	v_fmamk_f32 v80, v80, 0x3e38aa3b, v101
	v_exp_f32_e32 v104, v79
	v_add_f32_e32 v66, v94, v66
	v_fmac_f32_e32 v101, 0x3e38aa3b, v81
	v_exp_f32_e32 v105, v80
	v_add_f32_e32 v66, v95, v66
	v_exp_f32_e32 v101, v101
	v_add_f32_e32 v66, v96, v66
	v_add_f32_e32 v66, v97, v66
	v_add_f32_e32 v66, v104, v66
	v_add_f32_e32 v66, v105, v66
	v_add_f32_e32 v66, v101, v66
	v_mov_b32_e32 v67, v66
	s_nop 1
	v_permlane32_swap_b32_e32 v66, v67
	v_cvt_pk_bf16_f32 v80, v102, v103
	v_cvt_pk_bf16_f32 v81, v82, v84
	v_cvt_pk_bf16_f32 v82, v77, v83
	v_cvt_pk_bf16_f32 v83, v76, v78
	v_cvt_pk_bf16_f32 v76, v73, v75
	v_cvt_pk_bf16_f32 v77, v71, v74
	v_cvt_pk_bf16_f32 v78, v69, v72
	v_cvt_pk_bf16_f32 v79, v68, v70
	v_cvt_pk_bf16_f32 v68, v85, v86
	v_cvt_pk_bf16_f32 v69, v87, v88
	v_cvt_pk_bf16_f32 v70, v89, v90
	v_cvt_pk_bf16_f32 v71, v91, v92
	v_cvt_pk_bf16_f32 v72, v93, v94
	v_cvt_pk_bf16_f32 v73, v95, v96
	v_cvt_pk_bf16_f32 v74, v97, v104
	v_cvt_pk_bf16_f32 v75, v105, v101
	s_nop 0
	v_permlane32_swap_b32_e32 v80, v82
	v_permlane32_swap_b32_e32 v81, v83
	v_permlane32_swap_b32_e32 v76, v78
	v_permlane32_swap_b32_e32 v77, v79
	v_permlane32_swap_b32_e32 v68, v70
	v_permlane32_swap_b32_e32 v69, v71
	v_permlane32_swap_b32_e32 v72, v74
	v_permlane32_swap_b32_e32 v73, v75
	ds_read_b64_tr_b16 v[84:85], v173 offset:0
	ds_read_b64_tr_b16 v[86:87], v173 offset:0x800
	ds_read_b64_tr_b16 v[88:89], v173 offset:0x1000
	ds_read_b64_tr_b16 v[90:91], v173 offset:0x1800
	ds_read_b64_tr_b16 v[92:93], v173 offset:0x2000
	ds_read_b64_tr_b16 v[94:95], v173 offset:0x2800
	ds_read_b64_tr_b16 v[102:103], v173 offset:0x3000
	ds_read_b64_tr_b16 v[104:105], v173 offset:0x3800
	s_waitcnt lgkmcnt(0)
	s_nop 0
	v_mfma_f32_32x32x16_bf16 v[2:17], v[80:83], v[84:87], v[2:17]
	ds_read_b64_tr_b16 v[84:85], v173 offset:0x200
	ds_read_b64_tr_b16 v[86:87], v173 offset:0xa00
	v_mfma_f32_32x32x16_bf16 v[2:17], v[76:79], v[88:91], v[2:17]
	ds_read_b64_tr_b16 v[88:89], v173 offset:0x1200
	ds_read_b64_tr_b16 v[90:91], v173 offset:0x1a00
	v_mfma_f32_32x32x16_bf16 v[2:17], v[68:71], v[92:95], v[2:17]
	ds_read_b64_tr_b16 v[92:93], v173 offset:0x2200
	ds_read_b64_tr_b16 v[94:95], v173 offset:0x2a00
	ds_read_b64_tr_b16 v[106:107], v173 offset:0x3200
	ds_read_b64_tr_b16 v[108:109], v173 offset:0x3a00
	v_mfma_f32_32x32x16_bf16 v[2:17], v[72:75], v[102:105], v[2:17]
	s_waitcnt lgkmcnt(0)
	v_mfma_f32_32x32x16_bf16 v[50:65], v[80:83], v[84:87], v[50:65]
	ds_read_b64_tr_b16 v[84:85], v173 offset:0x400
	ds_read_b64_tr_b16 v[86:87], v173 offset:0xc00
	v_mfma_f32_32x32x16_bf16 v[50:65], v[76:79], v[88:91], v[50:65]
	ds_read_b64_tr_b16 v[88:89], v173 offset:0x1400
	ds_read_b64_tr_b16 v[90:91], v173 offset:0x1c00
	v_mfma_f32_32x32x16_bf16 v[50:65], v[68:71], v[92:95], v[50:65]
	ds_read_b64_tr_b16 v[92:93], v173 offset:0x2400
	ds_read_b64_tr_b16 v[94:95], v173 offset:0x2c00
	ds_read_b64_tr_b16 v[102:103], v173 offset:0x3400
	ds_read_b64_tr_b16 v[104:105], v173 offset:0x3c00
	v_mfma_f32_32x32x16_bf16 v[50:65], v[72:75], v[106:109], v[50:65]
	s_waitcnt lgkmcnt(0)
	v_mfma_f32_32x32x16_bf16 v[34:49], v[80:83], v[84:87], v[34:49]
	ds_read_b64_tr_b16 v[84:85], v173 offset:0x600
	ds_read_b64_tr_b16 v[86:87], v173 offset:0xe00
	v_mfma_f32_32x32x16_bf16 v[34:49], v[76:79], v[88:91], v[34:49]
	ds_read_b64_tr_b16 v[88:89], v173 offset:0x1600
	ds_read_b64_tr_b16 v[90:91], v173 offset:0x1e00
	v_mfma_f32_32x32x16_bf16 v[34:49], v[68:71], v[92:95], v[34:49]
	ds_read_b64_tr_b16 v[92:93], v173 offset:0x2600
	ds_read_b64_tr_b16 v[94:95], v173 offset:0x2e00
	ds_read_b64_tr_b16 v[106:107], v173 offset:0x3600
	ds_read_b64_tr_b16 v[108:109], v173 offset:0x3e00
	v_mfma_f32_32x32x16_bf16 v[34:49], v[72:75], v[102:105], v[34:49]
	s_waitcnt lgkmcnt(0)
	v_mfma_f32_32x32x16_bf16 v[18:33], v[80:83], v[84:87], v[18:33]
	v_mfma_f32_32x32x16_bf16 v[18:33], v[76:79], v[88:91], v[18:33]
	v_mfma_f32_32x32x16_bf16 v[18:33], v[68:71], v[92:95], v[18:33]
	v_mfma_f32_32x32x16_bf16 v[18:33], v[72:75], v[106:109], v[18:33]
	s_and_saveexec_b64 s[4:5], s[0:1]
	v_add_f32_e32 v68, v98, v99
	v_fmac_f32_e32 v68, v178, v141
	v_add_f32_e32 v66, v66, v67
	v_fmac_f32_e32 v66, v68, v100
	ds_write_b32 v171, v66
	s_or_b64 exec, exec, s[4:5]
	s_waitcnt lgkmcnt(0)
	ds_read_b128 v[66:69], v207
	ds_read_b128 v[70:73], v207 offset:32
	ds_read_b128 v[104:107], v207 offset:64
	ds_read_b128 v[108:111], v207 offset:96
	s_waitcnt lgkmcnt(0)
	s_barrier
; __device__ __forceinline__ unsigned char f2fp8(float a) { return (unsigned char)(__builtin_amdgcn_cvt_pk_fp8_f32(a, a, 0, false) & 0xff); }
; __device__ __forceinline__ float bf_lo(unsigned w) { return __uint_as_float(w << 16); }
; __device__ __forceinline__ float bf_hi(unsigned w) { return __uint_as_float(w & 0xffff0000u); }
; __device__ __forceinline__ int crow(int r, int hi) { return (r & 3) + 8 * (r >> 2) + 4 * hi; }
; template <int MODE>
; __device__ __forceinline__ void attn_pass(const bf16_t* __restrict__ Qb, const bf16_t* __restrict__ Kh, const bf16_t* __restrict__ Vh, const int NT, const int kr0, const int g4, const int map,
;                                           LAS unsigned char* lds, f32x16 (&o)[4]) {
;     ...
;     for (int r = 0; r < 16; ++r) { const float rl = __builtin_amdgcn_rcpf(li_l[crow(r, hi)]);
; #pragma unroll
;         for (int d = 0; d < 4; ++d) o[d][r] *= rl; }
; __device__ __forceinline__ void p3_attention(Frame& F) {
;     ...
;         float sw[4];
; #pragma unroll
;         for (int d = 0; d < 4; ++d) sw[d] = F.in[I_SUBLN][d * 32 + r32] * (1.0f - LAM_INIT);
;         u32x4 o1p[8];
; #pragma unroll
;         for (int k = 0; k < 8; ++k) o1p[k] = o1l[k * 512];
;         int hi1 = hi, r32a = r32; asm volatile("" : "+v"(hi1), "+v"(r32a));
;         unsigned char* od = F.ws + WS_ODF + (size_t)(b * SEQ + qb * 256 + wid * 32) * 1024 + h * 128 + r32a;
; #pragma unroll
;         for (int r = 0; r < 16; ++r) {
;             float dd[4], ss = 0.f;
; #pragma unroll
;             for (int d = 0; d < 4; ++d) { const unsigned pw = o1p[d * 2 + (r >> 3)][(r & 7) >> 1]; const float o1 = (r & 1) ? bf_hi(pw) : bf_lo(pw); dd[d] = o1 - lam * o[d][r]; ss += dd[d] * dd[d]; }
;             ss += __shfl_xor(ss, 1); ss += __shfl_xor(ss, 2); ss += __shfl_xor(ss, 4); ss += __shfl_xor(ss, 8); ss += __shfl_xor(ss, 16);
;             const float rs = 1.0f / sqrtf(ss * (1.0f / 128.0f) + RMS_EPS);
;             unsigned char* orow = od + (size_t)attn::crow(r, hi1) * 1024;
; #pragma unroll
;             for (int d = 0; d < 4; ++d) orow[d * 32] = f2fp8(dd[d] * rs * sw[d] * OSCALE);
	v_rcp_f32_e32 v75, v66
	v_rcp_f32_e32 v67, v67
	v_sub_f32_e32 v74, v199, v177
	v_mul_f32_e32 v103, v2, v75
	v_lshlrev_b32_e32 v2, 2, v172
	v_mul_f32_e32 v112, v50, v75
	global_load_dword v50, v2, s[60:61]
	global_load_dword v113, v2, s[60:61] offset:128
	global_load_dword v114, v2, s[60:61] offset:256
	s_nop 0
	global_load_dword v2, v2, s[60:61] offset:384
	v_mul_f32_e32 v117, v3, v67
	v_rcp_f32_e32 v3, v68
	v_mul_f32_e32 v115, v34, v75
	v_mul_f32_e32 v116, v18, v75
	v_add_f32_e32 v66, 0x3e4ccccd, v74
	v_mul_f32_e32 v121, v4, v3
	v_rcp_f32_e32 v4, v69
	v_mul_f32_e32 v122, v52, v3
	v_mul_f32_e32 v123, v36, v3
	v_mul_f32_e32 v124, v20, v3
	v_rcp_f32_e32 v3, v70
	v_mul_f32_e32 v125, v5, v4
	v_mul_f32_e32 v126, v53, v4
	v_mul_f32_e32 v127, v37, v4
	v_mul_f32_e32 v128, v21, v4
	v_rcp_f32_e32 v4, v71
	v_mul_f32_e32 v101, v6, v3
	v_mul_f32_e32 v102, v54, v3
	v_mul_f32_e32 v100, v38, v3
	v_mul_f32_e32 v99, v22, v3
	v_rcp_f32_e32 v3, v72
	v_mul_f32_e32 v97, v7, v4
	v_mul_f32_e32 v98, v55, v4
	v_mul_f32_e32 v96, v39, v4
	v_mul_f32_e32 v95, v23, v4
	v_rcp_f32_e32 v4, v73
	v_mul_f32_e32 v93, v8, v3
	v_mul_f32_e32 v94, v56, v3
	v_mul_f32_e32 v92, v40, v3
	v_mul_f32_e32 v91, v24, v3
	v_rcp_f32_e32 v3, v104
	v_mul_f32_e32 v89, v9, v4
	v_mul_f32_e32 v90, v57, v4
	v_mul_f32_e32 v88, v41, v4
	v_mul_f32_e32 v87, v25, v4
	v_rcp_f32_e32 v4, v105
	v_mul_f32_e32 v85, v10, v3
	v_mul_f32_e32 v86, v58, v3
	v_mul_f32_e32 v84, v42, v3
	v_mul_f32_e32 v83, v26, v3
	v_rcp_f32_e32 v3, v106
	v_mul_f32_e32 v81, v11, v4
	v_mul_f32_e32 v82, v59, v4
	v_mul_f32_e32 v80, v43, v4
	v_mul_f32_e32 v79, v27, v4
	v_rcp_f32_e32 v4, v107
	v_mul_f32_e32 v77, v12, v3
	v_mul_f32_e32 v78, v60, v3
	v_mul_f32_e32 v76, v44, v3
	v_mul_f32_e32 v75, v28, v3
	v_rcp_f32_e32 v3, v108
	v_mul_f32_e32 v73, v13, v4
	v_mul_f32_e32 v74, v61, v4
	v_mul_f32_e32 v72, v45, v4
	v_mul_f32_e32 v71, v29, v4
	v_rcp_f32_e32 v4, v109
	v_mul_f32_e32 v118, v51, v67
	v_mul_f32_e32 v119, v35, v67
	v_mul_f32_e32 v120, v19, v67
	v_mul_f32_e32 v69, v14, v3
	v_mul_f32_e32 v70, v62, v3
	v_mul_f32_e32 v68, v46, v3
	v_mul_f32_e32 v67, v30, v3
	v_rcp_f32_e32 v3, v110
	v_mul_f32_e32 v61, v15, v4
	v_mul_f32_e32 v62, v63, v4
	v_mul_f32_e32 v60, v47, v4
	v_mul_f32_e32 v59, v31, v4
	v_rcp_f32_e32 v4, v111
	v_mul_f32_e32 v56, v48, v3
	v_mul_f32_e32 v57, v16, v3
	v_mul_f32_e32 v58, v64, v3
	v_mul_f32_e32 v55, v32, v3
	v_mul_f32_e32 v45, v17, v4
	v_mul_f32_e32 v44, v65, v4
	v_mul_f32_e32 v43, v49, v4
	s_waitcnt vmcnt(3)
	v_mul_f32_e32 v41, 0x3f4ccccd, v50
	v_lshrrev_b32_e32 v50, 1, v0
	v_and_b32_e32 v35, 0xe0, v50
	v_add_u32_e32 v36, s42, v35
	v_mbcnt_lo_u32_b32 v35, -1, 0
	v_mbcnt_hi_u32_b32 v35, -1, v35
	v_and_b32_e32 v47, 64, v35
	v_xor_b32_e32 v46, 1, v35
	v_add_u32_e32 v48, 64, v47
	v_cmp_lt_i32_e32 vcc, v46, v48
	v_mul_f32_e32 v42, v33, v4
	s_waitcnt vmcnt(0)
	v_mul_f32_e32 v38, 0x3f4ccccd, v2
	v_cndmask_b32_e32 v46, v35, v46, vcc
	ds_read_b128 v[26:29], v200
	ds_read_b128 v[10:13], v200 offset:8192
	ds_read_b128 v[30:33], v200 offset:16384
	ds_read_b128 v[14:17], v200 offset:24576
	ds_read_b128 v[22:25], v200 offset:32768
	ds_read_b128 v[6:9], v200 offset:40960
	ds_read_b128 v[18:21], v200 offset:49152
	ds_read_b128 v[2:5], v200 offset:57344
	v_lshlrev_b32_e32 v47, 2, v46
	s_waitcnt lgkmcnt(7)
	v_lshlrev_b32_e32 v46, 16, v26
	v_fma_f32 v64, -v66, v103, v46
	s_waitcnt lgkmcnt(5)
	v_lshlrev_b32_e32 v46, 16, v30
	v_fma_f32 v103, -v66, v112, v46
	v_mul_f32_e32 v46, v103, v103
	s_waitcnt lgkmcnt(3)
	v_lshlrev_b32_e32 v49, 16, v22
	v_fmac_f32_e32 v46, v64, v64
	v_fma_f32 v104, -v66, v115, v49
	s_waitcnt lgkmcnt(1)
	v_lshlrev_b32_e32 v49, 16, v18
	v_fmac_f32_e32 v46, v104, v104
	v_fma_f32 v105, -v66, v116, v49
	v_fmac_f32_e32 v46, v105, v105
	ds_bpermute_b32 v51, v47, v46
	v_xor_b32_e32 v49, 2, v35
	v_cmp_lt_i32_e32 vcc, v49, v48
	v_ashrrev_i32_e32 v37, 31, v36
	v_lshlrev_b64 v[36:37], 10, v[36:37]
	v_cndmask_b32_e32 v49, v35, v49, vcc
	v_lshlrev_b32_e32 v49, 2, v49
	s_waitcnt lgkmcnt(0)
	v_add_f32_e32 v46, v46, v51
	ds_bpermute_b32 v52, v49, v46
	v_xor_b32_e32 v51, 4, v35
	v_cmp_lt_i32_e32 vcc, v51, v48
	v_lshl_add_u64 v[36:37], s[82:83], 0, v[36:37]
	v_lshl_add_u64 v[178:179], v[36:37], 0, s[38:39]
	v_cndmask_b32_e32 v51, v35, v51, vcc
	v_lshlrev_b32_e32 v51, 2, v51
	s_waitcnt lgkmcnt(0)
	v_add_f32_e32 v46, v46, v52
	ds_bpermute_b32 v53, v51, v46
	v_xor_b32_e32 v52, 8, v35
	v_cmp_lt_i32_e32 vcc, v52, v48
	s_mov_b32 s6, 0xf800000
	v_bfe_u32 v186, v0, 5, 1
	v_cndmask_b32_e32 v52, v35, v52, vcc
	v_lshlrev_b32_e32 v52, 2, v52
	s_waitcnt lgkmcnt(0)
	v_add_f32_e32 v46, v46, v53
	ds_bpermute_b32 v54, v52, v46
	v_xor_b32_e32 v53, 16, v35
	v_cmp_lt_i32_e32 vcc, v53, v48
	v_mov_b32_e32 v34, v172
	v_mov_b32_e32 v63, v186
	v_cndmask_b32_e32 v35, v35, v53, vcc
	v_lshlrev_b32_e32 v53, 2, v35
	s_waitcnt lgkmcnt(0)
	v_add_f32_e32 v46, v46, v54
	ds_bpermute_b32 v48, v53, v46
	v_and_b32_e32 v30, 0xffff0000, v30
	v_and_b32_e32 v26, 0xffff0000, v26
	v_fma_f32 v30, -v66, v118, v30
	s_waitcnt lgkmcnt(0)
; __device__ __forceinline__ unsigned char f2fp8(float a) { return (unsigned char)(__builtin_amdgcn_cvt_pk_fp8_f32(a, a, 0, false) & 0xff); }
; __device__ __forceinline__ float bf_lo(unsigned w) { return __uint_as_float(w << 16); }
; __device__ __forceinline__ float bf_hi(unsigned w) { return __uint_as_float(w & 0xffff0000u); }
; __device__ __forceinline__ int crow(int r, int hi) { return (r & 3) + 8 * (r >> 2) + 4 * hi; }
; __device__ __forceinline__ void p3_attention(Frame& F) {
;     ...
;         for (int r = 0; r < 16; ++r) {
;             float dd[4], ss = 0.f;
; #pragma unroll
;             for (int d = 0; d < 4; ++d) { const unsigned pw = o1p[d * 2 + (r >> 3)][(r & 7) >> 1]; const float o1 = (r & 1) ? bf_hi(pw) : bf_lo(pw); dd[d] = o1 - lam * o[d][r]; ss += dd[d] * dd[d]; }
;             ss += __shfl_xor(ss, 1); ss += __shfl_xor(ss, 2); ss += __shfl_xor(ss, 4); ss += __shfl_xor(ss, 8); ss += __shfl_xor(ss, 16);
;             const float rs = 1.0f / sqrtf(ss * (1.0f / 128.0f) + RMS_EPS);
;             unsigned char* orow = od + (size_t)attn::crow(r, hi1) * 1024;
; #pragma unroll
;             for (int d = 0; d < 4; ++d) orow[d * 32] = f2fp8(dd[d] * rs * sw[d] * OSCALE);
	v_add_f32_e32 v36, v46, v48
	v_mov_b32_e32 v48, 0x3727c5ac
	v_fmamk_f32 v36, v36, 0x3c000000, v48
	v_mul_f32_e32 v37, 0x4f800000, v36
	v_cmp_gt_f32_e32 vcc, s6, v36
	v_fma_f32 v26, -v66, v117, v26
	v_and_b32_e32 v22, 0xffff0000, v22
	v_cndmask_b32_e32 v36, v36, v37, vcc
	v_sqrt_f32_e32 v37, v36
	v_fma_f32 v22, -v66, v119, v22
	v_and_b32_e32 v18, 0xffff0000, v18
	v_fma_f32 v18, -v66, v120, v18
	v_add_u32_e32 v46, -1, v37
	v_fma_f32 v54, -v46, v37, v36
	v_cmp_ge_f32_e64 s[4:5], 0, v54
	v_add_u32_e32 v54, 1, v37
	v_ashrrev_i32_e32 v35, 31, v34
	v_cndmask_b32_e64 v46, v37, v46, s[4:5]
	v_fma_f32 v37, -v54, v37, v36
	v_cmp_lt_f32_e64 s[4:5], 0, v37
	v_lshl_add_u64 v[34:35], v[178:179], 0, v[34:35]
	s_mov_b64 s[42:43], 0x41600000
	v_cndmask_b32_e64 v37, v46, v54, s[4:5]
	v_mul_f32_e32 v46, 0x37800000, v37
	v_mov_b32_e32 v54, 0x260
	v_cndmask_b32_e32 v37, v37, v46, vcc
	v_cmp_class_f32_e32 vcc, v36, v54
	v_lshl_add_u64 v[34:35], v[34:35], 0, s[42:43]
	v_mul_f32_e32 v40, 0x3f4ccccd, v113
	v_cndmask_b32_e32 v37, v37, v36, vcc
	v_div_scale_f32 v65, s[4:5], v37, v37, 1.0
	v_rcp_f32_e32 v106, v65
	v_lshlrev_b32_e32 v36, 2, v63
	v_mul_f32_e32 v39, 0x3f4ccccd, v114
	v_mov_b32_e32 v46, 0
	v_fma_f32 v63, -v65, v106, 1.0
	v_fmac_f32_e32 v106, v63, v106
	v_div_scale_f32 v63, vcc, 1.0, v37, 1.0
	v_mul_f32_e32 v107, v63, v106
	v_fma_f32 v108, -v65, v107, v63
	v_fmac_f32_e32 v107, v108, v106
	v_fma_f32 v63, -v65, v107, v63
	v_div_fmas_f32 v63, v63, v106, v107
	v_div_fixup_f32 v63, v63, v37, 1.0
	v_mul_f32_e32 v37, v64, v63
	v_mul_f32_e32 v64, v30, v30
	v_fmac_f32_e32 v64, v26, v26
	v_fmac_f32_e32 v64, v22, v22
	v_fmac_f32_e32 v64, v18, v18
	ds_bpermute_b32 v65, v47, v64
	v_mul_f32_e32 v37, v41, v37
	v_mul_f32_e32 v37, 0x41800000, v37
	v_mov_b32_e32 v106, 0
	v_cvt_pk_fp8_f32 v106, v37, v37
	s_waitcnt lgkmcnt(0)
	v_add_f32_e32 v107, v64, v65
	ds_bpermute_b32 v108, v49, v107
	v_ashrrev_i32_e32 v37, 31, v36
	v_lshlrev_b64 v[64:65], 10, v[36:37]
	v_lshl_add_u64 v[64:65], v[34:35], 0, v[64:65]
	global_store_byte v[64:65], v106, off
	s_waitcnt lgkmcnt(0)
	v_add_f32_e32 v37, v107, v108
	ds_bpermute_b32 v106, v51, v37
	v_mul_f32_e32 v103, v103, v63
	v_mul_f32_e32 v103, v40, v103
	v_mul_f32_e32 v103, 0x41800000, v103
	v_mov_b32_e32 v107, 0
	s_waitcnt lgkmcnt(0)
	v_add_f32_e32 v37, v37, v106
	ds_bpermute_b32 v106, v52, v37
	v_cvt_pk_fp8_f32 v107, v103, v103
	v_mul_f32_e32 v103, v104, v63
	v_mul_f32_e32 v103, v39, v103
	v_mul_f32_e32 v103, 0x41800000, v103
	s_waitcnt lgkmcnt(0)
	v_add_f32_e32 v37, v37, v106
	ds_bpermute_b32 v104, v53, v37
	v_mov_b32_e32 v106, 0
	v_cvt_pk_fp8_f32 v106, v103, v103
	v_mul_f32_e32 v63, v105, v63
	v_mul_f32_e32 v63, v38, v63
	s_waitcnt lgkmcnt(0)
	v_add_f32_e32 v37, v37, v104
	v_fmamk_f32 v37, v37, 0x3c000000, v48
	v_mul_f32_e32 v103, 0x4f800000, v37
	v_cmp_gt_f32_e32 vcc, s6, v37
	v_mul_f32_e32 v63, 0x41800000, v63
	v_mov_b32_e32 v104, 0
	v_cndmask_b32_e32 v37, v37, v103, vcc
	v_sqrt_f32_e32 v103, v37
	v_cvt_pk_fp8_f32 v104, v63, v63
	global_store_byte v[64:65], v107, off offset:32
	global_store_byte v[64:65], v106, off offset:64
	global_store_byte v[64:65], v104, off offset:96
	v_add_u32_e32 v63, -1, v103
	v_fma_f32 v105, -v63, v103, v37
	v_cmp_ge_f32_e64 s[4:5], 0, v105
	v_add_u32_e32 v105, 1, v103
	v_mov_b32_e32 v107, 0
	v_cndmask_b32_e64 v63, v103, v63, s[4:5]
	v_fma_f32 v103, -v105, v103, v37
	v_cmp_lt_f32_e64 s[4:5], 0, v103
	s_cmp_gt_i32 s55, 14
	s_nop 0
	v_cndmask_b32_e64 v63, v63, v105, s[4:5]
	v_mul_f32_e32 v103, 0x37800000, v63
	v_cndmask_b32_e32 v63, v63, v103, vcc
	v_cmp_class_f32_e32 vcc, v37, v54
	v_lshlrev_b32_e32 v105, 16, v19
	v_fma_f32 v105, -v66, v124, v105
	v_cndmask_b32_e32 v37, v63, v37, vcc
	v_div_scale_f32 v63, s[4:5], v37, v37, 1.0
	v_rcp_f32_e32 v103, v63
	v_and_b32_e32 v19, 0xffff0000, v19
	v_fma_f32 v64, -v63, v103, 1.0
	v_fmac_f32_e32 v103, v64, v103
	v_div_scale_f32 v64, vcc, 1.0, v37, 1.0
	v_mul_f32_e32 v65, v64, v103
	v_fma_f32 v104, -v63, v65, v64
	v_fmac_f32_e32 v65, v104, v103
	v_fma_f32 v63, -v63, v65, v64
	v_div_fmas_f32 v63, v63, v103, v65
	v_lshlrev_b32_e32 v65, 16, v31
	v_div_fixup_f32 v37, v63, v37, 1.0
	v_lshlrev_b32_e32 v63, 16, v27
	v_fma_f32 v103, -v66, v122, v65
	v_fma_f32 v63, -v66, v121, v63
	v_mul_f32_e32 v65, v103, v103
	v_lshlrev_b32_e32 v104, 16, v23
	v_fmac_f32_e32 v65, v63, v63
	v_fma_f32 v104, -v66, v123, v104
	v_fmac_f32_e32 v65, v104, v104
	v_fmac_f32_e32 v65, v105, v105
	ds_bpermute_b32 v106, v47, v65
	v_mul_f32_e32 v26, v26, v37
	v_mul_f32_e32 v26, v41, v26
	v_mul_f32_e32 v26, 0x41800000, v26
	v_cvt_pk_fp8_f32 v107, v26, v26
	s_waitcnt lgkmcnt(0)
	v_add_f32_e32 v26, v65, v106
	ds_bpermute_b32 v106, v49, v26
	v_or_b32_e32 v64, 1, v36
	v_ashrrev_i32_e32 v65, 31, v64
	v_lshlrev_b64 v[64:65], 10, v[64:65]
	v_mul_f32_e32 v30, v30, v37
	s_waitcnt lgkmcnt(0)
	v_add_f32_e32 v26, v26, v106
	ds_bpermute_b32 v106, v51, v26
	v_lshl_add_u64 v[64:65], v[34:35], 0, v[64:65]
	v_mul_f32_e32 v30, v40, v30
	global_store_byte v[64:65], v107, off
	v_mul_f32_e32 v30, 0x41800000, v30
	s_waitcnt lgkmcnt(0)
	v_add_f32_e32 v26, v26, v106
	ds_bpermute_b32 v106, v52, v26
	v_mov_b32_e32 v107, 0
	v_cvt_pk_fp8_f32 v107, v30, v30
	v_mul_f32_e32 v22, v22, v37
	v_mul_f32_e32 v22, v39, v22
	s_waitcnt lgkmcnt(0)
	v_add_f32_e32 v26, v26, v106
	ds_bpermute_b32 v30, v53, v26
	v_mul_f32_e32 v22, 0x41800000, v22
	v_mov_b32_e32 v106, 0
	v_cvt_pk_fp8_f32 v106, v22, v22
	v_mul_f32_e32 v18, v18, v37
	s_waitcnt lgkmcnt(0)
; __device__ __forceinline__ unsigned char f2fp8(float a) { return (unsigned char)(__builtin_amdgcn_cvt_pk_fp8_f32(a, a, 0, false) & 0xff); }
; __device__ __forceinline__ float bf_lo(unsigned w) { return __uint_as_float(w << 16); }
; __device__ __forceinline__ float bf_hi(unsigned w) { return __uint_as_float(w & 0xffff0000u); }
; __device__ __forceinline__ int crow(int r, int hi) { return (r & 3) + 8 * (r >> 2) + 4 * hi; }
; __device__ __forceinline__ void p3_attention(Frame& F) {
;     ...
;         for (int r = 0; r < 16; ++r) {
;             float dd[4], ss = 0.f;
; #pragma unroll
;             for (int d = 0; d < 4; ++d) { const unsigned pw = o1p[d * 2 + (r >> 3)][(r & 7) >> 1]; const float o1 = (r & 1) ? bf_hi(pw) : bf_lo(pw); dd[d] = o1 - lam * o[d][r]; ss += dd[d] * dd[d]; }
;             ss += __shfl_xor(ss, 1); ss += __shfl_xor(ss, 2); ss += __shfl_xor(ss, 4); ss += __shfl_xor(ss, 8); ss += __shfl_xor(ss, 16);
;             const float rs = 1.0f / sqrtf(ss * (1.0f / 128.0f) + RMS_EPS);
;             unsigned char* orow = od + (size_t)attn::crow(r, hi1) * 1024;
; #pragma unroll
;             for (int d = 0; d < 4; ++d) orow[d * 32] = f2fp8(dd[d] * rs * sw[d] * OSCALE);
;         }
	v_add_f32_e32 v22, v26, v30
	v_fmamk_f32 v22, v22, 0x3c000000, v48
	v_mul_f32_e32 v26, 0x4f800000, v22
	v_cmp_gt_f32_e32 vcc, s6, v22
	v_mul_f32_e32 v18, v38, v18
	v_mul_f32_e32 v18, 0x41800000, v18
	v_cndmask_b32_e32 v22, v22, v26, vcc
	v_sqrt_f32_e32 v26, v22
	v_mov_b32_e32 v30, 0
	v_cvt_pk_fp8_f32 v30, v18, v18
	global_store_byte v[64:65], v107, off offset:32
	global_store_byte v[64:65], v106, off offset:64
	global_store_byte v[64:65], v30, off offset:96
	v_add_u32_e32 v18, -1, v26
	v_fma_f32 v37, -v18, v26, v22
	v_cmp_ge_f32_e64 s[4:5], 0, v37
	v_add_u32_e32 v37, 1, v26
	v_and_b32_e32 v27, 0xffff0000, v27
	v_cndmask_b32_e64 v18, v26, v18, s[4:5]
	v_fma_f32 v26, -v37, v26, v22
	v_cmp_lt_f32_e64 s[4:5], 0, v26
	v_fma_f32 v27, -v66, v125, v27
	v_and_b32_e32 v23, 0xffff0000, v23
	v_cndmask_b32_e64 v18, v18, v37, s[4:5]
	v_mul_f32_e32 v26, 0x37800000, v18
	v_cndmask_b32_e32 v18, v18, v26, vcc
	v_cmp_class_f32_e32 vcc, v22, v54
	v_fma_f32 v23, -v66, v127, v23
	v_mov_b32_e32 v65, 0
	v_cndmask_b32_e32 v18, v18, v22, vcc
	v_div_scale_f32 v22, s[4:5], v18, v18, 1.0
	v_rcp_f32_e32 v26, v22
	s_nop 0
	v_fma_f32 v30, -v22, v26, 1.0
	v_fmac_f32_e32 v26, v30, v26
	v_div_scale_f32 v30, vcc, 1.0, v18, 1.0
	v_mul_f32_e32 v37, v30, v26
	v_fma_f32 v64, -v22, v37, v30
	v_fmac_f32_e32 v37, v64, v26
	v_fma_f32 v22, -v22, v37, v30
	v_and_b32_e32 v30, 0xffff0000, v31
	v_fma_f32 v30, -v66, v126, v30
	v_mul_f32_e32 v31, v30, v30
	v_fmac_f32_e32 v31, v27, v27
	v_div_fmas_f32 v22, v22, v26, v37
	v_fmac_f32_e32 v31, v23, v23
	v_fma_f32 v37, -v66, v128, v19
	v_fmac_f32_e32 v31, v37, v37
	ds_bpermute_b32 v19, v47, v31
	v_div_fixup_f32 v22, v22, v18, 1.0
	v_mul_f32_e32 v26, v63, v22
	v_mul_f32_e32 v26, v41, v26
	v_mul_f32_e32 v26, 0x41800000, v26
	v_mov_b32_e32 v63, 0
	v_cvt_pk_fp8_f32 v63, v26, v26
	s_waitcnt lgkmcnt(0)
	v_add_f32_e32 v26, v31, v19
	ds_bpermute_b32 v31, v49, v26
	v_or_b32_e32 v18, 2, v36
	v_ashrrev_i32_e32 v19, 31, v18
	v_lshlrev_b64 v[18:19], 10, v[18:19]
	v_lshl_add_u64 v[18:19], v[34:35], 0, v[18:19]
	s_waitcnt lgkmcnt(0)
	v_add_f32_e32 v26, v26, v31
	ds_bpermute_b32 v31, v51, v26
	global_store_byte v[18:19], v63, off
	v_mul_f32_e32 v63, v103, v22
	v_mul_f32_e32 v63, v40, v63
	v_mul_f32_e32 v63, 0x41800000, v63
	s_waitcnt lgkmcnt(0)
	v_add_f32_e32 v26, v26, v31
	ds_bpermute_b32 v31, v52, v26
	v_mov_b32_e32 v64, 0
	v_cvt_pk_fp8_f32 v64, v63, v63
	v_mul_f32_e32 v63, v104, v22
	v_mul_f32_e32 v63, v39, v63
	s_waitcnt lgkmcnt(0)
	v_add_f32_e32 v26, v26, v31
	ds_bpermute_b32 v31, v53, v26
	v_mul_f32_e32 v22, v105, v22
	v_mul_f32_e32 v63, 0x41800000, v63
	v_mul_f32_e32 v22, v38, v22
	v_cvt_pk_fp8_f32 v65, v63, v63
	s_waitcnt lgkmcnt(0)
	v_add_f32_e32 v26, v26, v31
	v_fmamk_f32 v26, v26, 0x3c000000, v48
	v_mul_f32_e32 v31, 0x4f800000, v26
	v_cmp_gt_f32_e32 vcc, s6, v26
	v_mul_f32_e32 v22, 0x41800000, v22
	v_mov_b32_e32 v63, 0
	v_cndmask_b32_e32 v26, v26, v31, vcc
	v_sqrt_f32_e32 v31, v26
	v_cvt_pk_fp8_f32 v63, v22, v22
	global_store_byte v[18:19], v64, off offset:32
	global_store_byte v[18:19], v65, off offset:64
	global_store_byte v[18:19], v63, off offset:96
	v_add_u32_e32 v22, -1, v31
	v_fma_f32 v103, -v22, v31, v26
	v_cmp_ge_f32_e64 s[4:5], 0, v103
	v_add_u32_e32 v103, 1, v31
	v_lshlrev_b32_e32 v64, 16, v20
	v_cndmask_b32_e64 v22, v31, v22, s[4:5]
	v_fma_f32 v31, -v103, v31, v26
	v_cmp_lt_f32_e64 s[4:5], 0, v31
	v_fma_f32 v64, -v66, v99, v64
	v_mov_b32_e32 v99, 0
	v_cndmask_b32_e64 v22, v22, v103, s[4:5]
	v_mul_f32_e32 v31, 0x37800000, v22
	v_cndmask_b32_e32 v22, v22, v31, vcc
	v_cmp_class_f32_e32 vcc, v26, v54
	v_and_b32_e32 v20, 0xffff0000, v20
	v_fma_f32 v20, -v66, v95, v20
	v_cndmask_b32_e32 v22, v22, v26, vcc
	v_div_scale_f32 v26, s[4:5], v22, v22, 1.0
	v_rcp_f32_e32 v31, v26
	s_nop 0
	v_fma_f32 v18, -v26, v31, 1.0
	v_fmac_f32_e32 v31, v18, v31
	v_div_scale_f32 v18, vcc, 1.0, v22, 1.0
	v_mul_f32_e32 v19, v18, v31
	v_fma_f32 v63, -v26, v19, v18
	v_fmac_f32_e32 v19, v63, v31
	v_fma_f32 v18, -v26, v19, v18
	v_div_fmas_f32 v18, v18, v31, v19
	v_div_fixup_f32 v22, v18, v22, 1.0
	v_mul_f32_e32 v19, v27, v22
	v_lshlrev_b32_e32 v27, 16, v32
	v_lshlrev_b32_e32 v26, 16, v28
	v_fma_f32 v27, -v66, v102, v27
	v_fma_f32 v26, -v66, v101, v26
	v_mul_f32_e32 v31, v27, v27
	v_lshlrev_b32_e32 v63, 16, v24
	v_fmac_f32_e32 v31, v26, v26
	v_fma_f32 v63, -v66, v100, v63
	v_fmac_f32_e32 v31, v63, v63
	v_fmac_f32_e32 v31, v64, v64
	ds_bpermute_b32 v65, v47, v31
	v_mul_f32_e32 v19, v41, v19
	v_mul_f32_e32 v19, 0x41800000, v19
	v_or_b32_e32 v18, 3, v36
	v_cvt_pk_fp8_f32 v99, v19, v19
	s_waitcnt lgkmcnt(0)
	v_add_f32_e32 v31, v31, v65
	ds_bpermute_b32 v65, v49, v31
	v_ashrrev_i32_e32 v19, 31, v18
	v_lshlrev_b64 v[18:19], 10, v[18:19]
	v_mul_f32_e32 v30, v30, v22
	v_lshl_add_u64 v[18:19], v[34:35], 0, v[18:19]
	s_waitcnt lgkmcnt(0)
	v_add_f32_e32 v31, v31, v65
	ds_bpermute_b32 v65, v51, v31
	v_mul_f32_e32 v30, v40, v30
	global_store_byte v[18:19], v99, off
	v_mul_f32_e32 v30, 0x41800000, v30
	v_mov_b32_e32 v99, 0
	s_waitcnt lgkmcnt(0)
	v_add_f32_e32 v31, v31, v65
	ds_bpermute_b32 v65, v52, v31
	v_cvt_pk_fp8_f32 v99, v30, v30
	v_mul_f32_e32 v23, v23, v22
	v_mul_f32_e32 v23, v39, v23
	v_mul_f32_e32 v23, 0x41800000, v23
	s_waitcnt lgkmcnt(0)
	v_add_f32_e32 v30, v31, v65
	ds_bpermute_b32 v31, v53, v30
	v_mov_b32_e32 v65, 0
	v_cvt_pk_fp8_f32 v65, v23, v23
	v_mul_f32_e32 v22, v37, v22
	v_mul_f32_e32 v22, v38, v22
	s_waitcnt lgkmcnt(0)
; __device__ __forceinline__ unsigned char f2fp8(float a) { return (unsigned char)(__builtin_amdgcn_cvt_pk_fp8_f32(a, a, 0, false) & 0xff); }
; __device__ __forceinline__ float bf_lo(unsigned w) { return __uint_as_float(w << 16); }
; __device__ __forceinline__ float bf_hi(unsigned w) { return __uint_as_float(w & 0xffff0000u); }
; __device__ __forceinline__ int crow(int r, int hi) { return (r & 3) + 8 * (r >> 2) + 4 * hi; }
; __device__ __forceinline__ void p3_attention(Frame& F) {
;     ...
;         for (int r = 0; r < 16; ++r) {
;             float dd[4], ss = 0.f;
; #pragma unroll
;             for (int d = 0; d < 4; ++d) { const unsigned pw = o1p[d * 2 + (r >> 3)][(r & 7) >> 1]; const float o1 = (r & 1) ? bf_hi(pw) : bf_lo(pw); dd[d] = o1 - lam * o[d][r]; ss += dd[d] * dd[d]; }
;             ss += __shfl_xor(ss, 1); ss += __shfl_xor(ss, 2); ss += __shfl_xor(ss, 4); ss += __shfl_xor(ss, 8); ss += __shfl_xor(ss, 16);
;             const float rs = 1.0f / sqrtf(ss * (1.0f / 128.0f) + RMS_EPS);
;             unsigned char* orow = od + (size_t)attn::crow(r, hi1) * 1024;
; #pragma unroll
;             for (int d = 0; d < 4; ++d) orow[d * 32] = f2fp8(dd[d] * rs * sw[d] * OSCALE);
;         }
	v_add_f32_e32 v23, v30, v31
	v_fmamk_f32 v23, v23, 0x3c000000, v48
	v_mul_f32_e32 v30, 0x4f800000, v23
	v_cmp_gt_f32_e32 vcc, s6, v23
	v_mul_f32_e32 v22, 0x41800000, v22
	v_mov_b32_e32 v31, 0
	v_cndmask_b32_e32 v23, v23, v30, vcc
	v_sqrt_f32_e32 v30, v23
	v_cvt_pk_fp8_f32 v31, v22, v22
	global_store_byte v[18:19], v99, off offset:32
	global_store_byte v[18:19], v65, off offset:64
	global_store_byte v[18:19], v31, off offset:96
	v_add_u32_e32 v22, -1, v30
	v_fma_f32 v37, -v22, v30, v23
	v_cmp_ge_f32_e64 s[4:5], 0, v37
	v_add_u32_e32 v37, 1, v30
	v_and_b32_e32 v24, 0xffff0000, v24
	v_cndmask_b32_e64 v22, v30, v22, s[4:5]
	v_fma_f32 v30, -v37, v30, v23
	v_cmp_lt_f32_e64 s[4:5], 0, v30
	v_fma_f32 v24, -v66, v96, v24
	s_nop 0
	v_cndmask_b32_e64 v22, v22, v37, s[4:5]
	v_mul_f32_e32 v30, 0x37800000, v22
	v_cndmask_b32_e32 v22, v22, v30, vcc
	v_cmp_class_f32_e32 vcc, v23, v54
	s_nop 1
	v_cndmask_b32_e32 v22, v22, v23, vcc
	v_div_scale_f32 v23, s[4:5], v22, v22, 1.0
	v_rcp_f32_e32 v30, v23
	s_nop 0
	v_fma_f32 v18, -v23, v30, 1.0
	v_fmac_f32_e32 v30, v18, v30
	v_div_scale_f32 v18, vcc, 1.0, v22, 1.0
	v_mul_f32_e32 v19, v18, v30
	v_fma_f32 v31, -v23, v19, v18
	v_fmac_f32_e32 v19, v31, v30
	v_fma_f32 v18, -v23, v19, v18
	v_div_fmas_f32 v18, v18, v30, v19
	v_div_fixup_f32 v22, v18, v22, 1.0
	v_mul_f32_e32 v19, v26, v22
	v_and_b32_e32 v26, 0xffff0000, v32
	v_and_b32_e32 v23, 0xffff0000, v28
	v_fma_f32 v26, -v66, v98, v26
	v_fma_f32 v23, -v66, v97, v23
	v_mul_f32_e32 v28, v26, v26
	v_fmac_f32_e32 v28, v23, v23
	v_fmac_f32_e32 v28, v24, v24
	v_fmac_f32_e32 v28, v20, v20
	ds_bpermute_b32 v30, v47, v28
	v_mul_f32_e32 v19, v41, v19
	v_mul_f32_e32 v19, 0x41800000, v19
	v_mov_b32_e32 v31, 0
	v_add_u32_e32 v18, 8, v36
	s_waitcnt lgkmcnt(0)
	v_add_f32_e32 v28, v28, v30
	ds_bpermute_b32 v30, v49, v28
	v_cvt_pk_fp8_f32 v31, v19, v19
	v_ashrrev_i32_e32 v19, 31, v18
	v_lshlrev_b64 v[18:19], 10, v[18:19]
	v_mul_f32_e32 v27, v27, v22
	s_waitcnt lgkmcnt(0)
	v_add_f32_e32 v28, v28, v30
	ds_bpermute_b32 v30, v51, v28
	v_lshl_add_u64 v[18:19], v[34:35], 0, v[18:19]
	v_mul_f32_e32 v27, v40, v27
	global_store_byte v[18:19], v31, off
	v_mul_f32_e32 v27, 0x41800000, v27
	s_waitcnt lgkmcnt(0)
	v_add_f32_e32 v28, v28, v30
	ds_bpermute_b32 v30, v52, v28
	v_mov_b32_e32 v31, 0
	v_cvt_pk_fp8_f32 v31, v27, v27
	v_mul_f32_e32 v27, v63, v22
	v_mul_f32_e32 v27, v39, v27
	s_waitcnt lgkmcnt(0)
	v_add_f32_e32 v28, v28, v30
	ds_bpermute_b32 v30, v53, v28
	v_mul_f32_e32 v27, 0x41800000, v27
	v_mov_b32_e32 v32, 0
	v_cvt_pk_fp8_f32 v32, v27, v27
	v_mul_f32_e32 v22, v64, v22
	s_waitcnt lgkmcnt(0)
	v_add_f32_e32 v27, v28, v30
	v_fmamk_f32 v27, v27, 0x3c000000, v48
	v_mul_f32_e32 v28, 0x4f800000, v27
	v_cmp_gt_f32_e32 vcc, s6, v27
	v_mul_f32_e32 v22, v38, v22
	v_mul_f32_e32 v22, 0x41800000, v22
	v_cndmask_b32_e32 v27, v27, v28, vcc
	v_sqrt_f32_e32 v28, v27
	v_mov_b32_e32 v30, 0
	v_cvt_pk_fp8_f32 v30, v22, v22
	global_store_byte v[18:19], v31, off offset:32
	global_store_byte v[18:19], v32, off offset:64
	global_store_byte v[18:19], v30, off offset:96
	v_add_u32_e32 v22, -1, v28
	v_fma_f32 v37, -v22, v28, v27
	v_cmp_ge_f32_e64 s[4:5], 0, v37
	v_add_u32_e32 v37, 1, v28
	v_lshlrev_b32_e32 v31, 16, v21
	v_cndmask_b32_e64 v22, v28, v22, s[4:5]
	v_fma_f32 v28, -v37, v28, v27
	v_cmp_lt_f32_e64 s[4:5], 0, v28
	v_fma_f32 v31, -v66, v91, v31
	v_and_b32_e32 v21, 0xffff0000, v21
	v_cndmask_b32_e64 v22, v22, v37, s[4:5]
	v_mul_f32_e32 v28, 0x37800000, v22
	v_cndmask_b32_e32 v22, v22, v28, vcc
	v_cmp_class_f32_e32 vcc, v27, v54
	v_mov_b32_e32 v37, 0
	v_fma_f32 v21, -v66, v87, v21
	v_cndmask_b32_e32 v22, v22, v27, vcc
	v_div_scale_f32 v27, s[4:5], v22, v22, 1.0
	v_rcp_f32_e32 v28, v27
	s_nop 0
	v_fma_f32 v18, -v27, v28, 1.0
	v_fmac_f32_e32 v28, v18, v28
	v_div_scale_f32 v18, vcc, 1.0, v22, 1.0
	v_mul_f32_e32 v19, v18, v28
	v_fma_f32 v30, -v27, v19, v18
	v_fmac_f32_e32 v19, v30, v28
	v_fma_f32 v18, -v27, v19, v18
	v_div_fmas_f32 v18, v18, v28, v19
	v_div_fixup_f32 v22, v18, v22, 1.0
	v_lshlrev_b32_e32 v27, 16, v33
	v_mul_f32_e32 v19, v23, v22
	v_lshlrev_b32_e32 v23, 16, v29
	v_fma_f32 v27, -v66, v94, v27
	v_fma_f32 v23, -v66, v93, v23
	v_mul_f32_e32 v28, v27, v27
	v_lshlrev_b32_e32 v30, 16, v25
	v_fmac_f32_e32 v28, v23, v23
	v_fma_f32 v30, -v66, v92, v30
	v_fmac_f32_e32 v28, v30, v30
	v_fmac_f32_e32 v28, v31, v31
	ds_bpermute_b32 v32, v47, v28
	v_mul_f32_e32 v19, v41, v19
	v_mul_f32_e32 v19, 0x41800000, v19
	v_add_u32_e32 v18, 9, v36
	v_cvt_pk_fp8_f32 v37, v19, v19
	s_waitcnt lgkmcnt(0)
	v_add_f32_e32 v28, v28, v32
	ds_bpermute_b32 v32, v49, v28
	v_ashrrev_i32_e32 v19, 31, v18
	v_lshlrev_b64 v[18:19], 10, v[18:19]
	v_mul_f32_e32 v26, v26, v22
	v_lshl_add_u64 v[18:19], v[34:35], 0, v[18:19]
	s_waitcnt lgkmcnt(0)
	v_add_f32_e32 v28, v28, v32
	ds_bpermute_b32 v32, v51, v28
	v_mul_f32_e32 v26, v40, v26
	global_store_byte v[18:19], v37, off
	v_mul_f32_e32 v26, 0x41800000, v26
	v_mov_b32_e32 v37, 0
	s_waitcnt lgkmcnt(0)
	v_add_f32_e32 v28, v28, v32
	ds_bpermute_b32 v32, v52, v28
	v_cvt_pk_fp8_f32 v37, v26, v26
	v_mul_f32_e32 v24, v24, v22
	v_mul_f32_e32 v24, v39, v24
	v_mul_f32_e32 v20, v20, v22
	s_waitcnt lgkmcnt(0)
	v_add_f32_e32 v26, v28, v32
	ds_bpermute_b32 v28, v53, v26
	v_mul_f32_e32 v24, 0x41800000, v24
	v_mov_b32_e32 v32, 0
	v_cvt_pk_fp8_f32 v32, v24, v24
	v_mul_f32_e32 v20, v38, v20
	s_waitcnt lgkmcnt(0)
; __device__ __forceinline__ unsigned char f2fp8(float a) { return (unsigned char)(__builtin_amdgcn_cvt_pk_fp8_f32(a, a, 0, false) & 0xff); }
; __device__ __forceinline__ float bf_lo(unsigned w) { return __uint_as_float(w << 16); }
; __device__ __forceinline__ float bf_hi(unsigned w) { return __uint_as_float(w & 0xffff0000u); }
; __device__ __forceinline__ int crow(int r, int hi) { return (r & 3) + 8 * (r >> 2) + 4 * hi; }
; __device__ __forceinline__ void p3_attention(Frame& F) {
;     ...
;         for (int r = 0; r < 16; ++r) {
;             float dd[4], ss = 0.f;
; #pragma unroll
;             for (int d = 0; d < 4; ++d) { const unsigned pw = o1p[d * 2 + (r >> 3)][(r & 7) >> 1]; const float o1 = (r & 1) ? bf_hi(pw) : bf_lo(pw); dd[d] = o1 - lam * o[d][r]; ss += dd[d] * dd[d]; }
;             ss += __shfl_xor(ss, 1); ss += __shfl_xor(ss, 2); ss += __shfl_xor(ss, 4); ss += __shfl_xor(ss, 8); ss += __shfl_xor(ss, 16);
;             const float rs = 1.0f / sqrtf(ss * (1.0f / 128.0f) + RMS_EPS);
;             unsigned char* orow = od + (size_t)attn::crow(r, hi1) * 1024;
; #pragma unroll
;             for (int d = 0; d < 4; ++d) orow[d * 32] = f2fp8(dd[d] * rs * sw[d] * OSCALE);
;         }
	v_add_f32_e32 v22, v26, v28
	v_fmamk_f32 v22, v22, 0x3c000000, v48
	v_mul_f32_e32 v24, 0x4f800000, v22
	v_cmp_gt_f32_e32 vcc, s6, v22
	v_mul_f32_e32 v20, 0x41800000, v20
	v_mov_b32_e32 v26, 0
	v_cndmask_b32_e32 v22, v22, v24, vcc
	v_sqrt_f32_e32 v24, v22
	v_cvt_pk_fp8_f32 v26, v20, v20
	global_store_byte v[18:19], v37, off offset:32
	global_store_byte v[18:19], v32, off offset:64
	global_store_byte v[18:19], v26, off offset:96
	v_add_u32_e32 v20, -1, v24
	v_fma_f32 v28, -v20, v24, v22
	v_cmp_ge_f32_e64 s[4:5], 0, v28
	v_add_u32_e32 v28, 1, v24
	v_and_b32_e32 v25, 0xffff0000, v25
	v_cndmask_b32_e64 v20, v24, v20, s[4:5]
	v_fma_f32 v24, -v28, v24, v22
	v_cmp_lt_f32_e64 s[4:5], 0, v24
	v_fma_f32 v25, -v66, v88, v25
	s_nop 0
	v_cndmask_b32_e64 v20, v20, v28, s[4:5]
	v_mul_f32_e32 v24, 0x37800000, v20
	v_cndmask_b32_e32 v20, v20, v24, vcc
	v_cmp_class_f32_e32 vcc, v22, v54
	v_mov_b32_e32 v28, 0
	s_nop 0
	v_cndmask_b32_e32 v20, v20, v22, vcc
	v_div_scale_f32 v22, s[4:5], v20, v20, 1.0
	v_rcp_f32_e32 v24, v22
	s_nop 0
	v_fma_f32 v18, -v22, v24, 1.0
	v_fmac_f32_e32 v24, v18, v24
	v_div_scale_f32 v18, vcc, 1.0, v20, 1.0
	v_mul_f32_e32 v19, v18, v24
	v_fma_f32 v26, -v22, v19, v18
	v_fmac_f32_e32 v19, v26, v24
	v_fma_f32 v18, -v22, v19, v18
	v_div_fmas_f32 v18, v18, v24, v19
	v_div_fixup_f32 v20, v18, v20, 1.0
	v_mul_f32_e32 v19, v23, v20
	v_and_b32_e32 v23, 0xffff0000, v33
	v_and_b32_e32 v22, 0xffff0000, v29
	v_fma_f32 v23, -v66, v90, v23
	v_fma_f32 v22, -v66, v89, v22
	v_mul_f32_e32 v24, v23, v23
	v_fmac_f32_e32 v24, v22, v22
	v_fmac_f32_e32 v24, v25, v25
	v_fmac_f32_e32 v24, v21, v21
	ds_bpermute_b32 v26, v47, v24
	v_mul_f32_e32 v19, v41, v19
	v_mul_f32_e32 v19, 0x41800000, v19
	v_add_u32_e32 v18, 10, v36
	v_cvt_pk_fp8_f32 v28, v19, v19
	s_waitcnt lgkmcnt(0)
	v_add_f32_e32 v24, v24, v26
	ds_bpermute_b32 v26, v49, v24
	v_ashrrev_i32_e32 v19, 31, v18
	v_lshlrev_b64 v[18:19], 10, v[18:19]
	v_mul_f32_e32 v27, v27, v20
	v_lshl_add_u64 v[18:19], v[34:35], 0, v[18:19]
	s_waitcnt lgkmcnt(0)
	v_add_f32_e32 v24, v24, v26
	ds_bpermute_b32 v26, v51, v24
	v_mul_f32_e32 v27, v40, v27
	global_store_byte v[18:19], v28, off
	v_mul_f32_e32 v27, 0x41800000, v27
	v_mov_b32_e32 v28, 0
	s_waitcnt lgkmcnt(0)
	v_add_f32_e32 v24, v24, v26
	ds_bpermute_b32 v26, v52, v24
	v_cvt_pk_fp8_f32 v28, v27, v27
	v_mul_f32_e32 v27, v30, v20
	v_mul_f32_e32 v27, v39, v27
	v_mul_f32_e32 v20, v31, v20
	s_waitcnt lgkmcnt(0)
	v_add_f32_e32 v24, v24, v26
	ds_bpermute_b32 v26, v53, v24
	v_mul_f32_e32 v27, 0x41800000, v27
	v_mov_b32_e32 v29, 0
	v_mul_f32_e32 v20, v38, v20
	v_cvt_pk_fp8_f32 v29, v27, v27
	s_waitcnt lgkmcnt(0)
	v_add_f32_e32 v24, v24, v26
	v_fmamk_f32 v24, v24, 0x3c000000, v48
	v_mul_f32_e32 v26, 0x4f800000, v24
	v_cmp_gt_f32_e32 vcc, s6, v24
	v_mul_f32_e32 v20, 0x41800000, v20
	v_mov_b32_e32 v27, 0
	v_cndmask_b32_e32 v24, v24, v26, vcc
	v_sqrt_f32_e32 v26, v24
	v_cvt_pk_fp8_f32 v27, v20, v20
	global_store_byte v[18:19], v28, off offset:32
	global_store_byte v[18:19], v29, off offset:64
	global_store_byte v[18:19], v27, off offset:96
	v_add_u32_e32 v20, -1, v26
	v_fma_f32 v30, -v20, v26, v24
	v_cmp_ge_f32_e64 s[4:5], 0, v30
	v_add_u32_e32 v30, 1, v26
	v_lshlrev_b32_e32 v28, 16, v2
	v_cndmask_b32_e64 v20, v26, v20, s[4:5]
	v_fma_f32 v26, -v30, v26, v24
	v_cmp_lt_f32_e64 s[4:5], 0, v26
	v_fma_f32 v28, -v66, v83, v28
	v_and_b32_e32 v2, 0xffff0000, v2
	v_cndmask_b32_e64 v20, v20, v30, s[4:5]
	v_mul_f32_e32 v26, 0x37800000, v20
	v_cndmask_b32_e32 v20, v20, v26, vcc
	v_cmp_class_f32_e32 vcc, v24, v54
	v_mov_b32_e32 v30, 0
	v_fma_f32 v2, -v66, v79, v2
	v_cndmask_b32_e32 v20, v20, v24, vcc
	v_div_scale_f32 v24, s[4:5], v20, v20, 1.0
	v_rcp_f32_e32 v26, v24
	s_nop 0
	v_fma_f32 v18, -v24, v26, 1.0
	v_fmac_f32_e32 v26, v18, v26
	v_div_scale_f32 v18, vcc, 1.0, v20, 1.0
	v_mul_f32_e32 v19, v18, v26
	v_fma_f32 v27, -v24, v19, v18
	v_fmac_f32_e32 v19, v27, v26
	v_fma_f32 v18, -v24, v19, v18
	v_div_fmas_f32 v18, v18, v26, v19
	v_div_fixup_f32 v20, v18, v20, 1.0
	v_lshlrev_b32_e32 v24, 16, v14
	v_mul_f32_e32 v19, v22, v20
	v_lshlrev_b32_e32 v22, 16, v10
	v_fma_f32 v24, -v66, v86, v24
	v_fma_f32 v22, -v66, v85, v22
	v_mul_f32_e32 v26, v24, v24
	v_lshlrev_b32_e32 v27, 16, v6
	v_fmac_f32_e32 v26, v22, v22
	v_fma_f32 v27, -v66, v84, v27
	v_fmac_f32_e32 v26, v27, v27
	v_fmac_f32_e32 v26, v28, v28
	ds_bpermute_b32 v29, v47, v26
	v_mul_f32_e32 v19, v41, v19
	v_mul_f32_e32 v19, 0x41800000, v19
	v_add_u32_e32 v18, 11, v36
	v_cvt_pk_fp8_f32 v30, v19, v19
	s_waitcnt lgkmcnt(0)
	v_add_f32_e32 v26, v26, v29
	ds_bpermute_b32 v29, v49, v26
	v_ashrrev_i32_e32 v19, 31, v18
	v_lshlrev_b64 v[18:19], 10, v[18:19]
	v_mul_f32_e32 v23, v23, v20
	v_lshl_add_u64 v[18:19], v[34:35], 0, v[18:19]
	s_waitcnt lgkmcnt(0)
	v_add_f32_e32 v26, v26, v29
	ds_bpermute_b32 v29, v51, v26
	v_mul_f32_e32 v23, v40, v23
	global_store_byte v[18:19], v30, off
	v_mul_f32_e32 v23, 0x41800000, v23
	v_mov_b32_e32 v30, 0
	s_waitcnt lgkmcnt(0)
	v_add_f32_e32 v26, v26, v29
	ds_bpermute_b32 v29, v52, v26
	v_cvt_pk_fp8_f32 v30, v23, v23
	v_mul_f32_e32 v23, v25, v20
	v_mul_f32_e32 v23, v39, v23
	v_mul_f32_e32 v20, v21, v20
	s_waitcnt lgkmcnt(0)
	v_add_f32_e32 v25, v26, v29
	ds_bpermute_b32 v26, v53, v25
	v_mul_f32_e32 v23, 0x41800000, v23
	v_mov_b32_e32 v29, 0
	v_cvt_pk_fp8_f32 v29, v23, v23
	v_mul_f32_e32 v20, v38, v20
	s_waitcnt lgkmcnt(0)
; __device__ __forceinline__ unsigned char f2fp8(float a) { return (unsigned char)(__builtin_amdgcn_cvt_pk_fp8_f32(a, a, 0, false) & 0xff); }
; __device__ __forceinline__ float bf_lo(unsigned w) { return __uint_as_float(w << 16); }
; __device__ __forceinline__ float bf_hi(unsigned w) { return __uint_as_float(w & 0xffff0000u); }
; __device__ __forceinline__ int crow(int r, int hi) { return (r & 3) + 8 * (r >> 2) + 4 * hi; }
; __device__ __forceinline__ void p3_attention(Frame& F) {
;     ...
;         for (int r = 0; r < 16; ++r) {
;             float dd[4], ss = 0.f;
; #pragma unroll
;             for (int d = 0; d < 4; ++d) { const unsigned pw = o1p[d * 2 + (r >> 3)][(r & 7) >> 1]; const float o1 = (r & 1) ? bf_hi(pw) : bf_lo(pw); dd[d] = o1 - lam * o[d][r]; ss += dd[d] * dd[d]; }
;             ss += __shfl_xor(ss, 1); ss += __shfl_xor(ss, 2); ss += __shfl_xor(ss, 4); ss += __shfl_xor(ss, 8); ss += __shfl_xor(ss, 16);
;             const float rs = 1.0f / sqrtf(ss * (1.0f / 128.0f) + RMS_EPS);
;             unsigned char* orow = od + (size_t)attn::crow(r, hi1) * 1024;
; #pragma unroll
;             for (int d = 0; d < 4; ++d) orow[d * 32] = f2fp8(dd[d] * rs * sw[d] * OSCALE);
;         }
	v_add_f32_e32 v21, v25, v26
	v_fmamk_f32 v21, v21, 0x3c000000, v48
	v_mul_f32_e32 v23, 0x4f800000, v21
	v_cmp_gt_f32_e32 vcc, s6, v21
	v_mul_f32_e32 v20, 0x41800000, v20
	v_mov_b32_e32 v25, 0
	v_cndmask_b32_e32 v21, v21, v23, vcc
	v_sqrt_f32_e32 v23, v21
	v_cvt_pk_fp8_f32 v25, v20, v20
	global_store_byte v[18:19], v30, off offset:32
	global_store_byte v[18:19], v29, off offset:64
	global_store_byte v[18:19], v25, off offset:96
	v_add_u32_e32 v20, -1, v23
	v_fma_f32 v26, -v20, v23, v21
	v_cmp_ge_f32_e64 s[4:5], 0, v26
	v_add_u32_e32 v26, 1, v23
	v_and_b32_e32 v14, 0xffff0000, v14
	v_cndmask_b32_e64 v20, v23, v20, s[4:5]
	v_fma_f32 v23, -v26, v23, v21
	v_cmp_lt_f32_e64 s[4:5], 0, v23
	v_and_b32_e32 v10, 0xffff0000, v10
	v_fma_f32 v14, -v66, v82, v14
	v_cndmask_b32_e64 v20, v20, v26, s[4:5]
	v_mul_f32_e32 v23, 0x37800000, v20
	v_cndmask_b32_e32 v20, v20, v23, vcc
	v_cmp_class_f32_e32 vcc, v21, v54
	v_fma_f32 v10, -v66, v81, v10
	v_and_b32_e32 v6, 0xffff0000, v6
	v_cndmask_b32_e32 v20, v20, v21, vcc
	v_div_scale_f32 v21, s[4:5], v20, v20, 1.0
	v_rcp_f32_e32 v23, v21
	v_fma_f32 v6, -v66, v80, v6
	v_fma_f32 v18, -v21, v23, 1.0
	v_fmac_f32_e32 v23, v18, v23
	v_div_scale_f32 v18, vcc, 1.0, v20, 1.0
	v_mul_f32_e32 v19, v18, v23
	v_fma_f32 v25, -v21, v19, v18
	v_fmac_f32_e32 v19, v25, v23
	v_fma_f32 v18, -v21, v19, v18
	v_mul_f32_e32 v21, v14, v14
	v_fmac_f32_e32 v21, v10, v10
	v_div_fmas_f32 v18, v18, v23, v19
	v_fmac_f32_e32 v21, v6, v6
	v_div_fixup_f32 v20, v18, v20, 1.0
	v_fmac_f32_e32 v21, v2, v2
	v_mul_f32_e32 v19, v22, v20
	ds_bpermute_b32 v22, v47, v21
	v_mul_f32_e32 v19, v41, v19
	v_mul_f32_e32 v19, 0x41800000, v19
	v_mov_b32_e32 v23, 0
	v_add_u32_e32 v18, 16, v36
	s_waitcnt lgkmcnt(0)
	v_add_f32_e32 v21, v21, v22
	ds_bpermute_b32 v22, v49, v21
	v_cvt_pk_fp8_f32 v23, v19, v19
	v_ashrrev_i32_e32 v19, 31, v18
	v_lshlrev_b64 v[18:19], 10, v[18:19]
	v_lshl_add_u64 v[18:19], v[34:35], 0, v[18:19]
	s_waitcnt lgkmcnt(0)
	v_add_f32_e32 v21, v21, v22
	ds_bpermute_b32 v22, v51, v21
	global_store_byte v[18:19], v23, off
	v_mul_f32_e32 v23, v24, v20
	v_mul_f32_e32 v23, v40, v23
	v_mul_f32_e32 v23, 0x41800000, v23
	s_waitcnt lgkmcnt(0)
	v_add_f32_e32 v21, v21, v22
	ds_bpermute_b32 v22, v52, v21
	v_mov_b32_e32 v24, 0
	v_cvt_pk_fp8_f32 v24, v23, v23
	v_mul_f32_e32 v23, v27, v20
	v_mul_f32_e32 v23, v39, v23
	s_waitcnt lgkmcnt(0)
	v_add_f32_e32 v21, v21, v22
	ds_bpermute_b32 v22, v53, v21
	v_mul_f32_e32 v20, v28, v20
	v_mul_f32_e32 v23, 0x41800000, v23
	v_mov_b32_e32 v25, 0
	v_mul_f32_e32 v20, v38, v20
	s_waitcnt lgkmcnt(0)
	v_add_f32_e32 v21, v21, v22
	v_fmamk_f32 v21, v21, 0x3c000000, v48
	v_mul_f32_e32 v22, 0x4f800000, v21
	v_cmp_gt_f32_e32 vcc, s6, v21
	v_cvt_pk_fp8_f32 v25, v23, v23
	v_mul_f32_e32 v20, 0x41800000, v20
	v_cndmask_b32_e32 v21, v21, v22, vcc
	v_sqrt_f32_e32 v22, v21
	v_mov_b32_e32 v23, 0
	v_cvt_pk_fp8_f32 v23, v20, v20
	global_store_byte v[18:19], v24, off offset:32
	global_store_byte v[18:19], v25, off offset:64
	global_store_byte v[18:19], v23, off offset:96
	v_add_u32_e32 v20, -1, v22
	v_fma_f32 v26, -v20, v22, v21
	v_cmp_ge_f32_e64 s[4:5], 0, v26
	v_add_u32_e32 v26, 1, v22
	v_lshlrev_b32_e32 v24, 16, v3
	v_cndmask_b32_e64 v20, v22, v20, s[4:5]
	v_fma_f32 v22, -v26, v22, v21
	v_cmp_lt_f32_e64 s[4:5], 0, v22
	v_fma_f32 v24, -v66, v75, v24
	v_and_b32_e32 v3, 0xffff0000, v3
	v_cndmask_b32_e64 v20, v20, v26, s[4:5]
	v_mul_f32_e32 v22, 0x37800000, v20
	v_cndmask_b32_e32 v20, v20, v22, vcc
	v_cmp_class_f32_e32 vcc, v21, v54
	v_mov_b32_e32 v26, 0
	s_nop 0
	v_cndmask_b32_e32 v20, v20, v21, vcc
	v_div_scale_f32 v21, s[4:5], v20, v20, 1.0
	v_rcp_f32_e32 v22, v21
	s_nop 0
	v_fma_f32 v18, -v21, v22, 1.0
	v_fmac_f32_e32 v22, v18, v22
	v_div_scale_f32 v18, vcc, 1.0, v20, 1.0
	v_mul_f32_e32 v19, v18, v22
	v_fma_f32 v23, -v21, v19, v18
	v_fmac_f32_e32 v19, v23, v22
	v_fma_f32 v18, -v21, v19, v18
	v_div_fmas_f32 v18, v18, v22, v19
	v_lshlrev_b32_e32 v19, 16, v11
	v_fma_f32 v21, -v66, v77, v19
	v_lshlrev_b32_e32 v19, 16, v15
	v_fma_f32 v22, -v66, v78, v19
	v_mul_f32_e32 v19, v22, v22
	v_lshlrev_b32_e32 v23, 16, v7
	v_fmac_f32_e32 v19, v21, v21
	v_fma_f32 v23, -v66, v76, v23
	v_fmac_f32_e32 v19, v23, v23
	v_fmac_f32_e32 v19, v24, v24
	ds_bpermute_b32 v25, v47, v19
	v_div_fixup_f32 v20, v18, v20, 1.0
	v_mul_f32_e32 v10, v10, v20
	v_mul_f32_e32 v10, v41, v10
	v_mul_f32_e32 v10, 0x41800000, v10
	v_cvt_pk_fp8_f32 v26, v10, v10
	s_waitcnt lgkmcnt(0)
	v_add_f32_e32 v10, v19, v25
	ds_bpermute_b32 v25, v49, v10
	v_add_u32_e32 v18, 17, v36
	v_ashrrev_i32_e32 v19, 31, v18
	v_lshlrev_b64 v[18:19], 10, v[18:19]
	v_mul_f32_e32 v14, v14, v20
	s_waitcnt lgkmcnt(0)
	v_add_f32_e32 v10, v10, v25
	ds_bpermute_b32 v25, v51, v10
	v_lshl_add_u64 v[18:19], v[34:35], 0, v[18:19]
	v_mul_f32_e32 v14, v40, v14
	global_store_byte v[18:19], v26, off
	v_mul_f32_e32 v14, 0x41800000, v14
	s_waitcnt lgkmcnt(0)
	v_add_f32_e32 v10, v10, v25
	ds_bpermute_b32 v25, v52, v10
	v_mov_b32_e32 v26, 0
	v_cvt_pk_fp8_f32 v26, v14, v14
	v_mul_f32_e32 v6, v6, v20
	v_mul_f32_e32 v6, v39, v6
	s_waitcnt lgkmcnt(0)
	v_add_f32_e32 v10, v10, v25
	ds_bpermute_b32 v14, v53, v10
	v_mul_f32_e32 v6, 0x41800000, v6
	v_mov_b32_e32 v25, 0
	v_cvt_pk_fp8_f32 v25, v6, v6
	v_mul_f32_e32 v2, v2, v20
	s_waitcnt lgkmcnt(0)
; __device__ __forceinline__ unsigned char f2fp8(float a) { return (unsigned char)(__builtin_amdgcn_cvt_pk_fp8_f32(a, a, 0, false) & 0xff); }
; __device__ __forceinline__ float bf_lo(unsigned w) { return __uint_as_float(w << 16); }
; __device__ __forceinline__ float bf_hi(unsigned w) { return __uint_as_float(w & 0xffff0000u); }
; __device__ __forceinline__ int crow(int r, int hi) { return (r & 3) + 8 * (r >> 2) + 4 * hi; }
; __device__ __forceinline__ void p3_attention(Frame& F) {
;     ...
;         for (int r = 0; r < 16; ++r) {
;             float dd[4], ss = 0.f;
; #pragma unroll
;             for (int d = 0; d < 4; ++d) { const unsigned pw = o1p[d * 2 + (r >> 3)][(r & 7) >> 1]; const float o1 = (r & 1) ? bf_hi(pw) : bf_lo(pw); dd[d] = o1 - lam * o[d][r]; ss += dd[d] * dd[d]; }
;             ss += __shfl_xor(ss, 1); ss += __shfl_xor(ss, 2); ss += __shfl_xor(ss, 4); ss += __shfl_xor(ss, 8); ss += __shfl_xor(ss, 16);
;             const float rs = 1.0f / sqrtf(ss * (1.0f / 128.0f) + RMS_EPS);
;             unsigned char* orow = od + (size_t)attn::crow(r, hi1) * 1024;
; #pragma unroll
;             for (int d = 0; d < 4; ++d) orow[d * 32] = f2fp8(dd[d] * rs * sw[d] * OSCALE);
;         }
	v_add_f32_e32 v6, v10, v14
	v_fmamk_f32 v6, v6, 0x3c000000, v48
	v_mul_f32_e32 v10, 0x4f800000, v6
	v_cmp_gt_f32_e32 vcc, s6, v6
	v_mul_f32_e32 v2, v38, v2
	v_mul_f32_e32 v2, 0x41800000, v2
	v_cndmask_b32_e32 v6, v6, v10, vcc
	v_sqrt_f32_e32 v10, v6
	v_mov_b32_e32 v14, 0
	v_cvt_pk_fp8_f32 v14, v2, v2
	global_store_byte v[18:19], v26, off offset:32
	global_store_byte v[18:19], v25, off offset:64
	global_store_byte v[18:19], v14, off offset:96
	v_add_u32_e32 v2, -1, v10
	v_fma_f32 v20, -v2, v10, v6
	v_cmp_ge_f32_e64 s[4:5], 0, v20
	v_add_u32_e32 v20, 1, v10
	v_and_b32_e32 v11, 0xffff0000, v11
	v_cndmask_b32_e64 v2, v10, v2, s[4:5]
	v_fma_f32 v10, -v20, v10, v6
	v_cmp_lt_f32_e64 s[4:5], 0, v10
	v_fma_f32 v11, -v66, v73, v11
	v_and_b32_e32 v7, 0xffff0000, v7
	v_cndmask_b32_e64 v2, v2, v20, s[4:5]
	v_mul_f32_e32 v10, 0x37800000, v2
	v_cndmask_b32_e32 v2, v2, v10, vcc
	v_cmp_class_f32_e32 vcc, v6, v54
	v_fma_f32 v7, -v66, v72, v7
	v_mov_b32_e32 v20, 0
	v_cndmask_b32_e32 v2, v2, v6, vcc
	v_div_scale_f32 v6, s[4:5], v2, v2, 1.0
	v_rcp_f32_e32 v10, v6
	s_nop 0
	v_fma_f32 v14, -v6, v10, 1.0
	v_fmac_f32_e32 v10, v14, v10
	v_div_scale_f32 v14, vcc, 1.0, v2, 1.0
	v_mul_f32_e32 v18, v14, v10
	v_fma_f32 v19, -v6, v18, v14
	v_fmac_f32_e32 v18, v19, v10
	v_fma_f32 v6, -v6, v18, v14
	v_and_b32_e32 v14, 0xffff0000, v15
	v_fma_f32 v14, -v66, v74, v14
	v_mul_f32_e32 v15, v14, v14
	v_fmac_f32_e32 v15, v11, v11
	v_div_fmas_f32 v6, v6, v10, v18
	v_fmac_f32_e32 v15, v7, v7
	v_fma_f32 v18, -v66, v71, v3
	v_fmac_f32_e32 v15, v18, v18
	ds_bpermute_b32 v3, v47, v15
	v_div_fixup_f32 v6, v6, v2, 1.0
	v_mul_f32_e32 v10, v21, v6
	v_mul_f32_e32 v10, v41, v10
	v_mul_f32_e32 v10, 0x41800000, v10
	v_mov_b32_e32 v19, 0
	v_cvt_pk_fp8_f32 v19, v10, v10
	s_waitcnt lgkmcnt(0)
	v_add_f32_e32 v10, v15, v3
	ds_bpermute_b32 v15, v49, v10
	v_add_u32_e32 v2, 18, v36
	v_ashrrev_i32_e32 v3, 31, v2
	v_lshlrev_b64 v[2:3], 10, v[2:3]
	v_lshl_add_u64 v[2:3], v[34:35], 0, v[2:3]
	s_waitcnt lgkmcnt(0)
	v_add_f32_e32 v10, v10, v15
	ds_bpermute_b32 v15, v51, v10
	global_store_byte v[2:3], v19, off
	v_mul_f32_e32 v19, v22, v6
	v_mul_f32_e32 v19, v40, v19
	v_mul_f32_e32 v19, 0x41800000, v19
	s_waitcnt lgkmcnt(0)
	v_add_f32_e32 v10, v10, v15
	ds_bpermute_b32 v15, v52, v10
	v_cvt_pk_fp8_f32 v20, v19, v19
	v_mul_f32_e32 v19, v23, v6
	v_mul_f32_e32 v19, v39, v19
	v_mul_f32_e32 v6, v24, v6
	s_waitcnt lgkmcnt(0)
	v_add_f32_e32 v10, v10, v15
	ds_bpermute_b32 v15, v53, v10
	v_mul_f32_e32 v19, 0x41800000, v19
	v_mov_b32_e32 v21, 0
	v_mul_f32_e32 v6, v38, v6
	v_cvt_pk_fp8_f32 v21, v19, v19
	s_waitcnt lgkmcnt(0)
	v_add_f32_e32 v10, v10, v15
	v_fmamk_f32 v10, v10, 0x3c000000, v48
	v_mul_f32_e32 v15, 0x4f800000, v10
	v_cmp_gt_f32_e32 vcc, s6, v10
	v_mul_f32_e32 v6, 0x41800000, v6
	v_mov_b32_e32 v19, 0
	v_cndmask_b32_e32 v10, v10, v15, vcc
	v_sqrt_f32_e32 v15, v10
	v_cvt_pk_fp8_f32 v19, v6, v6
	global_store_byte v[2:3], v20, off offset:32
	global_store_byte v[2:3], v21, off offset:64
	global_store_byte v[2:3], v19, off offset:96
	v_add_u32_e32 v6, -1, v15
	v_fma_f32 v22, -v6, v15, v10
	v_cmp_ge_f32_e64 s[4:5], 0, v22
	v_add_u32_e32 v22, 1, v15
	v_lshlrev_b32_e32 v20, 16, v4
	v_cndmask_b32_e64 v6, v15, v6, s[4:5]
	v_fma_f32 v15, -v22, v15, v10
	v_cmp_lt_f32_e64 s[4:5], 0, v15
	v_fma_f32 v20, -v66, v67, v20
	v_and_b32_e32 v4, 0xffff0000, v4
	v_cndmask_b32_e64 v6, v6, v22, s[4:5]
	v_mul_f32_e32 v15, 0x37800000, v6
	v_cndmask_b32_e32 v6, v6, v15, vcc
	v_cmp_class_f32_e32 vcc, v10, v54
	v_mov_b32_e32 v22, 0
	v_fma_f32 v4, -v66, v59, v4
	v_cndmask_b32_e32 v6, v6, v10, vcc
	v_div_scale_f32 v10, s[4:5], v6, v6, 1.0
	v_rcp_f32_e32 v15, v10
	s_nop 0
	v_fma_f32 v2, -v10, v15, 1.0
	v_fmac_f32_e32 v15, v2, v15
	v_div_scale_f32 v2, vcc, 1.0, v6, 1.0
	v_mul_f32_e32 v3, v2, v15
	v_fma_f32 v19, -v10, v3, v2
	v_fmac_f32_e32 v3, v19, v15
	v_fma_f32 v2, -v10, v3, v2
	v_div_fmas_f32 v2, v2, v15, v3
	v_div_fixup_f32 v6, v2, v6, 1.0
	v_mul_f32_e32 v3, v11, v6
	v_lshlrev_b32_e32 v11, 16, v16
	v_lshlrev_b32_e32 v10, 16, v12
	v_fma_f32 v11, -v66, v70, v11
	v_fma_f32 v10, -v66, v69, v10
	v_mul_f32_e32 v15, v11, v11
	v_lshlrev_b32_e32 v19, 16, v8
	v_fmac_f32_e32 v15, v10, v10
	v_fma_f32 v19, -v66, v68, v19
	v_fmac_f32_e32 v15, v19, v19
	v_fmac_f32_e32 v15, v20, v20
	ds_bpermute_b32 v21, v47, v15
	v_mul_f32_e32 v3, v41, v3
	v_mul_f32_e32 v3, 0x41800000, v3
	v_add_u32_e32 v2, 19, v36
	v_cvt_pk_fp8_f32 v22, v3, v3
	s_waitcnt lgkmcnt(0)
	v_add_f32_e32 v15, v15, v21
	ds_bpermute_b32 v21, v49, v15
	v_ashrrev_i32_e32 v3, 31, v2
	v_lshlrev_b64 v[2:3], 10, v[2:3]
	v_mul_f32_e32 v14, v14, v6
	v_lshl_add_u64 v[2:3], v[34:35], 0, v[2:3]
	s_waitcnt lgkmcnt(0)
	v_add_f32_e32 v15, v15, v21
	ds_bpermute_b32 v21, v51, v15
	v_mul_f32_e32 v14, v40, v14
	global_store_byte v[2:3], v22, off
	v_mul_f32_e32 v14, 0x41800000, v14
	v_mov_b32_e32 v22, 0
	s_waitcnt lgkmcnt(0)
	v_add_f32_e32 v15, v15, v21
	ds_bpermute_b32 v21, v52, v15
	v_cvt_pk_fp8_f32 v22, v14, v14
	v_mul_f32_e32 v7, v7, v6
	v_mul_f32_e32 v7, v39, v7
	v_mul_f32_e32 v7, 0x41800000, v7
	s_waitcnt lgkmcnt(0)
	v_add_f32_e32 v14, v15, v21
	ds_bpermute_b32 v15, v53, v14
	v_mov_b32_e32 v21, 0
	v_cvt_pk_fp8_f32 v21, v7, v7
	v_mul_f32_e32 v6, v18, v6
	v_mul_f32_e32 v6, v38, v6
	s_waitcnt lgkmcnt(0)
; __device__ __forceinline__ unsigned char f2fp8(float a) { return (unsigned char)(__builtin_amdgcn_cvt_pk_fp8_f32(a, a, 0, false) & 0xff); }
; __device__ __forceinline__ float bf_lo(unsigned w) { return __uint_as_float(w << 16); }
; __device__ __forceinline__ float bf_hi(unsigned w) { return __uint_as_float(w & 0xffff0000u); }
; __device__ __forceinline__ int crow(int r, int hi) { return (r & 3) + 8 * (r >> 2) + 4 * hi; }
; __device__ __forceinline__ void p3_attention(Frame& F) {
;     ...
;         for (int r = 0; r < 16; ++r) {
;             float dd[4], ss = 0.f;
; #pragma unroll
;             for (int d = 0; d < 4; ++d) { const unsigned pw = o1p[d * 2 + (r >> 3)][(r & 7) >> 1]; const float o1 = (r & 1) ? bf_hi(pw) : bf_lo(pw); dd[d] = o1 - lam * o[d][r]; ss += dd[d] * dd[d]; }
;             ss += __shfl_xor(ss, 1); ss += __shfl_xor(ss, 2); ss += __shfl_xor(ss, 4); ss += __shfl_xor(ss, 8); ss += __shfl_xor(ss, 16);
;             const float rs = 1.0f / sqrtf(ss * (1.0f / 128.0f) + RMS_EPS);
;             unsigned char* orow = od + (size_t)attn::crow(r, hi1) * 1024;
; #pragma unroll
;             for (int d = 0; d < 4; ++d) orow[d * 32] = f2fp8(dd[d] * rs * sw[d] * OSCALE);
;         }
	v_add_f32_e32 v7, v14, v15
	v_fmamk_f32 v7, v7, 0x3c000000, v48
	v_mul_f32_e32 v14, 0x4f800000, v7
	v_cmp_gt_f32_e32 vcc, s6, v7
	v_mul_f32_e32 v6, 0x41800000, v6
	v_mov_b32_e32 v15, 0
	v_cndmask_b32_e32 v7, v7, v14, vcc
	v_sqrt_f32_e32 v14, v7
	v_cvt_pk_fp8_f32 v15, v6, v6
	global_store_byte v[2:3], v22, off offset:32
	global_store_byte v[2:3], v21, off offset:64
	global_store_byte v[2:3], v15, off offset:96
	v_add_u32_e32 v6, -1, v14
	v_fma_f32 v18, -v6, v14, v7
	v_cmp_ge_f32_e64 s[4:5], 0, v18
	v_add_u32_e32 v18, 1, v14
	v_and_b32_e32 v8, 0xffff0000, v8
	v_cndmask_b32_e64 v6, v14, v6, s[4:5]
	v_fma_f32 v14, -v18, v14, v7
	v_cmp_lt_f32_e64 s[4:5], 0, v14
	v_fma_f32 v8, -v66, v60, v8
	s_nop 0
	v_cndmask_b32_e64 v6, v6, v18, s[4:5]
	v_mul_f32_e32 v14, 0x37800000, v6
	v_cndmask_b32_e32 v6, v6, v14, vcc
	v_cmp_class_f32_e32 vcc, v7, v54
	s_nop 1
	v_cndmask_b32_e32 v6, v6, v7, vcc
	v_div_scale_f32 v7, s[4:5], v6, v6, 1.0
	v_rcp_f32_e32 v14, v7
	s_nop 0
	v_fma_f32 v2, -v7, v14, 1.0
	v_fmac_f32_e32 v14, v2, v14
	v_div_scale_f32 v2, vcc, 1.0, v6, 1.0
	v_mul_f32_e32 v3, v2, v14
	v_fma_f32 v15, -v7, v3, v2
	v_fmac_f32_e32 v3, v15, v14
	v_fma_f32 v2, -v7, v3, v2
	v_div_fmas_f32 v2, v2, v14, v3
	v_div_fixup_f32 v6, v2, v6, 1.0
	v_mul_f32_e32 v3, v10, v6
	v_and_b32_e32 v10, 0xffff0000, v16
	v_and_b32_e32 v7, 0xffff0000, v12
	v_fma_f32 v10, -v66, v62, v10
	v_fma_f32 v7, -v66, v61, v7
	v_mul_f32_e32 v12, v10, v10
	v_fmac_f32_e32 v12, v7, v7
	v_fmac_f32_e32 v12, v8, v8
	v_fmac_f32_e32 v12, v4, v4
	ds_bpermute_b32 v14, v47, v12
	v_mul_f32_e32 v3, v41, v3
	v_mul_f32_e32 v3, 0x41800000, v3
	v_mov_b32_e32 v15, 0
	v_add_u32_e32 v2, 24, v36
	s_waitcnt lgkmcnt(0)
	v_add_f32_e32 v12, v12, v14
	ds_bpermute_b32 v14, v49, v12
	v_cvt_pk_fp8_f32 v15, v3, v3
	v_ashrrev_i32_e32 v3, 31, v2
	v_lshlrev_b64 v[2:3], 10, v[2:3]
	v_mul_f32_e32 v11, v11, v6
	s_waitcnt lgkmcnt(0)
	v_add_f32_e32 v12, v12, v14
	ds_bpermute_b32 v14, v51, v12
	v_lshl_add_u64 v[2:3], v[34:35], 0, v[2:3]
	v_mul_f32_e32 v11, v40, v11
	global_store_byte v[2:3], v15, off
	v_mul_f32_e32 v11, 0x41800000, v11
	s_waitcnt lgkmcnt(0)
	v_add_f32_e32 v12, v12, v14
	ds_bpermute_b32 v14, v52, v12
	v_mov_b32_e32 v15, 0
	v_cvt_pk_fp8_f32 v15, v11, v11
	v_mul_f32_e32 v11, v19, v6
	v_mul_f32_e32 v11, v39, v11
	s_waitcnt lgkmcnt(0)
	v_add_f32_e32 v12, v12, v14
	ds_bpermute_b32 v14, v53, v12
	v_mul_f32_e32 v11, 0x41800000, v11
	v_mov_b32_e32 v16, 0
	v_cvt_pk_fp8_f32 v16, v11, v11
	v_mul_f32_e32 v6, v20, v6
	s_waitcnt lgkmcnt(0)
	v_add_f32_e32 v11, v12, v14
	v_fmamk_f32 v11, v11, 0x3c000000, v48
	v_mul_f32_e32 v12, 0x4f800000, v11
	v_cmp_gt_f32_e32 vcc, s6, v11
	v_mul_f32_e32 v6, v38, v6
	v_mul_f32_e32 v6, 0x41800000, v6
	v_cndmask_b32_e32 v11, v11, v12, vcc
	v_sqrt_f32_e32 v12, v11
	v_mov_b32_e32 v14, 0
	v_cvt_pk_fp8_f32 v14, v6, v6
	global_store_byte v[2:3], v15, off offset:32
	global_store_byte v[2:3], v16, off offset:64
	global_store_byte v[2:3], v14, off offset:96
	v_add_u32_e32 v6, -1, v12
	v_fma_f32 v18, -v6, v12, v11
	v_cmp_ge_f32_e64 s[4:5], 0, v18
	v_add_u32_e32 v18, 1, v12
	v_lshlrev_b32_e32 v15, 16, v5
	v_cndmask_b32_e64 v6, v12, v6, s[4:5]
	v_fma_f32 v12, -v18, v12, v11
	v_cmp_lt_f32_e64 s[4:5], 0, v12
	v_fma_f32 v15, -v66, v55, v15
	v_and_b32_e32 v5, 0xffff0000, v5
	v_cndmask_b32_e64 v6, v6, v18, s[4:5]
	v_mul_f32_e32 v12, 0x37800000, v6
	v_cndmask_b32_e32 v6, v6, v12, vcc
	v_cmp_class_f32_e32 vcc, v11, v54
	v_mov_b32_e32 v18, 0
	v_fma_f32 v5, -v66, v42, v5
	v_cndmask_b32_e32 v6, v6, v11, vcc
	v_div_scale_f32 v11, s[4:5], v6, v6, 1.0
	v_rcp_f32_e32 v12, v11
	s_nop 0
	v_fma_f32 v2, -v11, v12, 1.0
	v_fmac_f32_e32 v12, v2, v12
	v_div_scale_f32 v2, vcc, 1.0, v6, 1.0
	v_mul_f32_e32 v3, v2, v12
	v_fma_f32 v14, -v11, v3, v2
	v_fmac_f32_e32 v3, v14, v12
	v_fma_f32 v2, -v11, v3, v2
	v_div_fmas_f32 v2, v2, v12, v3
	v_div_fixup_f32 v6, v2, v6, 1.0
	v_lshlrev_b32_e32 v11, 16, v17
	v_mul_f32_e32 v3, v7, v6
	v_lshlrev_b32_e32 v7, 16, v13
	v_fma_f32 v11, -v66, v58, v11
	v_fma_f32 v7, -v66, v57, v7
	v_mul_f32_e32 v12, v11, v11
	v_lshlrev_b32_e32 v14, 16, v9
	v_fmac_f32_e32 v12, v7, v7
	v_fma_f32 v14, -v66, v56, v14
	v_fmac_f32_e32 v12, v14, v14
	v_fmac_f32_e32 v12, v15, v15
	ds_bpermute_b32 v16, v47, v12
	v_mul_f32_e32 v3, v41, v3
	v_mul_f32_e32 v3, 0x41800000, v3
	v_add_u32_e32 v2, 25, v36
	v_cvt_pk_fp8_f32 v18, v3, v3
	s_waitcnt lgkmcnt(0)
	v_add_f32_e32 v12, v12, v16
	ds_bpermute_b32 v16, v49, v12
	v_ashrrev_i32_e32 v3, 31, v2
	v_lshlrev_b64 v[2:3], 10, v[2:3]
	v_mul_f32_e32 v10, v10, v6
	v_lshl_add_u64 v[2:3], v[34:35], 0, v[2:3]
	s_waitcnt lgkmcnt(0)
	v_add_f32_e32 v12, v12, v16
	ds_bpermute_b32 v16, v51, v12
	v_mul_f32_e32 v10, v40, v10
	global_store_byte v[2:3], v18, off
	v_mul_f32_e32 v10, 0x41800000, v10
	v_mov_b32_e32 v18, 0
	s_waitcnt lgkmcnt(0)
	v_add_f32_e32 v12, v12, v16
	ds_bpermute_b32 v16, v52, v12
	v_cvt_pk_fp8_f32 v18, v10, v10
	v_mul_f32_e32 v8, v8, v6
	v_mul_f32_e32 v8, v39, v8
	v_mul_f32_e32 v4, v4, v6
	s_waitcnt lgkmcnt(0)
; __device__ __forceinline__ unsigned char f2fp8(float a) { return (unsigned char)(__builtin_amdgcn_cvt_pk_fp8_f32(a, a, 0, false) & 0xff); }
; __device__ __forceinline__ float bf_lo(unsigned w) { return __uint_as_float(w << 16); }
; __device__ __forceinline__ float bf_hi(unsigned w) { return __uint_as_float(w & 0xffff0000u); }
; __device__ __forceinline__ int crow(int r, int hi) { return (r & 3) + 8 * (r >> 2) + 4 * hi; }
; __device__ __forceinline__ void p3_attention(Frame& F) {
;     ...
;         for (int r = 0; r < 16; ++r) {
;             float dd[4], ss = 0.f;
; #pragma unroll
;             for (int d = 0; d < 4; ++d) { const unsigned pw = o1p[d * 2 + (r >> 3)][(r & 7) >> 1]; const float o1 = (r & 1) ? bf_hi(pw) : bf_lo(pw); dd[d] = o1 - lam * o[d][r]; ss += dd[d] * dd[d]; }
;             ss += __shfl_xor(ss, 1); ss += __shfl_xor(ss, 2); ss += __shfl_xor(ss, 4); ss += __shfl_xor(ss, 8); ss += __shfl_xor(ss, 16);
;             const float rs = 1.0f / sqrtf(ss * (1.0f / 128.0f) + RMS_EPS);
;             unsigned char* orow = od + (size_t)attn::crow(r, hi1) * 1024;
; #pragma unroll
;             for (int d = 0; d < 4; ++d) orow[d * 32] = f2fp8(dd[d] * rs * sw[d] * OSCALE);
;         }
;     ...
;         const int g4 = qb, kr0 = (4 * g4 - 4) < 0 ? 0 : ((4 * g4 - 4) > 52 ? 52 : 4 * g4 - 4);
	v_add_f32_e32 v10, v12, v16
	ds_bpermute_b32 v12, v53, v10
	v_mul_f32_e32 v8, 0x41800000, v8
	v_mov_b32_e32 v16, 0
	v_cvt_pk_fp8_f32 v16, v8, v8
	v_mul_f32_e32 v4, v38, v4
	s_waitcnt lgkmcnt(0)
	v_add_f32_e32 v6, v10, v12
	v_fmamk_f32 v6, v6, 0x3c000000, v48
	v_mul_f32_e32 v8, 0x4f800000, v6
	v_cmp_gt_f32_e32 vcc, s6, v6
	v_mul_f32_e32 v4, 0x41800000, v4
	v_mov_b32_e32 v10, 0
	v_cndmask_b32_e32 v6, v6, v8, vcc
	v_sqrt_f32_e32 v8, v6
	v_cvt_pk_fp8_f32 v10, v4, v4
	global_store_byte v[2:3], v18, off offset:32
	global_store_byte v[2:3], v16, off offset:64
	global_store_byte v[2:3], v10, off offset:96
	v_add_u32_e32 v4, -1, v8
	v_fma_f32 v12, -v4, v8, v6
	v_cmp_ge_f32_e64 s[4:5], 0, v12
	v_add_u32_e32 v12, 1, v8
	v_and_b32_e32 v9, 0xffff0000, v9
	v_cndmask_b32_e64 v4, v8, v4, s[4:5]
	v_fma_f32 v8, -v12, v8, v6
	v_cmp_lt_f32_e64 s[4:5], 0, v8
	v_fma_f32 v9, -v66, v43, v9
	s_nop 0
	v_cndmask_b32_e64 v4, v4, v12, s[4:5]
	v_mul_f32_e32 v8, 0x37800000, v4
	v_cndmask_b32_e32 v4, v4, v8, vcc
	v_cmp_class_f32_e32 vcc, v6, v54
	v_mov_b32_e32 v12, 0
	s_nop 0
	v_cndmask_b32_e32 v4, v4, v6, vcc
	v_div_scale_f32 v6, s[4:5], v4, v4, 1.0
	v_rcp_f32_e32 v8, v6
	s_nop 0
	v_fma_f32 v2, -v6, v8, 1.0
	v_fmac_f32_e32 v8, v2, v8
	v_div_scale_f32 v2, vcc, 1.0, v4, 1.0
	v_mul_f32_e32 v3, v2, v8
	v_fma_f32 v10, -v6, v3, v2
	v_fmac_f32_e32 v3, v10, v8
	v_fma_f32 v2, -v6, v3, v2
	v_div_fmas_f32 v2, v2, v8, v3
	v_div_fixup_f32 v4, v2, v4, 1.0
	v_mul_f32_e32 v3, v7, v4
	v_and_b32_e32 v7, 0xffff0000, v17
	v_and_b32_e32 v6, 0xffff0000, v13
	v_fma_f32 v7, -v66, v44, v7
	v_fma_f32 v6, -v66, v45, v6
	v_mul_f32_e32 v8, v7, v7
	v_fmac_f32_e32 v8, v6, v6
	v_fmac_f32_e32 v8, v9, v9
	v_fmac_f32_e32 v8, v5, v5
	ds_bpermute_b32 v10, v47, v8
	v_mul_f32_e32 v3, v41, v3
	v_mul_f32_e32 v3, 0x41800000, v3
	v_add_u32_e32 v2, 26, v36
	v_cvt_pk_fp8_f32 v12, v3, v3
	s_waitcnt lgkmcnt(0)
	v_add_f32_e32 v8, v8, v10
	ds_bpermute_b32 v10, v49, v8
	v_ashrrev_i32_e32 v3, 31, v2
	v_lshlrev_b64 v[2:3], 10, v[2:3]
	v_mul_f32_e32 v11, v11, v4
	v_lshl_add_u64 v[2:3], v[34:35], 0, v[2:3]
	s_waitcnt lgkmcnt(0)
	v_add_f32_e32 v8, v8, v10
	ds_bpermute_b32 v10, v51, v8
	v_mul_f32_e32 v11, v40, v11
	global_store_byte v[2:3], v12, off
	v_mul_f32_e32 v11, 0x41800000, v11
	v_mov_b32_e32 v12, 0
	s_waitcnt lgkmcnt(0)
	v_add_f32_e32 v8, v8, v10
	ds_bpermute_b32 v10, v52, v8
	v_cvt_pk_fp8_f32 v12, v11, v11
	v_mul_f32_e32 v11, v14, v4
	v_mul_f32_e32 v11, v39, v11
	v_mul_f32_e32 v4, v15, v4
	s_waitcnt lgkmcnt(0)
	v_add_f32_e32 v8, v8, v10
	ds_bpermute_b32 v10, v53, v8
	v_mul_f32_e32 v11, 0x41800000, v11
	v_mov_b32_e32 v13, 0
	v_mul_f32_e32 v4, v38, v4
	v_cvt_pk_fp8_f32 v13, v11, v11
	s_waitcnt lgkmcnt(0)
	v_add_f32_e32 v8, v8, v10
	v_fmac_f32_e32 v48, 0x3c000000, v8
	v_mul_f32_e32 v8, 0x4f800000, v48
	v_cmp_gt_f32_e32 vcc, s6, v48
	v_mul_f32_e32 v4, 0x41800000, v4
	v_mov_b32_e32 v11, 0
	v_cndmask_b32_e32 v8, v48, v8, vcc
	v_sqrt_f32_e32 v10, v8
	v_cvt_pk_fp8_f32 v11, v4, v4
	global_store_byte v[2:3], v12, off offset:32
	global_store_byte v[2:3], v13, off offset:64
	global_store_byte v[2:3], v11, off offset:96
	v_add_u32_e32 v4, -1, v10
	v_fma_f32 v14, -v4, v10, v8
	v_cmp_ge_f32_e64 s[4:5], 0, v14
	v_add_u32_e32 v14, 1, v10
	s_nop 0
	v_cndmask_b32_e64 v4, v10, v4, s[4:5]
	v_fma_f32 v10, -v14, v10, v8
	v_cmp_lt_f32_e64 s[4:5], 0, v10
	s_nop 1
	v_cndmask_b32_e64 v4, v4, v14, s[4:5]
	v_mul_f32_e32 v10, 0x37800000, v4
	v_cndmask_b32_e32 v4, v4, v10, vcc
	v_cmp_class_f32_e32 vcc, v8, v54
	s_nop 1
	v_cndmask_b32_e32 v4, v4, v8, vcc
	v_div_scale_f32 v8, s[4:5], v4, v4, 1.0
	v_rcp_f32_e32 v10, v8
	s_mov_b64 s[4:5], -1
	v_fma_f32 v2, -v8, v10, 1.0
	v_fmac_f32_e32 v10, v2, v10
	v_div_scale_f32 v2, vcc, 1.0, v4, 1.0
	v_mul_f32_e32 v3, v2, v10
	v_fma_f32 v11, -v8, v3, v2
	v_fmac_f32_e32 v3, v11, v10
	v_fma_f32 v2, -v8, v3, v2
	v_div_fmas_f32 v2, v2, v10, v3
	v_div_fixup_f32 v4, v2, v4, 1.0
	v_mul_f32_e32 v6, v6, v4
	v_mul_f32_e32 v6, v41, v6
	v_mul_f32_e32 v6, 0x41800000, v6
	v_mov_b32_e32 v8, 0
	v_cvt_pk_fp8_f32 v8, v6, v6
	v_mul_f32_e32 v6, v7, v4
	v_mul_f32_e32 v6, v40, v6
	v_mul_f32_e32 v6, 0x41800000, v6
	v_mov_b32_e32 v7, 0
	v_cvt_pk_fp8_f32 v7, v6, v6
	v_mul_f32_e32 v6, v9, v4
	v_add_u32_e32 v2, 27, v36
	v_mul_f32_e32 v6, v39, v6
	v_mul_f32_e32 v4, v5, v4
	v_ashrrev_i32_e32 v3, 31, v2
	v_mul_f32_e32 v6, 0x41800000, v6
	v_mov_b32_e32 v9, 0
	v_mul_f32_e32 v4, v38, v4
	v_lshlrev_b64 v[2:3], 10, v[2:3]
	v_cvt_pk_fp8_f32 v9, v6, v6
	v_mul_f32_e32 v4, 0x41800000, v4
	v_lshl_add_u64 v[2:3], v[34:35], 0, v[2:3]
	v_cvt_pk_fp8_f32 v46, v4, v4
	global_store_byte v[2:3], v8, off
	global_store_byte v[2:3], v7, off offset:32
	global_store_byte v[2:3], v9, off offset:64
	global_store_byte v[2:3], v46, off offset:96
	s_cbranch_scc0 .LBB0_452
	s_lshl_b32 s21, s55, 2
	s_mov_b32 s57, 52
	s_cbranch_execz .LBB0_453

; #define LAS __attribute__((address_space(3)))
; __device__ __forceinline__ void finishSM(f32x16& p0, f32x16& p1, float alpha, float& l_reg, bf16x8& pa0, bf16x8& pa1, bf16x8& pa2, bf16x8& pa3) {
; #pragma unroll
;     for (int r = 0; r < 16; ++r) p1[r] = __builtin_amdgcn_exp2f(p1[r]);
;     float ps = 0;
; #pragma unroll
;     for (int r = 0; r < 16; ++r) ps += p0[r];
; #pragma unroll
;     for (int r = 0; r < 16; ++r) ps += p1[r];
;     { auto rr = __builtin_amdgcn_permlane32_swap(__float_as_uint(ps), __float_as_uint(ps), false, false);
;       ps = __uint_as_float(rr[0]) + __uint_as_float(rr[1]); }
;     l_reg = l_reg * alpha + ps;
;     ...
;     PK4(p0, 0, pa0); PK4(p0, 8, pa1); PK4(p1, 0, pa2); PK4(p1, 8, pa3);
;     ...
; }
; template <int MODE>
; __device__ __forceinline__ void qkt(f32x16& p0, f32x16& p1, const LAS unsigned char* Ks, const bf16x8* qr, const LAS unsigned char* Qs, int r32, int hi, int cbase) {
;     p0 = f32x16{}; p1 = f32x16{};
; #pragma unroll
;     for (int d0 = 0; d0 < Cfg<MODE>::ND; ++d0) { const int cb = cbase + (d0 * 16 + hi * 8) * 2;
;         const bf16x8 b0 = *(const LAS bf16x8*)(Ks + KSWZ(r32, cb));
;         const bf16x8 b1 = *(const LAS bf16x8*)(Ks + KSWZ(32 + r32, cb));
;         bf16x8 q; if constexpr (MODE == 0) q = *(const LAS bf16x8*)(Qs + KSWZ(r32, cb)); else q = qr[d0];
;         p0 = __builtin_amdgcn_mfma_f32_32x32x16_bf16(b0, q, p0, 0, 0, 0);
;         p1 = __builtin_amdgcn_mfma_f32_32x32x16_bf16(b1, q, p1, 0, 0, 0); }
; }
; __device__ __forceinline__ int v_st(int k, int c) { const int kk = (k & ~0xC) | ((k & 4) << 1) | ((k & 8) >> 1); return ((kk >> 3) * 4 + (c >> 5)) * 512 + ((kk & 7) * 32 + (c & 31)) * 2; }
; __device__ __forceinline__ int v_rd_base(int lane) { return ((lane & 3) << 3) | (((lane >> 2) & 3) << 6) | (((lane >> 4) & 1) << 5) | (((lane >> 5) & 1) << 8); }
; template <int OFF> __device__ __forceinline__ s16x4 tr_read(int vb) {
;     s16x4 r; asm volatile("ds_read_b64_tr_b16 %0, %1 offset:%2" : "=&v"(r) : "v"(vb), "i"(OFF) : "memory"); return r;
; }
; template <int D0> __device__ __forceinline__ void pv_one(f32x16& od, int vb, bf16x8 pa0, bf16x8 pa1, bf16x8 pa2, bf16x8 pa3) {
;     const s16x4 l0 = tr_read<v_rd_off(D0, 0, 0)>(vb), h0 = tr_read<v_rd_off(D0, 0, 1)>(vb), l1 = tr_read<v_rd_off(D0, 1, 0)>(vb), h1 = tr_read<v_rd_off(D0, 1, 1)>(vb);
.LBB0_465:
	v_add_f32_e32 v68, 0, v234
	v_add_f32_e32 v68, v236, v68
	v_add_f32_e32 v68, v232, v68
	v_add_f32_e32 v68, v235, v68
	v_add_f32_e32 v68, v230, v68
	v_add_f32_e32 v68, v233, v68
	v_add_f32_e32 v68, v229, v68
	v_add_f32_e32 v68, v231, v68
	v_add_f32_e32 v68, v226, v68
	v_add_f32_e32 v68, v228, v68
	v_add_f32_e32 v68, v168, v68
	v_add_f32_e32 v68, v227, v68
	v_exp_f32_e32 v67, v156
	v_add_f32_e32 v68, v166, v68
	v_exp_f32_e32 v72, v157
	v_add_f32_e32 v68, v169, v68
	v_exp_f32_e32 v75, v154
	v_add_f32_e32 v68, v165, v68
	v_exp_f32_e32 v80, v155
	v_add_f32_e32 v68, v167, v68
	v_exp_f32_e32 v100, v152
	v_add_f32_e32 v68, v67, v68
	v_exp_f32_e32 v101, v153
	v_add_f32_e32 v68, v72, v68
	v_exp_f32_e32 v102, v150
	v_add_f32_e32 v68, v75, v68
	v_exp_f32_e32 v103, v151
	v_add_f32_e32 v68, v80, v68
	v_exp_f32_e32 v104, v148
	v_add_f32_e32 v68, v100, v68
	v_exp_f32_e32 v105, v149
	v_add_f32_e32 v68, v101, v68
	v_exp_f32_e32 v106, v146
	v_add_f32_e32 v68, v102, v68
	v_exp_f32_e32 v107, v147
	v_add_f32_e32 v68, v103, v68
	v_exp_f32_e32 v108, v162
	v_add_f32_e32 v68, v104, v68
	v_exp_f32_e32 v109, v163
	v_add_f32_e32 v68, v105, v68
	v_exp_f32_e32 v110, v160
	v_add_f32_e32 v68, v106, v68
	v_exp_f32_e32 v111, v161
	v_add_f32_e32 v68, v107, v68
	v_add_f32_e32 v68, v108, v68
	v_add_f32_e32 v68, v109, v68
	v_add_f32_e32 v68, v110, v68
	v_add_f32_e32 v113, v111, v68
	v_mov_b32_e32 v224, v113
	s_nop 1
	v_permlane32_swap_b32_e32 v113, v224
	v_cvt_pk_bf16_f32 v68, v234, v236
	v_cvt_pk_bf16_f32 v69, v232, v235
	v_cvt_pk_bf16_f32 v70, v230, v233
	v_cvt_pk_bf16_f32 v71, v229, v231
	v_cvt_pk_bf16_f32 v76, v226, v228
	v_cvt_pk_bf16_f32 v77, v168, v227
	v_cvt_pk_bf16_f32 v78, v166, v169
	v_cvt_pk_bf16_f32 v79, v165, v167
	v_cvt_pk_bf16_f32 v98, v67, v72
	v_cvt_pk_bf16_f32 v99, v75, v80
	v_cvt_pk_bf16_f32 v100, v100, v101
	v_cvt_pk_bf16_f32 v101, v102, v103
	v_cvt_pk_bf16_f32 v102, v104, v105
	v_cvt_pk_bf16_f32 v103, v106, v107
	v_cvt_pk_bf16_f32 v104, v108, v109
	v_cvt_pk_bf16_f32 v105, v110, v111
	s_nop 0
	v_permlane32_swap_b32_e32 v68, v70
	v_permlane32_swap_b32_e32 v69, v71
	v_permlane32_swap_b32_e32 v76, v78
	v_permlane32_swap_b32_e32 v77, v79
	v_permlane32_swap_b32_e32 v98, v100
	v_permlane32_swap_b32_e32 v99, v101
	v_permlane32_swap_b32_e32 v102, v104
	v_permlane32_swap_b32_e32 v103, v105
	s_cmp_gt_u32 s6, 1
	s_cselect_b32 s4, s3, 0x10c0
	s_ashr_i32 s5, s4, 31
	v_mov_b32_e32 v107, s5
	v_or_b32_e32 v106, s4, v174
	v_lshlrev_b64 v[106:107], 11, v[106:107]
	v_lshl_add_u64 v[110:111], v[176:177], 0, s[4:5]
	v_or_b32_e32 v106, v106, v190
	v_lshlrev_b64 v[110:111], 11, v[110:111]
	v_lshl_add_u64 v[108:109], s[38:39], 0, v[106:107]
	v_or_b32_e32 v110, v110, v190
	v_lshl_add_u64 v[106:107], s[24:25], 0, v[106:107]
	v_lshl_add_u64 v[114:115], s[38:39], 0, v[110:111]
	global_load_dwordx4 v[146:149], v[108:109], off
	global_load_dwordx4 v[150:153], v[114:115], off
	v_lshl_add_u64 v[108:109], s[24:25], 0, v[110:111]
	global_load_dwordx4 v[154:157], v[106:107], off
	global_load_dwordx4 v[158:161], v[108:109], off
	ds_read_b64_tr_b16 v[106:107], v175 offset:0
	ds_read_b64_tr_b16 v[108:109], v175 offset:0x800
	ds_read_b64_tr_b16 v[114:115], v175 offset:0x1000
	ds_read_b64_tr_b16 v[116:117], v175 offset:0x1800
	ds_read_b64_tr_b16 v[118:119], v175 offset:0x2000
	ds_read_b64_tr_b16 v[120:121], v175 offset:0x2800
	ds_read_b64_tr_b16 v[122:123], v175 offset:0x3000
	ds_read_b64_tr_b16 v[124:125], v175 offset:0x3800
	s_waitcnt lgkmcnt(0)
	s_nop 0
	v_mfma_f32_32x32x16_bf16 v[2:17], v[68:71], v[106:109], v[2:17]
	ds_read_b64_tr_b16 v[106:107], v175 offset:0x200
	ds_read_b64_tr_b16 v[108:109], v175 offset:0xa00
	v_mfma_f32_32x32x16_bf16 v[2:17], v[76:79], v[114:117], v[2:17]
	ds_read_b64_tr_b16 v[114:115], v175 offset:0x1200
	ds_read_b64_tr_b16 v[116:117], v175 offset:0x1a00
	v_mfma_f32_32x32x16_bf16 v[2:17], v[98:101], v[118:121], v[2:17]
	ds_read_b64_tr_b16 v[118:119], v175 offset:0x2200
	ds_read_b64_tr_b16 v[120:121], v175 offset:0x2a00
	ds_read_b64_tr_b16 v[126:127], v175 offset:0x3200
	ds_read_b64_tr_b16 v[128:129], v175 offset:0x3a00
	v_mfma_f32_32x32x16_bf16 v[2:17], v[102:105], v[122:125], v[2:17]
	s_waitcnt lgkmcnt(0)
	v_mfma_f32_32x32x16_bf16 v[50:65], v[68:71], v[106:109], v[50:65]
	ds_read_b64_tr_b16 v[106:107], v175 offset:0x400
	ds_read_b64_tr_b16 v[108:109], v175 offset:0xc00
	v_mfma_f32_32x32x16_bf16 v[50:65], v[76:79], v[114:117], v[50:65]
	ds_read_b64_tr_b16 v[114:115], v175 offset:0x1400
	ds_read_b64_tr_b16 v[116:117], v175 offset:0x1c00
	v_mfma_f32_32x32x16_bf16 v[50:65], v[98:101], v[118:121], v[50:65]
	ds_read_b64_tr_b16 v[118:119], v175 offset:0x2400
	ds_read_b64_tr_b16 v[120:121], v175 offset:0x2c00
	ds_read_b64_tr_b16 v[122:123], v175 offset:0x3400
	ds_read_b64_tr_b16 v[124:125], v175 offset:0x3c00
	v_mfma_f32_32x32x16_bf16 v[50:65], v[102:105], v[126:129], v[50:65]
	s_waitcnt lgkmcnt(0)
	v_mfma_f32_32x32x16_bf16 v[34:49], v[68:71], v[106:109], v[34:49]
	ds_read_b64_tr_b16 v[106:107], v175 offset:0x600
	ds_read_b64_tr_b16 v[108:109], v175 offset:0xe00
	v_mfma_f32_32x32x16_bf16 v[34:49], v[76:79], v[114:117], v[34:49]
	ds_read_b64_tr_b16 v[114:115], v175 offset:0x1600
	ds_read_b64_tr_b16 v[116:117], v175 offset:0x1e00
	v_mfma_f32_32x32x16_bf16 v[34:49], v[98:101], v[118:121], v[34:49]
	ds_read_b64_tr_b16 v[118:119], v175 offset:0x2600
	ds_read_b64_tr_b16 v[120:121], v175 offset:0x2e00
	ds_read_b64_tr_b16 v[126:127], v175 offset:0x3600
	ds_read_b64_tr_b16 v[128:129], v175 offset:0x3e00
	v_mfma_f32_32x32x16_bf16 v[34:49], v[102:105], v[122:125], v[34:49]
	s_waitcnt lgkmcnt(0)
	v_mfma_f32_32x32x16_bf16 v[18:33], v[68:71], v[106:109], v[18:33]
	v_max_f32_e32 v67, v83, v83
	v_max_f32_e32 v72, v82, v82
	v_max_f32_e32 v67, v72, v67
	v_max3_f32 v67, v67, v84, v85
	v_max3_f32 v67, v67, v86, v87
	v_max3_f32 v67, v67, v88, v89
	v_max3_f32 v67, v67, v90, v91
	v_max3_f32 v67, v67, v92, v93
	v_mfma_f32_32x32x16_bf16 v[18:33], v[76:79], v[114:117], v[18:33]
	v_max3_f32 v67, v67, v94, v95
	v_max3_f32 v67, v67, v96, v97
	v_max3_f32 v67, v67, v66, v237
	v_max3_f32 v67, v67, v238, v239
	v_max3_f32 v67, v67, v240, v241
	v_max3_f32 v67, v67, v242, v73
	v_max3_f32 v67, v67, v74, v243
	v_max3_f32 v67, v67, v244, v245
	v_mfma_f32_32x32x16_bf16 v[18:33], v[98:101], v[118:121], v[18:33]
	v_max3_f32 v67, v67, v246, v247
	v_max3_f32 v67, v67, v250, v81
	v_mov_b32_e32 v68, v67
	s_nop 1
	v_permlane32_swap_b32_e32 v67, v68
	v_max_f32_e32 v68, v68, v68
	v_max_f32_e32 v67, v67, v67
	v_max_f32_e32 v67, v67, v68
	v_max_f32_e32 v69, v164, v164
	v_sub_f32_e32 v68, v67, v164
	v_max_f32_e32 v67, v69, v67
	v_mfma_f32_32x32x16_bf16 v[18:33], v[102:105], v[126:129], v[18:33]
	v_sub_f32_e32 v69, v164, v67
	v_mul_f32_e32 v69, 0x3e0293ee, v69
	v_exp_f32_e32 v69, v69
	v_cmp_ge_f32_e32 vcc, s7, v68
	s_cmp_eq_u64 vcc, exec
	s_cselect_b64 s[4:5], -1, 0
	s_barrier
; #define SWAIT() do { if constexpr (MODE == 1) asm volatile("s_waitcnt vmcnt(3)" ::: "memory"); else asm volatile("s_waitcnt vmcnt(4)" ::: "memory"); } while (0)
; #define RESC(a) do { if (__any((a) < 1.f)) { if (hi == 0) al_l[r32] = (a); asm volatile("s_waitcnt lgkmcnt(0)" ::: "memory"); \
;     _Pragma("unroll") for (int d = 0; d < 4; ++d) _Pragma("unroll") for (int r = 0; r < 16; ++r) o[d][r] *= al_l[crow(r, hi)]; } } while (0)
; template <int MODE>
; __device__ __forceinline__ void attn_pass(const bf16_t* __restrict__ Qb, const bf16_t* __restrict__ Kh, const bf16_t* __restrict__ Vh, const int NT, const int kr0, const int g4, const int map,
;                                           LAS unsigned char* lds, f32x16 (&o)[4]) {
;     ...
;         __syncthreads(); SWAIT(); SWRITE(0, SE);
;         RESC(alB); __syncthreads();
	s_waitcnt vmcnt(4)
	v_cndmask_b32_e64 v225, v69, 1.0, s[4:5]
	v_cmp_gt_f32_e32 vcc, 1.0, v225
	s_waitcnt vmcnt(4)
	ds_write_b128 v199, v[130:133]
	ds_write_b128 v200, v[134:137]
	ds_write_b128 v192, v[138:141] offset:32768
	ds_write_b128 v193, v[142:145] offset:32768
	s_cbranch_vccz .LBB0_469
	s_and_saveexec_b64 s[42:43], s[0:1]
	ds_write_b32 v171, v225 offset:128
	s_or_b64 exec, exec, s[42:43]
	s_waitcnt lgkmcnt(0)
	ds_read_b128 v[68:71], v207 offset:224
	ds_read_b128 v[76:79], v207 offset:192
	ds_read_b128 v[98:101], v207 offset:160
	ds_read_b128 v[102:105], v207 offset:128
	s_waitcnt lgkmcnt(3)
	v_pk_mul_f32 v[16:17], v[16:17], v[70:71]
	s_waitcnt lgkmcnt(2)
	v_pk_mul_f32 v[12:13], v[12:13], v[78:79]
	s_waitcnt lgkmcnt(1)
	v_pk_mul_f32 v[8:9], v[8:9], v[100:101]
	s_waitcnt lgkmcnt(0)
	v_pk_mul_f32 v[4:5], v[4:5], v[104:105]
	v_pk_mul_f32 v[14:15], v[14:15], v[68:69]
	v_pk_mul_f32 v[10:11], v[10:11], v[76:77]
	v_pk_mul_f32 v[6:7], v[6:7], v[98:99]
	v_pk_mul_f32 v[2:3], v[2:3], v[102:103]
	v_pk_mul_f32 v[64:65], v[64:65], v[70:71]
	v_pk_mul_f32 v[60:61], v[60:61], v[78:79]
	v_pk_mul_f32 v[56:57], v[56:57], v[100:101]
	v_pk_mul_f32 v[52:53], v[52:53], v[104:105]
	v_pk_mul_f32 v[62:63], v[62:63], v[68:69]
	v_pk_mul_f32 v[58:59], v[58:59], v[76:77]
	v_pk_mul_f32 v[54:55], v[54:55], v[98:99]
	v_pk_mul_f32 v[50:51], v[50:51], v[102:103]
	v_pk_mul_f32 v[48:49], v[48:49], v[70:71]
	v_pk_mul_f32 v[44:45], v[44:45], v[78:79]
	v_pk_mul_f32 v[40:41], v[40:41], v[100:101]
	v_pk_mul_f32 v[36:37], v[36:37], v[104:105]
	v_pk_mul_f32 v[46:47], v[46:47], v[68:69]
	v_pk_mul_f32 v[42:43], v[42:43], v[76:77]
	v_pk_mul_f32 v[38:39], v[38:39], v[98:99]
	v_pk_mul_f32 v[34:35], v[34:35], v[102:103]
	v_pk_mul_f32 v[32:33], v[32:33], v[70:71]
	v_pk_mul_f32 v[28:29], v[28:29], v[78:79]
	v_pk_mul_f32 v[24:25], v[24:25], v[100:101]
	v_pk_mul_f32 v[20:21], v[20:21], v[104:105]
	v_pk_mul_f32 v[30:31], v[30:31], v[68:69]
	v_pk_mul_f32 v[26:27], v[26:27], v[76:77]
	v_pk_mul_f32 v[22:23], v[22:23], v[98:99]
	v_pk_mul_f32 v[18:19], v[18:19], v[102:103]

; #define SBAR() __builtin_amdgcn_sched_barrier(0)
; #define SWAIT() do { if constexpr (MODE == 1) asm volatile("s_waitcnt vmcnt(3)" ::: "memory"); else asm volatile("s_waitcnt vmcnt(4)" ::: "memory"); } while (0)
; #define RESC(a) do { if (__any((a) < 1.f)) { if (hi == 0) al_l[r32] = (a); asm volatile("s_waitcnt lgkmcnt(0)" ::: "memory"); \
;     _Pragma("unroll") for (int d = 0; d < 4; ++d) _Pragma("unroll") for (int r = 0; r < 16; ++r) o[d][r] *= al_l[crow(r, hi)]; } } while (0)
; template <int D0> __device__ __forceinline__ void pv_one(f32x16& od, int vb, bf16x8 pa0, bf16x8 pa1, bf16x8 pa2, bf16x8 pa3) {
;     const s16x4 l0 = tr_read<v_rd_off(D0, 0, 0)>(vb), h0 = tr_read<v_rd_off(D0, 0, 1)>(vb), l1 = tr_read<v_rd_off(D0, 1, 0)>(vb), h1 = tr_read<v_rd_off(D0, 1, 1)>(vb);
;     const s16x4 l2 = tr_read<v_rd_off(D0, 2, 0)>(vb), h2 = tr_read<v_rd_off(D0, 2, 1)>(vb), l3 = tr_read<v_rd_off(D0, 3, 0)>(vb), h3 = tr_read<v_rd_off(D0, 3, 1)>(vb);
;     asm volatile("s_waitcnt lgkmcnt(0)" ::: "memory"); SBAR();
;     ...
;     od = __builtin_amdgcn_mfma_f32_32x32x16_bf16(pa0, PKV(l0, h0), od, 0, 0, 0);
;     od = __builtin_amdgcn_mfma_f32_32x32x16_bf16(pa1, PKV(l1, h1), od, 0, 0, 0);
;     od = __builtin_amdgcn_mfma_f32_32x32x16_bf16(pa2, PKV(l2, h2), od, 0, 0, 0);
;     od = __builtin_amdgcn_mfma_f32_32x32x16_bf16(pa3, PKV(l3, h3), od, 0, 0, 0);
;     ...
; }
; __device__ __forceinline__ void pv_d0(f32x16* o, int vb, bf16x8 pa0, bf16x8 pa1, bf16x8 pa2, bf16x8 pa3) {
;     pv_one<0>(o[0], vb, pa0, pa1, pa2, pa3); pv_one<1>(o[1], vb, pa0, pa1, pa2, pa3); pv_one<2>(o[2], vb, pa0, pa1, pa2, pa3); pv_one<3>(o[3], vb, pa0, pa1, pa2, pa3);
; }
; template <int MODE>
; __device__ __forceinline__ void attn_pass(const bf16_t* __restrict__ Qb, const bf16_t* __restrict__ Kh, const bf16_t* __restrict__ Vh, const int NT, const int kr0, const int g4, const int map,
;                                           LAS unsigned char* lds, f32x16 (&o)[4]) {
;     ...
;         SBAR(); qkt<MODE>(pA0, pA1, K_lds, qr, Qs, r32, hi, cbase); MASK(pA0, pA1, j + 1);
;         finishSM(pB0, pB1, alB, l_reg, pa0, pa1, pa2, pa3); SBAR();
;         if (j + 3 < NT) SLOAD(SE, j + 3); SBAR();
;         pv_d0(o, vb0 + SHM_V, pa0, pa1, pa2, pa3); partialSM<MODE>(pA0, pA1, m_reg, mnA, alA);
;         __syncthreads(); SWAIT(); SWRITE(1, SO);
;         RESC(alA); __syncthreads();
.LBB0_477:
	ds_read_b64_tr_b16 v[228:229], v173 offset:0
	ds_read_b64_tr_b16 v[230:231], v173 offset:0x800
	ds_read_b64_tr_b16 v[232:233], v173 offset:0x1000
	ds_read_b64_tr_b16 v[234:235], v173 offset:0x1800
	ds_read_b64_tr_b16 v[236:237], v173 offset:0x2000
	ds_read_b64_tr_b16 v[238:239], v173 offset:0x2800
	ds_read_b64_tr_b16 v[240:241], v173 offset:0x3000
	ds_read_b64_tr_b16 v[242:243], v173 offset:0x3800
	s_waitcnt lgkmcnt(0)
	s_nop 0
	v_mfma_f32_32x32x16_bf16 v[2:17], v[68:71], v[228:231], v[2:17]
	ds_read_b64_tr_b16 v[228:229], v173 offset:0x200
	ds_read_b64_tr_b16 v[230:231], v173 offset:0xa00
	v_mfma_f32_32x32x16_bf16 v[2:17], v[76:79], v[232:235], v[2:17]
	ds_read_b64_tr_b16 v[232:233], v173 offset:0x1200
	ds_read_b64_tr_b16 v[234:235], v173 offset:0x1a00
	v_mfma_f32_32x32x16_bf16 v[2:17], v[166:169], v[236:239], v[2:17]
	ds_read_b64_tr_b16 v[236:237], v173 offset:0x2200
	ds_read_b64_tr_b16 v[238:239], v173 offset:0x2a00
	ds_read_b64_tr_b16 v[244:245], v173 offset:0x3200
	ds_read_b64_tr_b16 v[246:247], v173 offset:0x3a00
	v_mfma_f32_32x32x16_bf16 v[2:17], v[162:165], v[240:243], v[2:17]
	s_waitcnt lgkmcnt(0)
	v_mfma_f32_32x32x16_bf16 v[50:65], v[68:71], v[228:231], v[50:65]
	ds_read_b64_tr_b16 v[228:229], v173 offset:0x400
	ds_read_b64_tr_b16 v[230:231], v173 offset:0xc00
	v_mfma_f32_32x32x16_bf16 v[50:65], v[76:79], v[232:235], v[50:65]
	ds_read_b64_tr_b16 v[232:233], v173 offset:0x1400
	ds_read_b64_tr_b16 v[234:235], v173 offset:0x1c00
	v_mfma_f32_32x32x16_bf16 v[50:65], v[166:169], v[236:239], v[50:65]
	ds_read_b64_tr_b16 v[236:237], v173 offset:0x2400
	ds_read_b64_tr_b16 v[238:239], v173 offset:0x2c00
	ds_read_b64_tr_b16 v[240:241], v173 offset:0x3400
	ds_read_b64_tr_b16 v[242:243], v173 offset:0x3c00
	v_mfma_f32_32x32x16_bf16 v[50:65], v[162:165], v[244:247], v[50:65]
	s_waitcnt lgkmcnt(0)
	v_mfma_f32_32x32x16_bf16 v[34:49], v[68:71], v[228:231], v[34:49]
	ds_read_b64_tr_b16 v[228:229], v173 offset:0x600
	ds_read_b64_tr_b16 v[230:231], v173 offset:0xe00
	v_mfma_f32_32x32x16_bf16 v[34:49], v[76:79], v[232:235], v[34:49]
	ds_read_b64_tr_b16 v[232:233], v173 offset:0x1600
	ds_read_b64_tr_b16 v[234:235], v173 offset:0x1e00
	v_mfma_f32_32x32x16_bf16 v[34:49], v[166:169], v[236:239], v[34:49]
	ds_read_b64_tr_b16 v[236:237], v173 offset:0x2600
	ds_read_b64_tr_b16 v[238:239], v173 offset:0x2e00
	ds_read_b64_tr_b16 v[244:245], v173 offset:0x3600
	ds_read_b64_tr_b16 v[246:247], v173 offset:0x3e00
	v_mfma_f32_32x32x16_bf16 v[34:49], v[162:165], v[240:243], v[34:49]
	s_waitcnt lgkmcnt(0)
	v_mfma_f32_32x32x16_bf16 v[18:33], v[68:71], v[228:231], v[18:33]
	v_max_f32_e32 v75, v83, v83
	v_max_f32_e32 v80, v82, v82
	v_max_f32_e32 v75, v80, v75
	v_max3_f32 v75, v75, v84, v85
	v_max3_f32 v75, v75, v86, v87
	v_max3_f32 v68, v75, v88, v89
	v_max3_f32 v68, v68, v90, v91
	v_max3_f32 v68, v68, v92, v93
	v_mfma_f32_32x32x16_bf16 v[18:33], v[76:79], v[232:235], v[18:33]
	v_max3_f32 v68, v68, v94, v95
	v_max3_f32 v68, v68, v96, v97
	v_max3_f32 v66, v68, v66, v99
	v_max3_f32 v66, v66, v100, v101
	v_max3_f32 v66, v66, v102, v103
	v_max3_f32 v66, v66, v104, v73
	v_max3_f32 v66, v66, v74, v107
	v_max3_f32 v66, v66, v108, v109
	v_mfma_f32_32x32x16_bf16 v[18:33], v[166:169], v[236:239], v[18:33]
	v_max3_f32 v66, v66, v110, v111
	v_max3_f32 v66, v66, v112, v81
	v_mov_b32_e32 v68, v66
	s_nop 1
	v_permlane32_swap_b32_e32 v66, v68
	v_max_f32_e32 v68, v68, v68
	v_max_f32_e32 v66, v66, v66
	v_max_f32_e32 v66, v66, v68
	v_max_f32_e32 v69, v226, v226
	v_sub_f32_e32 v68, v66, v226
	v_max_f32_e32 v66, v69, v66
	v_mfma_f32_32x32x16_bf16 v[18:33], v[162:165], v[244:247], v[18:33]
	v_sub_f32_e32 v69, v226, v66
	v_mul_f32_e32 v69, 0x3e0293ee, v69
	v_exp_f32_e32 v69, v69
	v_cmp_ge_f32_e32 vcc, s7, v68
	s_cmp_eq_u64 vcc, exec
	s_cselect_b64 s[4:5], -1, 0
	s_barrier
	s_waitcnt vmcnt(4)
	v_cndmask_b32_e64 v98, v69, 1.0, s[4:5]
	v_cmp_gt_f32_e32 vcc, 1.0, v98
	s_waitcnt vmcnt(4)
	ds_write_b128 v199, v[146:149] offset:16384
	s_waitcnt vmcnt(4)
	ds_write_b128 v200, v[150:153] offset:16384
	s_waitcnt vmcnt(4)
	ds_write_b128 v192, v[154:157] offset:49152
	s_waitcnt vmcnt(4)
	ds_write_b128 v193, v[158:161] offset:49152
	s_cbranch_vccz .LBB0_481
	s_and_saveexec_b64 s[44:45], s[0:1]
	ds_write_b32 v171, v98 offset:128
	s_or_b64 exec, exec, s[44:45]
	s_waitcnt lgkmcnt(0)
	ds_read_b128 v[68:71], v207 offset:224
	ds_read_b128 v[74:77], v207 offset:192
	ds_read_b128 v[100:103], v207 offset:160
	ds_read_b128 v[104:107], v207 offset:128
	s_waitcnt lgkmcnt(3)
	v_pk_mul_f32 v[16:17], v[16:17], v[70:71]
	s_waitcnt lgkmcnt(2)
	v_pk_mul_f32 v[12:13], v[12:13], v[76:77]
	s_waitcnt lgkmcnt(1)
	v_pk_mul_f32 v[8:9], v[8:9], v[102:103]
	s_waitcnt lgkmcnt(0)
	v_pk_mul_f32 v[4:5], v[4:5], v[106:107]
	v_pk_mul_f32 v[14:15], v[14:15], v[68:69]
	v_pk_mul_f32 v[10:11], v[10:11], v[74:75]
	v_pk_mul_f32 v[6:7], v[6:7], v[100:101]
	v_pk_mul_f32 v[2:3], v[2:3], v[104:105]
	v_pk_mul_f32 v[64:65], v[64:65], v[70:71]
	v_pk_mul_f32 v[60:61], v[60:61], v[76:77]
	v_pk_mul_f32 v[56:57], v[56:57], v[102:103]
	v_pk_mul_f32 v[52:53], v[52:53], v[106:107]
	v_pk_mul_f32 v[62:63], v[62:63], v[68:69]
	v_pk_mul_f32 v[58:59], v[58:59], v[74:75]
	v_pk_mul_f32 v[54:55], v[54:55], v[100:101]
	v_pk_mul_f32 v[50:51], v[50:51], v[104:105]
	v_pk_mul_f32 v[48:49], v[48:49], v[70:71]
	v_pk_mul_f32 v[44:45], v[44:45], v[76:77]
	v_pk_mul_f32 v[40:41], v[40:41], v[102:103]
	v_pk_mul_f32 v[36:37], v[36:37], v[106:107]
	v_pk_mul_f32 v[46:47], v[46:47], v[68:69]
	v_pk_mul_f32 v[42:43], v[42:43], v[74:75]
	v_pk_mul_f32 v[38:39], v[38:39], v[100:101]
	v_pk_mul_f32 v[34:35], v[34:35], v[104:105]
	v_pk_mul_f32 v[32:33], v[32:33], v[70:71]
	v_pk_mul_f32 v[28:29], v[28:29], v[76:77]
	v_pk_mul_f32 v[24:25], v[24:25], v[102:103]
	v_pk_mul_f32 v[20:21], v[20:21], v[106:107]
	v_pk_mul_f32 v[30:31], v[30:31], v[68:69]
	v_pk_mul_f32 v[26:27], v[26:27], v[74:75]
	v_pk_mul_f32 v[22:23], v[22:23], v[100:101]
	v_pk_mul_f32 v[18:19], v[18:19], v[104:105]

; #define LAS __attribute__((address_space(3)))
; __device__ __forceinline__ void finishSM(f32x16& p0, f32x16& p1, float alpha, float& l_reg, bf16x8& pa0, bf16x8& pa1, bf16x8& pa2, bf16x8& pa3) {
; #pragma unroll
;     for (int r = 0; r < 16; ++r) p1[r] = __builtin_amdgcn_exp2f(p1[r]);
;     float ps = 0;
; #pragma unroll
;     for (int r = 0; r < 16; ++r) ps += p0[r];
; #pragma unroll
;     for (int r = 0; r < 16; ++r) ps += p1[r];
;     { auto rr = __builtin_amdgcn_permlane32_swap(__float_as_uint(ps), __float_as_uint(ps), false, false);
;       ps = __uint_as_float(rr[0]) + __uint_as_float(rr[1]); }
;     l_reg = l_reg * alpha + ps;
;     ...
;     PK4(p0, 0, pa0); PK4(p0, 8, pa1); PK4(p1, 0, pa2); PK4(p1, 8, pa3);
;     ...
; }
; template <int MODE>
; __device__ __forceinline__ void qkt(f32x16& p0, f32x16& p1, const LAS unsigned char* Ks, const bf16x8* qr, const LAS unsigned char* Qs, int r32, int hi, int cbase) {
;     p0 = f32x16{}; p1 = f32x16{};
; #pragma unroll
;     for (int d0 = 0; d0 < Cfg<MODE>::ND; ++d0) { const int cb = cbase + (d0 * 16 + hi * 8) * 2;
;         const bf16x8 b0 = *(const LAS bf16x8*)(Ks + KSWZ(r32, cb));
;         const bf16x8 b1 = *(const LAS bf16x8*)(Ks + KSWZ(32 + r32, cb));
;         bf16x8 q; if constexpr (MODE == 0) q = *(const LAS bf16x8*)(Qs + KSWZ(r32, cb)); else q = qr[d0];
;         p0 = __builtin_amdgcn_mfma_f32_32x32x16_bf16(b0, q, p0, 0, 0, 0);
;         p1 = __builtin_amdgcn_mfma_f32_32x32x16_bf16(b1, q, p1, 0, 0, 0); }
; }
; __device__ __forceinline__ int v_st(int k, int c) { const int kk = (k & ~0xC) | ((k & 4) << 1) | ((k & 8) >> 1); return ((kk >> 3) * 4 + (c >> 5)) * 512 + ((kk & 7) * 32 + (c & 31)) * 2; }
; __device__ __forceinline__ int v_rd_base(int lane) { return ((lane & 3) << 3) | (((lane >> 2) & 3) << 6) | (((lane >> 4) & 1) << 5) | (((lane >> 5) & 1) << 8); }
; template <int OFF> __device__ __forceinline__ s16x4 tr_read(int vb) {
;     s16x4 r; asm volatile("ds_read_b64_tr_b16 %0, %1 offset:%2" : "=&v"(r) : "v"(vb), "i"(OFF) : "memory"); return r;
; }
; template <int D0> __device__ __forceinline__ void pv_one(f32x16& od, int vb, bf16x8 pa0, bf16x8 pa1, bf16x8 pa2, bf16x8 pa3) {
;     const s16x4 l0 = tr_read<v_rd_off(D0, 0, 0)>(vb), h0 = tr_read<v_rd_off(D0, 0, 1)>(vb), l1 = tr_read<v_rd_off(D0, 1, 0)>(vb), h1 = tr_read<v_rd_off(D0, 1, 1)>(vb);
.LBB0_485:
	s_or_b64 exec, exec, s[4:5]
	s_nop 7
	v_add_f32_e32 v66, 0, v234
	v_add_f32_e32 v66, v236, v66
	v_add_f32_e32 v66, v232, v66
	v_add_f32_e32 v66, v235, v66
	v_add_f32_e32 v66, v230, v66
	v_add_f32_e32 v66, v233, v66
	v_add_f32_e32 v66, v229, v66
	v_add_f32_e32 v66, v231, v66
	v_add_f32_e32 v66, v226, v66
	v_add_f32_e32 v66, v228, v66
	v_add_f32_e32 v66, v168, v66
	v_add_f32_e32 v66, v227, v66
	v_exp_f32_e32 v76, v156
	v_add_f32_e32 v66, v166, v66
	v_exp_f32_e32 v77, v157
	v_add_f32_e32 v66, v169, v66
	v_exp_f32_e32 v78, v154
	v_add_f32_e32 v66, v165, v66
	v_exp_f32_e32 v79, v155
	v_add_f32_e32 v66, v167, v66
	v_exp_f32_e32 v80, v152
	v_add_f32_e32 v66, v76, v66
	v_exp_f32_e32 v81, v153
	v_add_f32_e32 v66, v77, v66
	v_exp_f32_e32 v82, v150
	v_add_f32_e32 v66, v78, v66
	v_exp_f32_e32 v83, v151
	v_add_f32_e32 v66, v79, v66
	v_exp_f32_e32 v84, v148
	v_add_f32_e32 v66, v80, v66
	v_exp_f32_e32 v85, v149
	v_add_f32_e32 v66, v81, v66
	v_exp_f32_e32 v86, v146
	v_add_f32_e32 v66, v82, v66
	v_exp_f32_e32 v87, v147
	v_add_f32_e32 v66, v83, v66
	v_exp_f32_e32 v88, v162
	v_add_f32_e32 v66, v84, v66
	v_exp_f32_e32 v89, v163
	v_add_f32_e32 v66, v85, v66
	v_exp_f32_e32 v90, v160
	v_add_f32_e32 v66, v86, v66
	v_exp_f32_e32 v91, v161
	v_add_f32_e32 v66, v87, v66
	v_add_f32_e32 v66, v88, v66
	v_add_f32_e32 v66, v89, v66
	v_add_f32_e32 v66, v90, v66
	v_add_f32_e32 v66, v91, v66
	v_mov_b32_e32 v67, v66
	v_cvt_pk_bf16_f32 v68, v234, v236
	v_cvt_pk_bf16_f32 v69, v232, v235
	v_cvt_pk_bf16_f32 v70, v230, v233
	v_cvt_pk_bf16_f32 v71, v229, v231
	v_cvt_pk_bf16_f32 v72, v226, v228
	v_cvt_pk_bf16_f32 v73, v168, v227
	v_cvt_pk_bf16_f32 v74, v166, v169
	v_cvt_pk_bf16_f32 v75, v165, v167
	v_cvt_pk_bf16_f32 v76, v76, v77
	v_cvt_pk_bf16_f32 v77, v78, v79
	v_cvt_pk_bf16_f32 v78, v80, v81
	v_cvt_pk_bf16_f32 v79, v82, v83
	v_cvt_pk_bf16_f32 v80, v84, v85
	v_cvt_pk_bf16_f32 v81, v86, v87
	v_cvt_pk_bf16_f32 v82, v88, v89
	v_cvt_pk_bf16_f32 v83, v90, v91
	s_nop 1
	v_permlane32_swap_b32_e32 v66, v67
	v_permlane32_swap_b32_e32 v68, v70
	v_permlane32_swap_b32_e32 v69, v71
	v_permlane32_swap_b32_e32 v72, v74
	v_permlane32_swap_b32_e32 v73, v75
	v_permlane32_swap_b32_e32 v76, v78
	v_permlane32_swap_b32_e32 v77, v79
	v_permlane32_swap_b32_e32 v80, v82
	v_permlane32_swap_b32_e32 v81, v83
	ds_read_b64_tr_b16 v[84:85], v175 offset:0
	ds_read_b64_tr_b16 v[86:87], v175 offset:0x800
	ds_read_b64_tr_b16 v[88:89], v175 offset:0x1000
	ds_read_b64_tr_b16 v[90:91], v175 offset:0x1800
	ds_read_b64_tr_b16 v[92:93], v175 offset:0x2000
	ds_read_b64_tr_b16 v[94:95], v175 offset:0x2800
	ds_read_b64_tr_b16 v[132:133], v175 offset:0x3000
	ds_read_b64_tr_b16 v[134:135], v175 offset:0x3800
	s_waitcnt lgkmcnt(0)
	s_nop 0
	v_mfma_f32_32x32x16_bf16 v[2:17], v[68:71], v[84:87], v[2:17]
	ds_read_b64_tr_b16 v[84:85], v175 offset:0x200
	ds_read_b64_tr_b16 v[86:87], v175 offset:0xa00
	v_mfma_f32_32x32x16_bf16 v[2:17], v[72:75], v[88:91], v[2:17]
	ds_read_b64_tr_b16 v[88:89], v175 offset:0x1200
	ds_read_b64_tr_b16 v[90:91], v175 offset:0x1a00
	v_mfma_f32_32x32x16_bf16 v[2:17], v[76:79], v[92:95], v[2:17]
	ds_read_b64_tr_b16 v[92:93], v175 offset:0x2200
	ds_read_b64_tr_b16 v[94:95], v175 offset:0x2a00
	ds_read_b64_tr_b16 v[136:137], v175 offset:0x3200
	ds_read_b64_tr_b16 v[138:139], v175 offset:0x3a00
	v_mfma_f32_32x32x16_bf16 v[2:17], v[80:83], v[132:135], v[2:17]
	s_waitcnt lgkmcnt(0)
	v_mfma_f32_32x32x16_bf16 v[50:65], v[68:71], v[84:87], v[50:65]
	ds_read_b64_tr_b16 v[84:85], v175 offset:0x400
	ds_read_b64_tr_b16 v[86:87], v175 offset:0xc00
	v_mfma_f32_32x32x16_bf16 v[50:65], v[72:75], v[88:91], v[50:65]
	ds_read_b64_tr_b16 v[88:89], v175 offset:0x1400
	ds_read_b64_tr_b16 v[90:91], v175 offset:0x1c00
	v_mfma_f32_32x32x16_bf16 v[50:65], v[76:79], v[92:95], v[50:65]
	ds_read_b64_tr_b16 v[92:93], v175 offset:0x2400
	ds_read_b64_tr_b16 v[94:95], v175 offset:0x2c00
	ds_read_b64_tr_b16 v[132:133], v175 offset:0x3400
	ds_read_b64_tr_b16 v[134:135], v175 offset:0x3c00
	v_mfma_f32_32x32x16_bf16 v[50:65], v[80:83], v[136:139], v[50:65]
	s_waitcnt lgkmcnt(0)
	v_mfma_f32_32x32x16_bf16 v[34:49], v[68:71], v[84:87], v[34:49]
	ds_read_b64_tr_b16 v[84:85], v175 offset:0x600
	ds_read_b64_tr_b16 v[86:87], v175 offset:0xe00
	v_mfma_f32_32x32x16_bf16 v[34:49], v[72:75], v[88:91], v[34:49]
	ds_read_b64_tr_b16 v[88:89], v175 offset:0x1600
	ds_read_b64_tr_b16 v[90:91], v175 offset:0x1e00
	v_mfma_f32_32x32x16_bf16 v[34:49], v[76:79], v[92:95], v[34:49]
	ds_read_b64_tr_b16 v[92:93], v175 offset:0x2600
	ds_read_b64_tr_b16 v[94:95], v175 offset:0x2e00
	ds_read_b64_tr_b16 v[136:137], v175 offset:0x3600
	ds_read_b64_tr_b16 v[138:139], v175 offset:0x3e00
	v_mfma_f32_32x32x16_bf16 v[34:49], v[80:83], v[132:135], v[34:49]
	s_waitcnt lgkmcnt(0)
	v_mfma_f32_32x32x16_bf16 v[18:33], v[68:71], v[84:87], v[18:33]
	v_max_f32_e32 v96, v111, v111
	v_max_f32_e32 v97, v110, v110
	v_max_f32_e32 v96, v97, v96
	v_max3_f32 v96, v96, v114, v118
	v_max3_f32 v96, v96, v119, v120
	v_max3_f32 v68, v96, v121, v122
	v_max3_f32 v68, v68, v123, v124
	v_max3_f32 v68, v68, v125, v126
	v_mfma_f32_32x32x16_bf16 v[18:33], v[72:75], v[88:91], v[18:33]
	v_max3_f32 v68, v68, v127, v128
	v_max3_f32 v68, v68, v129, v130
	v_max3_f32 v68, v68, v99, v100
	v_max3_f32 v68, v68, v101, v102
	v_max3_f32 v68, v68, v103, v104
	v_max3_f32 v68, v68, v105, v106
	v_max3_f32 v68, v68, v107, v108
	v_max3_f32 v68, v68, v109, v112
	v_mfma_f32_32x32x16_bf16 v[18:33], v[76:79], v[92:95], v[18:33]
	v_max3_f32 v68, v68, v113, v116
	v_max3_f32 v68, v68, v117, v115
	v_mov_b32_e32 v69, v68
	s_nop 1
	v_permlane32_swap_b32_e32 v68, v69
	v_max_f32_e32 v69, v69, v69
	v_max_f32_e32 v68, v68, v68
	v_max_f32_e32 v68, v68, v69
	v_max_f32_e32 v70, v164, v164
	v_max_f32_e32 v70, v70, v68
	v_sub_f32_e32 v69, v68, v164
	v_mfma_f32_32x32x16_bf16 v[18:33], v[80:83], v[136:139], v[18:33]
	v_sub_f32_e32 v68, v164, v70
	s_mov_b32 s3, 0x42b504f3
	v_mul_f32_e32 v68, 0x3e0293ee, v68
	v_exp_f32_e32 v68, v68
	v_cmp_ge_f32_e32 vcc, s3, v69
	s_cmp_eq_u64 vcc, exec
	s_cselect_b64 vcc, -1, 0
	v_cndmask_b32_e32 v69, v70, v164, vcc
	v_cndmask_b32_e64 v68, v68, 1.0, vcc
	v_mul_f32_e32 v69, 0xbe0293ee, v69
	v_fmamk_f32 v70, v110, 0x3e0293ee, v69
	v_fmamk_f32 v71, v111, 0x3e0293ee, v69
	v_fmamk_f32 v72, v114, 0x3e0293ee, v69
	v_fmamk_f32 v73, v118, 0x3e0293ee, v69
	v_fmamk_f32 v74, v119, 0x3e0293ee, v69
	v_fmamk_f32 v75, v120, 0x3e0293ee, v69
	v_fmamk_f32 v76, v121, 0x3e0293ee, v69
	v_fmamk_f32 v77, v122, 0x3e0293ee, v69
	v_fmamk_f32 v78, v123, 0x3e0293ee, v69
	v_fmamk_f32 v79, v124, 0x3e0293ee, v69
	v_fmamk_f32 v80, v125, 0x3e0293ee, v69
	v_fmamk_f32 v81, v126, 0x3e0293ee, v69
	v_fmamk_f32 v82, v127, 0x3e0293ee, v69
	v_fmamk_f32 v83, v128, 0x3e0293ee, v69
	v_fmamk_f32 v84, v129, 0x3e0293ee, v69
	v_fmamk_f32 v85, v130, 0x3e0293ee, v69
	v_cmp_gt_f32_e32 vcc, 1.0, v68
	s_barrier
; #define SBAR() __builtin_amdgcn_sched_barrier(0)
; #define RESC(a) do { if (__any((a) < 1.f)) { if (hi == 0) al_l[r32] = (a); asm volatile("s_waitcnt lgkmcnt(0)" ::: "memory"); \
;     _Pragma("unroll") for (int d = 0; d < 4; ++d) _Pragma("unroll") for (int r = 0; r < 16; ++r) o[d][r] *= al_l[crow(r, hi)]; } } while (0)
; __device__ __forceinline__ void finishSM(f32x16& p0, f32x16& p1, float alpha, float& l_reg, bf16x8& pa0, bf16x8& pa1, bf16x8& pa2, bf16x8& pa3) {
; #pragma unroll
;     for (int r = 0; r < 16; ++r) p1[r] = __builtin_amdgcn_exp2f(p1[r]);
;     float ps = 0;
; #pragma unroll
;     for (int r = 0; r < 16; ++r) ps += p0[r];
; #pragma unroll
;     for (int r = 0; r < 16; ++r) ps += p1[r];
;     { auto rr = __builtin_amdgcn_permlane32_swap(__float_as_uint(ps), __float_as_uint(ps), false, false);
;       ps = __uint_as_float(rr[0]) + __uint_as_float(rr[1]); }
;     l_reg = l_reg * alpha + ps;
;     ...
;     PK4(p0, 0, pa0); PK4(p0, 8, pa1); PK4(p1, 0, pa2); PK4(p1, 8, pa3);
; template <int MODE>
; __device__ __forceinline__ void attn_pass(const bf16_t* __restrict__ Qb, const bf16_t* __restrict__ Kh, const bf16_t* __restrict__ Vh, const int NT, const int kr0, const int g4, const int map,
;                                           LAS unsigned char* lds, f32x16 (&o)[4]) {
;     ...
;     __syncthreads(); RESC(alB);
;     finishSM(pB0, pB1, alB, l_reg, pa0, pa1, pa2, pa3); SBAR();
;     pv_d0(o, vb0 + SHM_V, pa0, pa1, pa2, pa3);
	s_cbranch_vccz .LBB0_489
	s_and_saveexec_b64 s[4:5], s[0:1]
	ds_write_b32 v171, v68 offset:128
	s_or_b64 exec, exec, s[4:5]
	s_waitcnt lgkmcnt(0)
	v_lshl_add_u32 v110, v187, 2, v1
	ds_read_b128 v[86:89], v110 offset:224
	ds_read_b128 v[90:93], v110 offset:192
	ds_read_b128 v[94:97], v110 offset:160
	ds_read_b128 v[118:121], v110 offset:128
	s_waitcnt lgkmcnt(3)
	v_pk_mul_f32 v[16:17], v[16:17], v[88:89]
	s_waitcnt lgkmcnt(2)
	v_pk_mul_f32 v[12:13], v[12:13], v[92:93]
	s_waitcnt lgkmcnt(1)
	v_pk_mul_f32 v[8:9], v[8:9], v[96:97]
	s_waitcnt lgkmcnt(0)
	v_pk_mul_f32 v[4:5], v[4:5], v[120:121]
	v_pk_mul_f32 v[14:15], v[14:15], v[86:87]
	v_pk_mul_f32 v[10:11], v[10:11], v[90:91]
	v_pk_mul_f32 v[6:7], v[6:7], v[94:95]
	v_pk_mul_f32 v[2:3], v[2:3], v[118:119]
	v_pk_mul_f32 v[64:65], v[64:65], v[88:89]
	v_pk_mul_f32 v[60:61], v[60:61], v[92:93]
	v_pk_mul_f32 v[56:57], v[56:57], v[96:97]
	v_pk_mul_f32 v[52:53], v[52:53], v[120:121]
	v_pk_mul_f32 v[62:63], v[62:63], v[86:87]
	v_pk_mul_f32 v[58:59], v[58:59], v[90:91]
	v_pk_mul_f32 v[54:55], v[54:55], v[94:95]
	v_pk_mul_f32 v[50:51], v[50:51], v[118:119]
	v_pk_mul_f32 v[48:49], v[48:49], v[88:89]
	v_pk_mul_f32 v[44:45], v[44:45], v[92:93]
	v_pk_mul_f32 v[40:41], v[40:41], v[96:97]
	v_pk_mul_f32 v[36:37], v[36:37], v[120:121]
	v_pk_mul_f32 v[46:47], v[46:47], v[86:87]
	v_pk_mul_f32 v[42:43], v[42:43], v[90:91]
	v_pk_mul_f32 v[38:39], v[38:39], v[94:95]
	v_pk_mul_f32 v[34:35], v[34:35], v[118:119]
	v_pk_mul_f32 v[32:33], v[32:33], v[88:89]
	v_pk_mul_f32 v[28:29], v[28:29], v[92:93]
	v_pk_mul_f32 v[24:25], v[24:25], v[96:97]
	v_pk_mul_f32 v[20:21], v[20:21], v[120:121]
	v_pk_mul_f32 v[30:31], v[30:31], v[86:87]
	v_pk_mul_f32 v[26:27], v[26:27], v[90:91]
	v_pk_mul_f32 v[22:23], v[22:23], v[94:95]
	v_pk_mul_f32 v[18:19], v[18:19], v[118:119]
.LBB0_489:
	v_exp_f32_e32 v91, v70
	v_exp_f32_e32 v93, v71
	v_exp_f32_e32 v89, v72
	v_fmamk_f32 v94, v99, 0x3e0293ee, v69
	v_fmamk_f32 v95, v100, 0x3e0293ee, v69
	v_fmamk_f32 v96, v101, 0x3e0293ee, v69
	v_fmamk_f32 v97, v102, 0x3e0293ee, v69
	v_fmamk_f32 v99, v103, 0x3e0293ee, v69
	v_fmamk_f32 v100, v104, 0x3e0293ee, v69
	v_fmamk_f32 v101, v105, 0x3e0293ee, v69
	v_fmamk_f32 v102, v106, 0x3e0293ee, v69
	v_fmamk_f32 v103, v107, 0x3e0293ee, v69
	v_fmamk_f32 v104, v108, 0x3e0293ee, v69
	v_fmamk_f32 v105, v109, 0x3e0293ee, v69
	v_fmamk_f32 v106, v112, 0x3e0293ee, v69
	v_fmamk_f32 v107, v113, 0x3e0293ee, v69
	v_exp_f32_e32 v92, v73
	v_exp_f32_e32 v86, v76
	v_exp_f32_e32 v76, v78
	v_exp_f32_e32 v78, v79
	v_fmamk_f32 v70, v116, 0x3e0293ee, v69
	v_fmamk_f32 v79, v117, 0x3e0293ee, v69
	v_fmac_f32_e32 v69, 0x3e0293ee, v115
	v_exp_f32_e32 v87, v74
	v_exp_f32_e32 v108, v69
	v_add_f32_e32 v69, 0, v91
	v_exp_f32_e32 v90, v75
	v_add_f32_e32 v69, v93, v69
	v_add_f32_e32 v69, v89, v69
	v_exp_f32_e32 v88, v77
	v_add_f32_e32 v69, v92, v69
	v_add_f32_e32 v69, v87, v69
	v_add_f32_e32 v69, v90, v69
	v_exp_f32_e32 v74, v80
	v_add_f32_e32 v69, v86, v69
	v_exp_f32_e32 v77, v81
	v_add_f32_e32 v69, v88, v69
	v_exp_f32_e32 v72, v82
	v_add_f32_e32 v69, v76, v69
	v_exp_f32_e32 v75, v83
	v_add_f32_e32 v69, v78, v69
	v_exp_f32_e32 v71, v84
	v_add_f32_e32 v69, v74, v69
	v_exp_f32_e32 v73, v85
	v_add_f32_e32 v69, v77, v69
	v_exp_f32_e32 v84, v94
	v_add_f32_e32 v69, v72, v69
	v_exp_f32_e32 v85, v95
	v_add_f32_e32 v69, v75, v69
	v_exp_f32_e32 v94, v96
	v_add_f32_e32 v69, v71, v69
	v_exp_f32_e32 v95, v97
	v_add_f32_e32 v69, v73, v69
	v_exp_f32_e32 v96, v99
	v_add_f32_e32 v69, v84, v69
	v_exp_f32_e32 v97, v100
	v_add_f32_e32 v69, v85, v69
	v_exp_f32_e32 v99, v101
	v_add_f32_e32 v69, v94, v69
	v_exp_f32_e32 v100, v102
	v_add_f32_e32 v69, v95, v69
	v_exp_f32_e32 v101, v103
	v_add_f32_e32 v69, v96, v69
	v_exp_f32_e32 v102, v104
	v_add_f32_e32 v69, v97, v69
	v_exp_f32_e32 v103, v105
	v_add_f32_e32 v69, v99, v69
	v_exp_f32_e32 v104, v106
	v_add_f32_e32 v69, v100, v69
	v_exp_f32_e32 v105, v107
	v_add_f32_e32 v69, v101, v69
	v_exp_f32_e32 v106, v70
	v_add_f32_e32 v69, v102, v69
	v_exp_f32_e32 v107, v79
	v_add_f32_e32 v69, v103, v69
	v_add_f32_e32 v69, v104, v69
	v_add_f32_e32 v69, v105, v69
	v_add_f32_e32 v69, v106, v69
	v_add_f32_e32 v69, v107, v69
	v_add_f32_e32 v69, v108, v69
	v_mov_b32_e32 v70, v69
	s_nop 1
	v_permlane32_swap_b32_e32 v69, v70
	v_cvt_pk_bf16_f32 v80, v91, v93
	v_cvt_pk_bf16_f32 v81, v89, v92
	v_cvt_pk_bf16_f32 v82, v87, v90
	v_cvt_pk_bf16_f32 v83, v86, v88
	v_cvt_pk_bf16_f32 v76, v76, v78
	v_cvt_pk_bf16_f32 v77, v74, v77
	v_cvt_pk_bf16_f32 v78, v72, v75
	v_cvt_pk_bf16_f32 v79, v71, v73
	v_cvt_pk_bf16_f32 v72, v84, v85
	v_cvt_pk_bf16_f32 v73, v94, v95
	v_cvt_pk_bf16_f32 v74, v96, v97
	v_cvt_pk_bf16_f32 v75, v99, v100
	v_cvt_pk_bf16_f32 v84, v101, v102
	v_cvt_pk_bf16_f32 v85, v103, v104
	v_cvt_pk_bf16_f32 v86, v105, v106
	v_cvt_pk_bf16_f32 v87, v107, v108
	s_nop 0
	v_permlane32_swap_b32_e32 v80, v82
	v_permlane32_swap_b32_e32 v81, v83
	v_permlane32_swap_b32_e32 v76, v78
	v_permlane32_swap_b32_e32 v77, v79
	v_permlane32_swap_b32_e32 v72, v74
	v_permlane32_swap_b32_e32 v73, v75
	v_permlane32_swap_b32_e32 v84, v86
	v_permlane32_swap_b32_e32 v85, v87
	ds_read_b64_tr_b16 v[88:89], v173 offset:0
	ds_read_b64_tr_b16 v[90:91], v173 offset:0x800
	ds_read_b64_tr_b16 v[92:93], v173 offset:0x1000
	ds_read_b64_tr_b16 v[94:95], v173 offset:0x1800
	ds_read_b64_tr_b16 v[100:101], v173 offset:0x2000
	ds_read_b64_tr_b16 v[102:103], v173 offset:0x2800
	ds_read_b64_tr_b16 v[104:105], v173 offset:0x3000
	ds_read_b64_tr_b16 v[106:107], v173 offset:0x3800
	s_waitcnt lgkmcnt(0)
; #define SBAR() __builtin_amdgcn_sched_barrier(0)
; __device__ __forceinline__ int crow(int r, int hi) { return (r & 3) + 8 * (r >> 2) + 4 * hi; }
; template <int D0> __device__ __forceinline__ void pv_one(f32x16& od, int vb, bf16x8 pa0, bf16x8 pa1, bf16x8 pa2, bf16x8 pa3) {
;     const s16x4 l0 = tr_read<v_rd_off(D0, 0, 0)>(vb), h0 = tr_read<v_rd_off(D0, 0, 1)>(vb), l1 = tr_read<v_rd_off(D0, 1, 0)>(vb), h1 = tr_read<v_rd_off(D0, 1, 1)>(vb);
;     const s16x4 l2 = tr_read<v_rd_off(D0, 2, 0)>(vb), h2 = tr_read<v_rd_off(D0, 2, 1)>(vb), l3 = tr_read<v_rd_off(D0, 3, 0)>(vb), h3 = tr_read<v_rd_off(D0, 3, 1)>(vb);
;     asm volatile("s_waitcnt lgkmcnt(0)" ::: "memory"); SBAR();
;     ...
;     od = __builtin_amdgcn_mfma_f32_32x32x16_bf16(pa0, PKV(l0, h0), od, 0, 0, 0);
;     od = __builtin_amdgcn_mfma_f32_32x32x16_bf16(pa1, PKV(l1, h1), od, 0, 0, 0);
;     od = __builtin_amdgcn_mfma_f32_32x32x16_bf16(pa2, PKV(l2, h2), od, 0, 0, 0);
;     od = __builtin_amdgcn_mfma_f32_32x32x16_bf16(pa3, PKV(l3, h3), od, 0, 0, 0);
;     ...
; }
; __device__ __forceinline__ void pv_d0(f32x16* o, int vb, bf16x8 pa0, bf16x8 pa1, bf16x8 pa2, bf16x8 pa3) {
;     pv_one<0>(o[0], vb, pa0, pa1, pa2, pa3); pv_one<1>(o[1], vb, pa0, pa1, pa2, pa3); pv_one<2>(o[2], vb, pa0, pa1, pa2, pa3); pv_one<3>(o[3], vb, pa0, pa1, pa2, pa3);
; }
; template <int MODE>
; __device__ __forceinline__ void attn_pass(const bf16_t* __restrict__ Qb, const bf16_t* __restrict__ Kh, const bf16_t* __restrict__ Vh, const int NT, const int kr0, const int g4, const int map,
;                                           LAS unsigned char* lds, f32x16 (&o)[4]) {
;     ...
;     pv_d0(o, vb0 + SHM_V, pa0, pa1, pa2, pa3);
;     if (hi == 0) li_l[r32] = l_reg; asm volatile("s_waitcnt lgkmcnt(0)" ::: "memory");
; #pragma unroll
;     for (int r = 0; r < 16; ++r) { const float rl = __builtin_amdgcn_rcpf(li_l[crow(r, hi)]);
; #pragma unroll
;         for (int d = 0; d < 4; ++d) o[d][r] *= rl; }
;     __syncthreads();
	s_nop 0
	v_mfma_f32_32x32x16_bf16 v[2:17], v[80:83], v[88:91], v[2:17]
	ds_read_b64_tr_b16 v[88:89], v173 offset:0x200
	ds_read_b64_tr_b16 v[90:91], v173 offset:0xa00
	v_mfma_f32_32x32x16_bf16 v[2:17], v[76:79], v[92:95], v[2:17]
	ds_read_b64_tr_b16 v[92:93], v173 offset:0x1200
	ds_read_b64_tr_b16 v[94:95], v173 offset:0x1a00
	v_mfma_f32_32x32x16_bf16 v[2:17], v[72:75], v[100:103], v[2:17]
	ds_read_b64_tr_b16 v[100:101], v173 offset:0x2200
	ds_read_b64_tr_b16 v[102:103], v173 offset:0x2a00
	ds_read_b64_tr_b16 v[108:109], v173 offset:0x3200
	ds_read_b64_tr_b16 v[110:111], v173 offset:0x3a00
	v_mfma_f32_32x32x16_bf16 v[2:17], v[84:87], v[104:107], v[2:17]
	s_waitcnt lgkmcnt(0)
	v_mfma_f32_32x32x16_bf16 v[50:65], v[80:83], v[88:91], v[50:65]
	ds_read_b64_tr_b16 v[88:89], v173 offset:0x400
	ds_read_b64_tr_b16 v[90:91], v173 offset:0xc00
	v_mfma_f32_32x32x16_bf16 v[50:65], v[76:79], v[92:95], v[50:65]
	ds_read_b64_tr_b16 v[92:93], v173 offset:0x1400
	ds_read_b64_tr_b16 v[94:95], v173 offset:0x1c00
	v_mfma_f32_32x32x16_bf16 v[50:65], v[72:75], v[100:103], v[50:65]
	ds_read_b64_tr_b16 v[100:101], v173 offset:0x2400
	ds_read_b64_tr_b16 v[102:103], v173 offset:0x2c00
	ds_read_b64_tr_b16 v[104:105], v173 offset:0x3400
	ds_read_b64_tr_b16 v[106:107], v173 offset:0x3c00
	v_mfma_f32_32x32x16_bf16 v[50:65], v[84:87], v[108:111], v[50:65]
	s_waitcnt lgkmcnt(0)
	v_mfma_f32_32x32x16_bf16 v[34:49], v[80:83], v[88:91], v[34:49]
	ds_read_b64_tr_b16 v[88:89], v173 offset:0x600
	ds_read_b64_tr_b16 v[90:91], v173 offset:0xe00
	v_mfma_f32_32x32x16_bf16 v[34:49], v[76:79], v[92:95], v[34:49]
	ds_read_b64_tr_b16 v[92:93], v173 offset:0x1600
	ds_read_b64_tr_b16 v[94:95], v173 offset:0x1e00
	v_mfma_f32_32x32x16_bf16 v[34:49], v[72:75], v[100:103], v[34:49]
	ds_read_b64_tr_b16 v[100:101], v173 offset:0x2600
	ds_read_b64_tr_b16 v[102:103], v173 offset:0x2e00
	ds_read_b64_tr_b16 v[108:109], v173 offset:0x3600
	ds_read_b64_tr_b16 v[110:111], v173 offset:0x3e00
	v_mfma_f32_32x32x16_bf16 v[34:49], v[84:87], v[104:107], v[34:49]
	s_waitcnt lgkmcnt(0)
	v_mfma_f32_32x32x16_bf16 v[18:33], v[80:83], v[88:91], v[18:33]
	v_mfma_f32_32x32x16_bf16 v[18:33], v[76:79], v[92:95], v[18:33]
	v_mfma_f32_32x32x16_bf16 v[18:33], v[72:75], v[100:103], v[18:33]
	v_mfma_f32_32x32x16_bf16 v[18:33], v[84:87], v[108:111], v[18:33]
	s_and_saveexec_b64 s[4:5], s[0:1]
	v_add_f32_e32 v66, v66, v67
	v_fmac_f32_e32 v66, v188, v98
	v_add_f32_e32 v67, v69, v70
	v_fmac_f32_e32 v67, v66, v68
	ds_write_b32 v171, v67
	s_or_b64 exec, exec, s[4:5]
	s_waitcnt lgkmcnt(0)
	v_lshl_add_u32 v1, v187, 2, v1
	ds_read_b128 v[66:69], v1
	ds_read_b128 v[70:73], v1 offset:32
	s_mov_b64 s[0:1], 0x40600000
	s_waitcnt lgkmcnt(1)
	v_rcp_f32_e32 v66, v66
	v_rcp_f32_e32 v67, v67
	v_mul_f32_e32 v74, v2, v66
	v_mul_f32_e32 v50, v50, v66
	v_mul_f32_e32 v34, v34, v66
	v_mul_f32_e32 v18, v18, v66
	v_mul_f32_e32 v66, v3, v67
	v_rcp_f32_e32 v2, v68
	v_rcp_f32_e32 v3, v69
	v_mul_f32_e32 v51, v51, v67
	v_mul_f32_e32 v35, v35, v67
	v_mul_f32_e32 v19, v19, v67
	v_mul_f32_e32 v67, v4, v2
	v_mul_f32_e32 v52, v52, v2
	v_mul_f32_e32 v36, v36, v2
	v_mul_f32_e32 v20, v20, v2
	v_mul_f32_e32 v68, v5, v3
	s_waitcnt lgkmcnt(0)
	v_rcp_f32_e32 v2, v70
	v_mul_f32_e32 v53, v53, v3
	v_mul_f32_e32 v37, v37, v3
	v_mul_f32_e32 v21, v21, v3
	v_rcp_f32_e32 v3, v71
	v_mul_f32_e32 v69, v6, v2
	v_mul_f32_e32 v54, v54, v2
	v_mul_f32_e32 v38, v38, v2
	v_mul_f32_e32 v22, v22, v2
	v_mul_f32_e32 v70, v7, v3
	v_mul_f32_e32 v55, v55, v3
	v_mul_f32_e32 v39, v39, v3
	v_mul_f32_e32 v23, v23, v3
	ds_read_b128 v[2:5], v1 offset:64
	v_rcp_f32_e32 v6, v72
	v_rcp_f32_e32 v72, v73
	v_mul_f32_e32 v71, v8, v6
	v_mul_f32_e32 v56, v56, v6
	v_mul_f32_e32 v40, v40, v6
	v_mul_f32_e32 v24, v24, v6
	v_mul_f32_e32 v73, v9, v72
	ds_read_b128 v[6:9], v1 offset:96
	s_waitcnt lgkmcnt(1)
	v_rcp_f32_e32 v1, v2
	v_rcp_f32_e32 v2, v3
	v_rcp_f32_e32 v3, v4
	s_waitcnt lgkmcnt(0)
	v_mul_f32_e32 v10, v10, v1
	v_mul_f32_e32 v58, v58, v1
	v_mul_f32_e32 v42, v42, v1
	v_mul_f32_e32 v1, v26, v1
	v_mul_f32_e32 v11, v11, v2
	v_mul_f32_e32 v26, v59, v2
	v_mul_f32_e32 v43, v43, v2
	v_mul_f32_e32 v27, v27, v2
	v_rcp_f32_e32 v2, v5
	v_mul_f32_e32 v12, v12, v3
	v_mul_f32_e32 v59, v60, v3
	v_mul_f32_e32 v44, v44, v3
	v_mul_f32_e32 v28, v28, v3
	v_rcp_f32_e32 v3, v6
	v_mul_f32_e32 v13, v13, v2
	v_mul_f32_e32 v60, v61, v2
	v_mul_f32_e32 v45, v45, v2
	v_mul_f32_e32 v29, v29, v2
	v_rcp_f32_e32 v2, v7
	v_mul_f32_e32 v14, v14, v3
	v_mul_f32_e32 v61, v62, v3
	v_mul_f32_e32 v46, v46, v3
	v_mul_f32_e32 v30, v30, v3
	v_rcp_f32_e32 v3, v8
	v_mul_f32_e32 v15, v15, v2
	v_mul_f32_e32 v8, v63, v2
	v_mul_f32_e32 v47, v47, v2
	v_mul_f32_e32 v31, v31, v2
	v_rcp_f32_e32 v2, v9
	s_barrier
; __device__ __forceinline__ unsigned char f2fp8(float a) { return (unsigned char)(__builtin_amdgcn_cvt_pk_fp8_f32(a, a, 0, false) & 0xff); }
; __device__ __forceinline__ int crow(int r, int hi) { return (r & 3) + 8 * (r >> 2) + 4 * hi; }
; __device__ __forceinline__ void p3_attention(Frame& F) {
;     ...
;         int hi2 = hi, r32b = r32; asm volatile("" : "+v"(hi2), "+v"(r32b));
;         unsigned char* od = F.ws + WS_ONA + (size_t)(b * SEQ + g4 * 256 + wid * 32) * 1024 + h * 128 + r32b;
; #pragma unroll
;         for (int r = 0; r < 16; ++r) { unsigned char* orow = od + (size_t)attn::crow(r, hi2) * 1024;
; #pragma unroll
;             for (int d = 0; d < 4; ++d) orow[d * 32] = f2fp8(o[d][r] * OSCALE); }
	v_mul_f32_e32 v9, v64, v3
	v_lshlrev_b32_e32 v4, 2, v186
	v_ashrrev_i32_e32 v5, 31, v4
	v_lshlrev_b64 v[6:7], 10, v[4:5]
	v_mul_f32_e32 v5, 0x41800000, v74
	v_mov_b32_e32 v64, 0
	v_ashrrev_i32_e32 v173, 31, v172
	v_cvt_pk_fp8_f32 v64, v5, v5
	v_mul_f32_e32 v5, 0x41800000, v50
	v_mov_b32_e32 v50, 0
	v_mul_f32_e32 v16, v16, v3
	v_mul_f32_e32 v48, v48, v3
	v_mul_f32_e32 v32, v32, v3
	v_mul_f32_e32 v17, v17, v2
	v_mul_f32_e32 v62, v65, v2
	v_mul_f32_e32 v49, v49, v2
	v_mul_f32_e32 v33, v33, v2
	v_lshl_add_u64 v[2:3], v[178:179], 0, v[172:173]
	v_cvt_pk_fp8_f32 v50, v5, v5
	v_mul_f32_e32 v5, 0x41800000, v34
	v_mov_b32_e32 v34, 0
	v_lshl_add_u64 v[2:3], v[2:3], 0, s[0:1]
	v_cvt_pk_fp8_f32 v34, v5, v5
	v_mul_f32_e32 v5, 0x41800000, v18
	v_mov_b32_e32 v18, 0
	v_lshl_add_u64 v[6:7], v[2:3], 0, v[6:7]
	v_cvt_pk_fp8_f32 v18, v5, v5
	global_store_byte v[6:7], v64, off
	global_store_byte v[6:7], v50, off offset:32
	global_store_byte v[6:7], v34, off offset:64
	global_store_byte v[6:7], v18, off offset:96
	v_mul_f32_e32 v5, 0x41800000, v66
	v_mov_b32_e32 v18, 0
	v_or_b32_e32 v6, 1, v4
	v_cvt_pk_fp8_f32 v18, v5, v5
	v_mul_f32_e32 v5, 0x41800000, v51
	v_mov_b32_e32 v34, 0
	v_ashrrev_i32_e32 v7, 31, v6
	v_cvt_pk_fp8_f32 v34, v5, v5
	v_mul_f32_e32 v5, 0x41800000, v35
	v_mov_b32_e32 v35, 0
	v_lshlrev_b64 v[6:7], 10, v[6:7]
	v_cvt_pk_fp8_f32 v35, v5, v5
	v_mul_f32_e32 v5, 0x41800000, v19
	v_mov_b32_e32 v19, 0
	v_lshl_add_u64 v[6:7], v[2:3], 0, v[6:7]
	v_cvt_pk_fp8_f32 v19, v5, v5
	global_store_byte v[6:7], v18, off
	global_store_byte v[6:7], v34, off offset:32
	global_store_byte v[6:7], v35, off offset:64
	global_store_byte v[6:7], v19, off offset:96
	v_mul_f32_e32 v5, 0x41800000, v67
	v_mov_b32_e32 v18, 0
	v_or_b32_e32 v6, 2, v4
	v_cvt_pk_fp8_f32 v18, v5, v5
	v_mul_f32_e32 v5, 0x41800000, v52
	v_mov_b32_e32 v19, 0
	v_ashrrev_i32_e32 v7, 31, v6
	v_cvt_pk_fp8_f32 v19, v5, v5
	v_mul_f32_e32 v5, 0x41800000, v36
	v_mov_b32_e32 v34, 0
	v_lshlrev_b64 v[6:7], 10, v[6:7]
	v_cvt_pk_fp8_f32 v34, v5, v5
	v_mul_f32_e32 v5, 0x41800000, v20
	v_mov_b32_e32 v20, 0
	v_lshl_add_u64 v[6:7], v[2:3], 0, v[6:7]
	v_cvt_pk_fp8_f32 v20, v5, v5
	global_store_byte v[6:7], v18, off
	global_store_byte v[6:7], v19, off offset:32
	global_store_byte v[6:7], v34, off offset:64
	global_store_byte v[6:7], v20, off offset:96
	v_mul_f32_e32 v5, 0x41800000, v68
	v_mov_b32_e32 v18, 0
	v_or_b32_e32 v6, 3, v4
	v_cvt_pk_fp8_f32 v18, v5, v5
	v_mul_f32_e32 v5, 0x41800000, v53
	v_mov_b32_e32 v19, 0
	v_ashrrev_i32_e32 v7, 31, v6
	v_cvt_pk_fp8_f32 v19, v5, v5
	v_mul_f32_e32 v5, 0x41800000, v37
	v_mov_b32_e32 v20, 0
	v_lshlrev_b64 v[6:7], 10, v[6:7]
	v_cvt_pk_fp8_f32 v20, v5, v5
	v_mul_f32_e32 v5, 0x41800000, v21
	v_mov_b32_e32 v21, 0
	v_lshl_add_u64 v[6:7], v[2:3], 0, v[6:7]
	v_cvt_pk_fp8_f32 v21, v5, v5
	global_store_byte v[6:7], v18, off
	global_store_byte v[6:7], v19, off offset:32
	global_store_byte v[6:7], v20, off offset:64
	global_store_byte v[6:7], v21, off offset:96
	v_mul_f32_e32 v5, 0x41800000, v69
	v_mov_b32_e32 v18, 0
	v_add_u32_e32 v6, 8, v4
	v_cvt_pk_fp8_f32 v18, v5, v5
	v_mul_f32_e32 v5, 0x41800000, v54
	v_mov_b32_e32 v19, 0
	v_ashrrev_i32_e32 v7, 31, v6
	v_cvt_pk_fp8_f32 v19, v5, v5
	v_mul_f32_e32 v5, 0x41800000, v38
	v_mov_b32_e32 v20, 0
	v_lshlrev_b64 v[6:7], 10, v[6:7]
	v_cvt_pk_fp8_f32 v20, v5, v5
	v_mul_f32_e32 v5, 0x41800000, v22
	v_mov_b32_e32 v21, 0
	v_lshl_add_u64 v[6:7], v[2:3], 0, v[6:7]
	v_cvt_pk_fp8_f32 v21, v5, v5
	global_store_byte v[6:7], v18, off
	global_store_byte v[6:7], v19, off offset:32
	global_store_byte v[6:7], v20, off offset:64
	global_store_byte v[6:7], v21, off offset:96
	v_mul_f32_e32 v5, 0x41800000, v70
	v_mov_b32_e32 v18, 0
	v_add_u32_e32 v6, 9, v4
	v_cvt_pk_fp8_f32 v18, v5, v5
	v_mul_f32_e32 v5, 0x41800000, v55
	v_mov_b32_e32 v19, 0
	v_ashrrev_i32_e32 v7, 31, v6
	v_cvt_pk_fp8_f32 v19, v5, v5
	v_mul_f32_e32 v5, 0x41800000, v39
	v_mov_b32_e32 v20, 0
	v_lshlrev_b64 v[6:7], 10, v[6:7]
	v_cvt_pk_fp8_f32 v20, v5, v5
	v_mul_f32_e32 v5, 0x41800000, v23
	v_mov_b32_e32 v21, 0
	v_lshl_add_u64 v[6:7], v[2:3], 0, v[6:7]
	v_cvt_pk_fp8_f32 v21, v5, v5
	global_store_byte v[6:7], v18, off
	global_store_byte v[6:7], v19, off offset:32
	global_store_byte v[6:7], v20, off offset:64
	global_store_byte v[6:7], v21, off offset:96
	v_mul_f32_e32 v5, 0x41800000, v71
	v_mov_b32_e32 v18, 0
	v_add_u32_e32 v6, 10, v4
	v_cvt_pk_fp8_f32 v18, v5, v5
	v_mul_f32_e32 v5, 0x41800000, v56
	v_mov_b32_e32 v19, 0
	v_ashrrev_i32_e32 v7, 31, v6
	v_cvt_pk_fp8_f32 v19, v5, v5
	v_mul_f32_e32 v5, 0x41800000, v40
	v_mov_b32_e32 v20, 0
	v_lshlrev_b64 v[6:7], 10, v[6:7]
	v_cvt_pk_fp8_f32 v20, v5, v5
	v_mul_f32_e32 v5, 0x41800000, v24
	v_mov_b32_e32 v21, 0
	v_lshl_add_u64 v[6:7], v[2:3], 0, v[6:7]
	v_cvt_pk_fp8_f32 v21, v5, v5
	v_mul_f32_e32 v57, v57, v72
	global_store_byte v[6:7], v18, off
	global_store_byte v[6:7], v19, off offset:32
	global_store_byte v[6:7], v20, off offset:64
	global_store_byte v[6:7], v21, off offset:96
	v_mul_f32_e32 v5, 0x41800000, v73
	v_mov_b32_e32 v18, 0
	v_mul_f32_e32 v41, v41, v72
	v_add_u32_e32 v6, 11, v4
	v_cvt_pk_fp8_f32 v18, v5, v5
	v_mul_f32_e32 v5, 0x41800000, v57
	v_mov_b32_e32 v19, 0
	v_mul_f32_e32 v25, v25, v72
	v_ashrrev_i32_e32 v7, 31, v6
	v_cvt_pk_fp8_f32 v19, v5, v5
	v_mul_f32_e32 v5, 0x41800000, v41
	v_mov_b32_e32 v20, 0
	v_lshlrev_b64 v[6:7], 10, v[6:7]
	v_cvt_pk_fp8_f32 v20, v5, v5
	v_mul_f32_e32 v5, 0x41800000, v25
	v_mov_b32_e32 v21, 0
; __device__ __forceinline__ unsigned char f2fp8(float a) { return (unsigned char)(__builtin_amdgcn_cvt_pk_fp8_f32(a, a, 0, false) & 0xff); }
; __device__ __forceinline__ int crow(int r, int hi) { return (r & 3) + 8 * (r >> 2) + 4 * hi; }
; __device__ __forceinline__ void p3_attention(Frame& F) {
;     ...
;         int hi2 = hi, r32b = r32; asm volatile("" : "+v"(hi2), "+v"(r32b));
;         unsigned char* od = F.ws + WS_ONA + (size_t)(b * SEQ + g4 * 256 + wid * 32) * 1024 + h * 128 + r32b;
; #pragma unroll
;         for (int r = 0; r < 16; ++r) { unsigned char* orow = od + (size_t)attn::crow(r, hi2) * 1024;
; #pragma unroll
;             for (int d = 0; d < 4; ++d) orow[d * 32] = f2fp8(o[d][r] * OSCALE); }
	v_lshl_add_u64 v[6:7], v[2:3], 0, v[6:7]
	v_cvt_pk_fp8_f32 v21, v5, v5
	v_mul_f32_e32 v5, 0x41800000, v10
	v_mov_b32_e32 v10, 0
	global_store_byte v[6:7], v18, off
	global_store_byte v[6:7], v19, off offset:32
	global_store_byte v[6:7], v20, off offset:64
	global_store_byte v[6:7], v21, off offset:96
	v_add_u32_e32 v6, 16, v4
	v_cvt_pk_fp8_f32 v10, v5, v5
	v_mul_f32_e32 v5, 0x41800000, v58
	v_mov_b32_e32 v18, 0
	v_ashrrev_i32_e32 v7, 31, v6
	v_cvt_pk_fp8_f32 v18, v5, v5
	v_mul_f32_e32 v5, 0x41800000, v42
	v_mov_b32_e32 v19, 0
	v_lshlrev_b64 v[6:7], 10, v[6:7]
	v_cvt_pk_fp8_f32 v19, v5, v5
	v_mul_f32_e32 v1, 0x41800000, v1
	v_mov_b32_e32 v5, 0
	v_lshl_add_u64 v[6:7], v[2:3], 0, v[6:7]
	v_cvt_pk_fp8_f32 v5, v1, v1
	global_store_byte v[6:7], v10, off
	global_store_byte v[6:7], v18, off offset:32
	global_store_byte v[6:7], v19, off offset:64
	global_store_byte v[6:7], v5, off offset:96
	v_mul_f32_e32 v1, 0x41800000, v11
	v_mov_b32_e32 v5, 0
	v_add_u32_e32 v6, 17, v4
	v_cvt_pk_fp8_f32 v5, v1, v1
	v_mul_f32_e32 v1, 0x41800000, v26
	v_mov_b32_e32 v10, 0
	v_ashrrev_i32_e32 v7, 31, v6
	v_cvt_pk_fp8_f32 v10, v1, v1
	v_mul_f32_e32 v1, 0x41800000, v43
	v_mov_b32_e32 v11, 0
	v_lshlrev_b64 v[6:7], 10, v[6:7]
	v_cvt_pk_fp8_f32 v11, v1, v1
	v_mul_f32_e32 v1, 0x41800000, v27
	v_mov_b32_e32 v18, 0
	v_lshl_add_u64 v[6:7], v[2:3], 0, v[6:7]
	v_cvt_pk_fp8_f32 v18, v1, v1
	global_store_byte v[6:7], v5, off
	global_store_byte v[6:7], v10, off offset:32
	global_store_byte v[6:7], v11, off offset:64
	global_store_byte v[6:7], v18, off offset:96
	v_mul_f32_e32 v1, 0x41800000, v12
	v_mov_b32_e32 v5, 0
	v_add_u32_e32 v6, 18, v4
	v_cvt_pk_fp8_f32 v5, v1, v1
	v_mul_f32_e32 v1, 0x41800000, v59
	v_mov_b32_e32 v10, 0
	v_ashrrev_i32_e32 v7, 31, v6
	v_cvt_pk_fp8_f32 v10, v1, v1
	v_mul_f32_e32 v1, 0x41800000, v44
	v_mov_b32_e32 v11, 0
	v_lshlrev_b64 v[6:7], 10, v[6:7]
	v_cvt_pk_fp8_f32 v11, v1, v1
	v_mul_f32_e32 v1, 0x41800000, v28
	v_mov_b32_e32 v12, 0
	v_lshl_add_u64 v[6:7], v[2:3], 0, v[6:7]
	v_cvt_pk_fp8_f32 v12, v1, v1
	global_store_byte v[6:7], v5, off
	global_store_byte v[6:7], v10, off offset:32
	global_store_byte v[6:7], v11, off offset:64
	global_store_byte v[6:7], v12, off offset:96
	v_mul_f32_e32 v1, 0x41800000, v13
	v_mov_b32_e32 v5, 0
	v_add_u32_e32 v6, 19, v4
	v_cvt_pk_fp8_f32 v5, v1, v1
	v_mul_f32_e32 v1, 0x41800000, v60
	v_mov_b32_e32 v10, 0
	v_ashrrev_i32_e32 v7, 31, v6
	v_cvt_pk_fp8_f32 v10, v1, v1
	v_mul_f32_e32 v1, 0x41800000, v45
	v_mov_b32_e32 v11, 0
	v_lshlrev_b64 v[6:7], 10, v[6:7]
	v_cvt_pk_fp8_f32 v11, v1, v1
	v_mul_f32_e32 v1, 0x41800000, v29
	v_mov_b32_e32 v12, 0
	v_lshl_add_u64 v[6:7], v[2:3], 0, v[6:7]
	v_cvt_pk_fp8_f32 v12, v1, v1
	global_store_byte v[6:7], v5, off
	global_store_byte v[6:7], v10, off offset:32
	global_store_byte v[6:7], v11, off offset:64
	global_store_byte v[6:7], v12, off offset:96
	v_mul_f32_e32 v1, 0x41800000, v14
	v_mov_b32_e32 v5, 0
	v_add_u32_e32 v6, 24, v4
	v_cvt_pk_fp8_f32 v5, v1, v1
	v_mul_f32_e32 v1, 0x41800000, v61
	v_mov_b32_e32 v10, 0
	v_ashrrev_i32_e32 v7, 31, v6
	v_cvt_pk_fp8_f32 v10, v1, v1
	v_mul_f32_e32 v1, 0x41800000, v46
	v_mov_b32_e32 v11, 0
	v_lshlrev_b64 v[6:7], 10, v[6:7]
	v_cvt_pk_fp8_f32 v11, v1, v1
	v_mul_f32_e32 v1, 0x41800000, v30
	v_mov_b32_e32 v12, 0
	v_lshl_add_u64 v[6:7], v[2:3], 0, v[6:7]
	v_cvt_pk_fp8_f32 v12, v1, v1
	global_store_byte v[6:7], v5, off
	global_store_byte v[6:7], v10, off offset:32
	global_store_byte v[6:7], v11, off offset:64
	global_store_byte v[6:7], v12, off offset:96
	v_mul_f32_e32 v1, 0x41800000, v15
	v_mov_b32_e32 v5, 0
	v_add_u32_e32 v6, 25, v4
	v_cvt_pk_fp8_f32 v5, v1, v1
	v_mul_f32_e32 v1, 0x41800000, v8
	v_mov_b32_e32 v8, 0
	v_ashrrev_i32_e32 v7, 31, v6
	v_cvt_pk_fp8_f32 v8, v1, v1
	v_mul_f32_e32 v1, 0x41800000, v47
	v_mov_b32_e32 v10, 0
	v_lshlrev_b64 v[6:7], 10, v[6:7]
	v_cvt_pk_fp8_f32 v10, v1, v1
	v_mul_f32_e32 v1, 0x41800000, v31
	v_mov_b32_e32 v11, 0
	v_lshl_add_u64 v[6:7], v[2:3], 0, v[6:7]
	v_cvt_pk_fp8_f32 v11, v1, v1
	global_store_byte v[6:7], v5, off
	global_store_byte v[6:7], v8, off offset:32
	global_store_byte v[6:7], v10, off offset:64
	global_store_byte v[6:7], v11, off offset:96
	v_mul_f32_e32 v1, 0x41800000, v16
	v_mov_b32_e32 v5, 0
	v_add_u32_e32 v6, 26, v4
	v_cvt_pk_fp8_f32 v5, v1, v1
	v_mul_f32_e32 v1, 0x41800000, v9
	v_mov_b32_e32 v8, 0
	v_ashrrev_i32_e32 v7, 31, v6
	v_cvt_pk_fp8_f32 v8, v1, v1
	v_mul_f32_e32 v1, 0x41800000, v48
	v_mov_b32_e32 v9, 0
	v_lshlrev_b64 v[6:7], 10, v[6:7]
	v_cvt_pk_fp8_f32 v9, v1, v1
	v_mul_f32_e32 v1, 0x41800000, v32
	v_mov_b32_e32 v10, 0
	v_lshl_add_u64 v[6:7], v[2:3], 0, v[6:7]
	v_cvt_pk_fp8_f32 v10, v1, v1
	v_add_u32_e32 v4, 27, v4
	global_store_byte v[6:7], v5, off
	global_store_byte v[6:7], v8, off offset:32
	global_store_byte v[6:7], v9, off offset:64
	global_store_byte v[6:7], v10, off offset:96
	v_ashrrev_i32_e32 v5, 31, v4
	v_lshlrev_b64 v[4:5], 10, v[4:5]
	v_lshl_add_u64 v[2:3], v[2:3], 0, v[4:5]
	v_mul_f32_e32 v1, 0x41800000, v17
	v_mov_b32_e32 v4, 0
	v_cvt_pk_fp8_f32 v4, v1, v1
	v_mul_f32_e32 v1, 0x41800000, v62
	v_mov_b32_e32 v5, 0
	v_cvt_pk_fp8_f32 v5, v1, v1
	v_mul_f32_e32 v1, 0x41800000, v49
	v_mov_b32_e32 v6, 0
	v_mov_b32_e32 v63, 0
	v_cvt_pk_fp8_f32 v6, v1, v1
	v_mul_f32_e32 v1, 0x41800000, v33
	v_cvt_pk_fp8_f32 v63, v1, v1
	global_store_byte v[2:3], v4, off
	global_store_byte v[2:3], v5, off offset:32
	global_store_byte v[2:3], v6, off offset:64
	global_store_byte v[2:3], v63, off offset:96
